# chunk-item code copies: hipcc's integer f32->bf16 rounding sequences fused into v_cvt_pk_bf16_f32 (72 pairs, 378 singles)
# speedup vs baseline: 1.0008x; 1.0008x over previous
; #define LAS __attribute__((address_space(3)))
; __device__ __forceinline__ unsigned pk2(float lo, float hi) { return f2bf(lo) | (f2bf(hi) << 16); }
; __device__ __forceinline__ void gdn_local_item(const Params& P, LAS unsigned char* lds, int item, int tid, bool defer, int& pend, unsigned& pend_fb) {
;     ...
;             if (part <= 1) {
;                 LAS bf16* dst = (part == 0 ? qb16 : kb16) + c * 136 + grp * 16;
;                 v4u o0, o1; o0.x = pk2(y[0], y[1]); o0.y = pk2(y[2], y[3]); o0.z = pk2(y[4], y[5]); o0.w = pk2(y[6], y[7]);
;                 o1.x = pk2(y[8], y[9]); o1.y = pk2(y[10], y[11]); o1.z = pk2(y[12], y[13]); o1.w = pk2(y[14], y[15]);
;                 *(LAS v4u*)dst = o0; *(LAS v4u*)(dst + 8) = o1;
;             }
.LBB0_523:
	s_andn2_b64 vcc, exec, s[10:11]
	s_cbranch_vccnz .LBB0_518
	v_cvt_pk_bf16_f32 v4, v4, v5
	v_cvt_pk_bf16_f32 v5, v6, v7
	v_cvt_pk_bf16_f32 v6, v8, v9
	v_cvt_pk_bf16_f32 v7, v10, v11
	v_cvt_pk_bf16_f32 v8, v16, v17
	v_cvt_pk_bf16_f32 v9, v18, v19
	s_cmp_eq_u32 s12, 0
	s_mov_b32 s0, 0x14c00
	v_cvt_pk_bf16_f32 v10, v12, v13
	s_cselect_b32 s0, s0, 0x10800
	s_add_i32 s0, s0, 0
	v_add3_u32 v20, s0, v47, v52
	v_cvt_pk_bf16_f32 v11, v14, v15
	ds_write_b128 v20, v[4:7]
	ds_write_b128 v20, v[8:11] offset:16
	s_branch .LBB0_518

; __device__ __forceinline__ unsigned f2bf(float f) { unsigned u = __builtin_bit_cast(unsigned, f); return (u + 0x7fffu + ((u >> 16) & 1u)) >> 16; }
; __device__ __forceinline__ void gdn_local_item(const Params& P, LAS unsigned char* lds, int item, int tid, bool defer, int& pend, unsigned& pend_fb) {
;     ...
;             const int sidx = 16 * sig + col; const float gs = sgc[sidx];
; #pragma unroll
;             for (int i = 0; i < 4; ++i) {
;                 const int c = 16 * rho + 4 * g + i;
;                 const float dec = (c >= sidx) ? __expf(sgc[c] - gs) : 0.f;
;                 if (mat == 0) AmT[sidx * 68 + c] = (c > sidx) ? sbeta[c] * acc[i] * dec : 0.f;
;                 else atts[c * 64 + sidx] = (bf16)f2bf(acc[i] * dec);
.LBB0_530:
	s_or_b64 exec, exec, s[0:1]
	v_lshl_add_u32 v32, v94, 1, s30
	s_mov_b64 s[0:1], -1
	s_and_b64 vcc, exec, s[10:11]
	s_cbranch_vccz .LBB0_532
	v_mul_f32_e32 v26, v20, v25
	v_cvt_pk_bf16_f32 v26, v26, v26
	v_lshl_add_u32 v27, v24, 7, v32
	ds_write_b16_d16_hi v27, v26
	s_mov_b64 s[0:1], 0

; __device__ __forceinline__ unsigned f2bf(float f) { unsigned u = __builtin_bit_cast(unsigned, f); return (u + 0x7fffu + ((u >> 16) & 1u)) >> 16; }
; __device__ __forceinline__ void gdn_local_item(const Params& P, LAS unsigned char* lds, int item, int tid, bool defer, int& pend, unsigned& pend_fb) {
;     ...
;             const int sidx = 16 * sig + col; const float gs = sgc[sidx];
; #pragma unroll
;             for (int i = 0; i < 4; ++i) {
;                 const int c = 16 * rho + 4 * g + i;
;                 const float dec = (c >= sidx) ? __expf(sgc[c] - gs) : 0.f;
;                 if (mat == 0) AmT[sidx * 68 + c] = (c > sidx) ? sbeta[c] * acc[i] * dec : 0.f;
;                 else atts[c * 64 + sidx] = (bf16)f2bf(acc[i] * dec);
.LBB0_538:
	s_or_b64 exec, exec, s[0:1]
	v_cndmask_b32_e64 v26, 0, 1, s[10:11]
	v_cmp_ne_u32_e64 s[6:7], 1, v26
	s_andn2_b64 vcc, exec, s[10:11]
	s_mov_b64 s[0:1], -1
	s_cbranch_vccnz .LBB0_540
	v_mul_f32_e32 v26, v21, v20
	v_cvt_pk_bf16_f32 v26, v26, v26
	v_lshl_add_u32 v27, v25, 7, v32
	s_mov_b64 s[0:1], 0
	ds_write_b16_d16_hi v27, v26

; __device__ __forceinline__ unsigned f2bf(float f) { unsigned u = __builtin_bit_cast(unsigned, f); return (u + 0x7fffu + ((u >> 16) & 1u)) >> 16; }
; __device__ __forceinline__ void gdn_local_item(const Params& P, LAS unsigned char* lds, int item, int tid, bool defer, int& pend, unsigned& pend_fb) {
;     ...
;             const int sidx = 16 * sig + col; const float gs = sgc[sidx];
; #pragma unroll
;             for (int i = 0; i < 4; ++i) {
;                 const int c = 16 * rho + 4 * g + i;
;                 const float dec = (c >= sidx) ? __expf(sgc[c] - gs) : 0.f;
;                 if (mat == 0) AmT[sidx * 68 + c] = (c > sidx) ? sbeta[c] * acc[i] * dec : 0.f;
;                 else atts[c * 64 + sidx] = (bf16)f2bf(acc[i] * dec);
.LBB0_555:
	v_mul_f32_e32 v21, v22, v20
	v_cvt_pk_bf16_f32 v21, v21, v21
	v_lshl_add_u32 v27, v26, 7, v32
	ds_write_b16_d16_hi v27, v21
	s_cbranch_execnz .LBB0_559

; __device__ __forceinline__ unsigned f2bf(float f) { unsigned u = __builtin_bit_cast(unsigned, f); return (u + 0x7fffu + ((u >> 16) & 1u)) >> 16; }
; __device__ __forceinline__ void gdn_local_item(const Params& P, LAS unsigned char* lds, int item, int tid, bool defer, int& pend, unsigned& pend_fb) {
;     ...
;             const int sidx = 16 * sig + col; const float gs = sgc[sidx];
; #pragma unroll
;             for (int i = 0; i < 4; ++i) {
;                 const int c = 16 * rho + 4 * g + i;
;                 const float dec = (c >= sidx) ? __expf(sgc[c] - gs) : 0.f;
;                 if (mat == 0) AmT[sidx * 68 + c] = (c > sidx) ? sbeta[c] * acc[i] * dec : 0.f;
;                 else atts[c * 64 + sidx] = (bf16)f2bf(acc[i] * dec);
.LBB0_563:
	v_mul_f32_e32 v21, v23, v20
	v_cvt_pk_bf16_f32 v21, v21, v21
	v_lshl_add_u32 v22, v27, 7, v32
	ds_write_b16_d16_hi v22, v21
	s_cbranch_execnz .LBB0_567

; __device__ __forceinline__ unsigned f2bf(float f) { unsigned u = __builtin_bit_cast(unsigned, f); return (u + 0x7fffu + ((u >> 16) & 1u)) >> 16; }
; __device__ __forceinline__ void gdn_local_item(const Params& P, LAS unsigned char* lds, int item, int tid, bool defer, int& pend, unsigned& pend_fb) {
;     ...
;             const int sidx = 16 * sig + col; const float gs = sgc[sidx];
; #pragma unroll
;             for (int i = 0; i < 4; ++i) {
;                 const int c = 16 * rho + 4 * g + i;
;                 const float dec = (c >= sidx) ? __expf(sgc[c] - gs) : 0.f;
;                 if (mat == 0) AmT[sidx * 68 + c] = (c > sidx) ? sbeta[c] * acc[i] * dec : 0.f;
;                 else atts[c * 64 + sidx] = (bf16)f2bf(acc[i] * dec);
.LBB0_581:
	s_or_b64 exec, exec, s[0:1]
	s_mov_b64 s[0:1], -1
	s_and_b64 vcc, exec, s[6:7]
	s_waitcnt lgkmcnt(0)
	v_lshlrev_b32_e32 v30, 7, v27
	s_cbranch_vccnz .LBB0_583
	v_mul_f32_e32 v21, v23, v20
	v_cvt_pk_bf16_f32 v21, v21, v21
	v_add3_u32 v22, s30, v30, v36
	s_mov_b64 s[0:1], 0
	ds_write_b16_d16_hi v22, v21

; __device__ __forceinline__ unsigned f2bf(float f) { unsigned u = __builtin_bit_cast(unsigned, f); return (u + 0x7fffu + ((u >> 16) & 1u)) >> 16; }
; __device__ __forceinline__ void gdn_local_item(const Params& P, LAS unsigned char* lds, int item, int tid, bool defer, int& pend, unsigned& pend_fb) {
;     ...
;             const int sidx = 16 * sig + col; const float gs = sgc[sidx];
; #pragma unroll
;             for (int i = 0; i < 4; ++i) {
;                 const int c = 16 * rho + 4 * g + i;
;                 const float dec = (c >= sidx) ? __expf(sgc[c] - gs) : 0.f;
;                 if (mat == 0) AmT[sidx * 68 + c] = (c > sidx) ? sbeta[c] * acc[i] * dec : 0.f;
;                 else atts[c * 64 + sidx] = (bf16)f2bf(acc[i] * dec);
.LBB0_600:
	v_mul_f32_e32 v32, v20, v31
	v_cvt_pk_bf16_f32 v32, v32, v32
	v_add3_u32 v35, s30, v29, v36
	ds_write_b16_d16_hi v35, v32
	v_add_u32_e32 v35, s31, v33
	s_cbranch_execnz .LBB0_571

; __device__ __forceinline__ unsigned f2bf(float f) { unsigned u = __builtin_bit_cast(unsigned, f); return (u + 0x7fffu + ((u >> 16) & 1u)) >> 16; }
; __device__ __forceinline__ void gdn_local_item(const Params& P, LAS unsigned char* lds, int item, int tid, bool defer, int& pend, unsigned& pend_fb) {
;     ...
;             const int sidx = 16 * sig + col; const float gs = sgc[sidx];
; #pragma unroll
;             for (int i = 0; i < 4; ++i) {
;                 const int c = 16 * rho + 4 * g + i;
;                 const float dec = (c >= sidx) ? __expf(sgc[c] - gs) : 0.f;
;                 if (mat == 0) AmT[sidx * 68 + c] = (c > sidx) ? sbeta[c] * acc[i] * dec : 0.f;
;                 else atts[c * 64 + sidx] = (bf16)f2bf(acc[i] * dec);
.LBB0_604:
	v_mul_f32_e32 v31, v21, v20
	v_cvt_pk_bf16_f32 v31, v31, v31
	v_add3_u32 v37, s30, v32, v36
	ds_write_b16_d16_hi v37, v31
	s_cbranch_execnz .LBB0_575

; __device__ __forceinline__ unsigned f2bf(float f) { unsigned u = __builtin_bit_cast(unsigned, f); return (u + 0x7fffu + ((u >> 16) & 1u)) >> 16; }
; __device__ __forceinline__ void gdn_local_item(const Params& P, LAS unsigned char* lds, int item, int tid, bool defer, int& pend, unsigned& pend_fb) {
;     ...
;             const int sidx = 16 * sig + col; const float gs = sgc[sidx];
; #pragma unroll
;             for (int i = 0; i < 4; ++i) {
;                 const int c = 16 * rho + 4 * g + i;
;                 const float dec = (c >= sidx) ? __expf(sgc[c] - gs) : 0.f;
;                 if (mat == 0) AmT[sidx * 68 + c] = (c > sidx) ? sbeta[c] * acc[i] * dec : 0.f;
;                 else atts[c * 64 + sidx] = (bf16)f2bf(acc[i] * dec);
.LBB0_608:
	v_mul_f32_e32 v21, v22, v20
	v_cvt_pk_bf16_f32 v21, v21, v21
	v_add3_u32 v37, s30, v31, v36
	ds_write_b16_d16_hi v37, v21
	s_cbranch_execnz .LBB0_579

; __device__ __forceinline__ unsigned f2bf(float f) { unsigned u = __builtin_bit_cast(unsigned, f); return (u + 0x7fffu + ((u >> 16) & 1u)) >> 16; }
; __device__ __forceinline__ void gdn_local_item(const Params& P, LAS unsigned char* lds, int item, int tid, bool defer, int& pend, unsigned& pend_fb) {
;     ...
;             const int sidx = 16 * sig + col; const float gs = sgc[sidx];
; #pragma unroll
;             for (int i = 0; i < 4; ++i) {
;                 const int c = 16 * rho + 4 * g + i;
;                 const float dec = (c >= sidx) ? __expf(sgc[c] - gs) : 0.f;
;                 if (mat == 0) AmT[sidx * 68 + c] = (c > sidx) ? sbeta[c] * acc[i] * dec : 0.f;
;                 else atts[c * 64 + sidx] = (bf16)f2bf(acc[i] * dec);
.LBB0_612:
	v_mul_f32_e32 v35, v20, v38
	v_cvt_pk_bf16_f32 v35, v35, v35
	v_add3_u32 v39, s30, v29, v37
	ds_write_b16_d16_hi v39, v35
	v_add_u32_e32 v35, s31, v33
	s_cbranch_execnz .LBB0_591

; __device__ __forceinline__ unsigned f2bf(float f) { unsigned u = __builtin_bit_cast(unsigned, f); return (u + 0x7fffu + ((u >> 16) & 1u)) >> 16; }
; __device__ __forceinline__ void gdn_local_item(const Params& P, LAS unsigned char* lds, int item, int tid, bool defer, int& pend, unsigned& pend_fb) {
;     ...
;             const int sidx = 16 * sig + col; const float gs = sgc[sidx];
; #pragma unroll
;             for (int i = 0; i < 4; ++i) {
;                 const int c = 16 * rho + 4 * g + i;
;                 const float dec = (c >= sidx) ? __expf(sgc[c] - gs) : 0.f;
;                 if (mat == 0) AmT[sidx * 68 + c] = (c > sidx) ? sbeta[c] * acc[i] * dec : 0.f;
;                 else atts[c * 64 + sidx] = (bf16)f2bf(acc[i] * dec);
.LBB0_617:
	v_mul_f32_e32 v38, v21, v20
	v_cvt_pk_bf16_f32 v38, v38, v38
	v_add3_u32 v39, s30, v32, v37
	ds_write_b16_d16_hi v39, v38
	s_cbranch_execnz .LBB0_594

; __device__ __forceinline__ unsigned f2bf(float f) { unsigned u = __builtin_bit_cast(unsigned, f); return (u + 0x7fffu + ((u >> 16) & 1u)) >> 16; }
; __device__ __forceinline__ void gdn_local_item(const Params& P, LAS unsigned char* lds, int item, int tid, bool defer, int& pend, unsigned& pend_fb) {
;     ...
;             const int sidx = 16 * sig + col; const float gs = sgc[sidx];
; #pragma unroll
;             for (int i = 0; i < 4; ++i) {
;                 const int c = 16 * rho + 4 * g + i;
;                 const float dec = (c >= sidx) ? __expf(sgc[c] - gs) : 0.f;
;                 if (mat == 0) AmT[sidx * 68 + c] = (c > sidx) ? sbeta[c] * acc[i] * dec : 0.f;
;                 else atts[c * 64 + sidx] = (bf16)f2bf(acc[i] * dec);
.LBB0_622:
	v_mul_f32_e32 v21, v22, v20
	v_cvt_pk_bf16_f32 v21, v21, v21
	v_add3_u32 v38, s30, v31, v37
	ds_write_b16_d16_hi v38, v21
	s_cbranch_execnz .LBB0_597

; __device__ __forceinline__ unsigned f2bf(float f) { unsigned u = __builtin_bit_cast(unsigned, f); return (u + 0x7fffu + ((u >> 16) & 1u)) >> 16; }
; __device__ __forceinline__ void gdn_local_item(const Params& P, LAS unsigned char* lds, int item, int tid, bool defer, int& pend, unsigned& pend_fb) {
;     ...
;             const int sidx = 16 * sig + col; const float gs = sgc[sidx];
; #pragma unroll
;             for (int i = 0; i < 4; ++i) {
;                 const int c = 16 * rho + 4 * g + i;
;                 const float dec = (c >= sidx) ? __expf(sgc[c] - gs) : 0.f;
;                 if (mat == 0) AmT[sidx * 68 + c] = (c > sidx) ? sbeta[c] * acc[i] * dec : 0.f;
;                 else atts[c * 64 + sidx] = (bf16)f2bf(acc[i] * dec);
.LBB0_627:
	v_mul_f32_e32 v21, v23, v20
	v_cvt_pk_bf16_f32 v21, v21, v21
	v_add3_u32 v22, s30, v30, v37
	ds_write_b16_d16_hi v22, v21
	s_cbranch_execnz .LBB0_631

; __device__ __forceinline__ unsigned f2bf(float f) { unsigned u = __builtin_bit_cast(unsigned, f); return (u + 0x7fffu + ((u >> 16) & 1u)) >> 16; }
; __device__ __forceinline__ void gdn_local_item(const Params& P, LAS unsigned char* lds, int item, int tid, bool defer, int& pend, unsigned& pend_fb) {
;     ...
;             const int sidx = 16 * sig + col; const float gs = sgc[sidx];
; #pragma unroll
;             for (int i = 0; i < 4; ++i) {
;                 const int c = 16 * rho + 4 * g + i;
;                 const float dec = (c >= sidx) ? __expf(sgc[c] - gs) : 0.f;
;                 if (mat == 0) AmT[sidx * 68 + c] = (c > sidx) ? sbeta[c] * acc[i] * dec : 0.f;
;                 else atts[c * 64 + sidx] = (bf16)f2bf(acc[i] * dec);
.LBB0_644:
	v_mul_f32_e32 v8, v4, v11
	v_cvt_pk_bf16_f32 v8, v8, v8
	v_add3_u32 v12, s30, v29, v10
	ds_write_b16_d16_hi v12, v8
	v_add_u32_e32 v8, s31, v21
	s_cbranch_execnz .LBB0_635

; __device__ __forceinline__ unsigned f2bf(float f) { unsigned u = __builtin_bit_cast(unsigned, f); return (u + 0x7fffu + ((u >> 16) & 1u)) >> 16; }
; __device__ __forceinline__ void gdn_local_item(const Params& P, LAS unsigned char* lds, int item, int tid, bool defer, int& pend, unsigned& pend_fb) {
;     ...
;             const int sidx = 16 * sig + col; const float gs = sgc[sidx];
; #pragma unroll
;             for (int i = 0; i < 4; ++i) {
;                 const int c = 16 * rho + 4 * g + i;
;                 const float dec = (c >= sidx) ? __expf(sgc[c] - gs) : 0.f;
;                 if (mat == 0) AmT[sidx * 68 + c] = (c > sidx) ? sbeta[c] * acc[i] * dec : 0.f;
;                 else atts[c * 64 + sidx] = (bf16)f2bf(acc[i] * dec);
.LBB0_649:
	v_mul_f32_e32 v11, v5, v4
	v_cvt_pk_bf16_f32 v11, v11, v11
	v_add3_u32 v12, s30, v32, v10
	ds_write_b16_d16_hi v12, v11
	s_cbranch_execnz .LBB0_638

; __device__ __forceinline__ unsigned f2bf(float f) { unsigned u = __builtin_bit_cast(unsigned, f); return (u + 0x7fffu + ((u >> 16) & 1u)) >> 16; }
; __device__ __forceinline__ void gdn_local_item(const Params& P, LAS unsigned char* lds, int item, int tid, bool defer, int& pend, unsigned& pend_fb) {
;     ...
;             const int sidx = 16 * sig + col; const float gs = sgc[sidx];
; #pragma unroll
;             for (int i = 0; i < 4; ++i) {
;                 const int c = 16 * rho + 4 * g + i;
;                 const float dec = (c >= sidx) ? __expf(sgc[c] - gs) : 0.f;
;                 if (mat == 0) AmT[sidx * 68 + c] = (c > sidx) ? sbeta[c] * acc[i] * dec : 0.f;
;                 else atts[c * 64 + sidx] = (bf16)f2bf(acc[i] * dec);
.LBB0_654:
	v_mul_f32_e32 v5, v6, v4
	v_cvt_pk_bf16_f32 v5, v5, v5
	v_add3_u32 v11, s30, v31, v10
	ds_write_b16_d16_hi v11, v5
	s_cbranch_execnz .LBB0_641

; __device__ __forceinline__ unsigned f2bf(float f) { unsigned u = __builtin_bit_cast(unsigned, f); return (u + 0x7fffu + ((u >> 16) & 1u)) >> 16; }
; __device__ __forceinline__ void gdn_local_item(const Params& P, LAS unsigned char* lds, int item, int tid, bool defer, int& pend, unsigned& pend_fb) {
;     ...
;             const int sidx = 16 * sig + col; const float gs = sgc[sidx];
; #pragma unroll
;             for (int i = 0; i < 4; ++i) {
;                 const int c = 16 * rho + 4 * g + i;
;                 const float dec = (c >= sidx) ? __expf(sgc[c] - gs) : 0.f;
;                 if (mat == 0) AmT[sidx * 68 + c] = (c > sidx) ? sbeta[c] * acc[i] * dec : 0.f;
;                 else atts[c * 64 + sidx] = (bf16)f2bf(acc[i] * dec);
.LBB0_659:
	v_mul_f32_e32 v5, v7, v4
	v_cvt_pk_bf16_f32 v5, v5, v5
	v_add3_u32 v6, s30, v30, v10
	ds_write_b16_d16_hi v6, v5
	s_cbranch_execnz .LBB0_663

; #define LAS __attribute__((address_space(3)))
; __device__ __forceinline__ void st16_wt(void* p, v4u v) { asm volatile("global_store_dwordx4 %0, %1, off sc0 sc1\n\ts_nop 1" :: "v"(p), "v"(v) : "memory"); }
; __device__ __forceinline__ unsigned pk2(float lo, float hi) { return f2bf(lo) | (f2bf(hi) << 16); }
; __device__ __forceinline__ void gdn_local_item(const Params& P, LAS unsigned char* lds, int item, int tid, bool defer, int& pend, unsigned& pend_fb) {
;     ...
;         bf16* QD = (bf16*)(ws + WS_QD) + (size_t)item * 8192;
;         bf16* KD = (bf16*)(ws + WS_KD) + (size_t)item * 8192;
;         bf16* ATT = (bf16*)(ws + WS_ATT) + (size_t)item * 4096;
; #pragma unroll
;         for (int r = 0; r < 2; ++r) {
;             const int id = tid + 512 * r;
;             { const int c = id >> 4, gam = id & 15, s32 = gam >> 2, g = gam & 3;
;               const v2u lo = *(const LAS v2u*)(qb16 + c * 136 + 32 * s32 + 4 * g), hi = *(const LAS v2u*)(qb16 + c * 136 + 32 * s32 + 16 + 4 * g);
;               const float e = seg[c];
;               v4u o; o.x = pk2(bflo(lo.x) * e, bfhi(lo.x) * e); o.y = pk2(bflo(lo.y) * e, bfhi(lo.y) * e); o.z = pk2(bflo(hi.x) * e, bfhi(hi.x) * e); o.w = pk2(bflo(hi.y) * e, bfhi(hi.y) * e);
;               st16_wt(QD + c * 128 + 8 * gam, o); }
;             { const int dk = id >> 3, gam = id & 7, s32 = gam >> 2, g = gam & 3, c0 = 32 * s32 + 4 * g;
;               float v[8];
; #pragma unroll
;               for (int j = 0; j < 4; ++j) { v[j] = ks[(c0 + j) * 132 + dk] * sek[c0 + j]; v[4 + j] = ks[(c0 + 16 + j) * 132 + dk] * sek[c0 + 16 + j]; }
;               v4u o; o.x = pk2(v[0], v[1]); o.y = pk2(v[2], v[3]); o.z = pk2(v[4], v[5]); o.w = pk2(v[6], v[7]);
;               st16_wt(KD + dk * 64 + 8 * gam, o); }
.LBB0_663:
	s_ashr_i32 s85, s84, 31
	s_lshl_b64 s[0:1], s[84:85], 13
	s_lshl_b64 s[8:9], s[84:85], 14
	s_add_u32 s14, s53, s8
	v_lshlrev_b32_e32 v96, 3, v94
	s_addc_u32 s15, s97, s9
	v_and_b32_e32 v97, 0x60, v96
	v_and_b32_e32 v12, 12, v45
	v_ashrrev_i32_e32 v17, 4, v91
	s_add_u32 s16, s86, s8
	v_lshl_add_u32 v28, v97, 1, s56
	v_and_b32_e32 v7, 32, v44
	v_mul_lo_u32 v99, v17, s73
	v_lshlrev_b32_e32 v98, 1, v12
	s_waitcnt lgkmcnt(0)
	s_barrier
	s_addc_u32 s17, s52, s9
	v_or_b32_e32 v29, v7, v12
	v_add3_u32 v12, v28, v99, v98
	s_add_i32 s85, 0, 0x27400
	ds_read2_b64 v[12:15], v12 offset1:4
	v_lshl_add_u32 v16, v17, 2, s85
	ds_read_b32 v16, v16
	v_lshlrev_b32_e32 v4, 4, v94
	v_mov_b32_e32 v5, v2
	s_waitcnt lgkmcnt(1)
	v_lshlrev_b32_e32 v21, 16, v15
	v_lshlrev_b32_e32 v20, 16, v14
	v_and_b32_e32 v15, 0xffff0000, v15
	v_and_b32_e32 v14, 0xffff0000, v14
	v_lshlrev_b32_e32 v19, 16, v13
	v_lshlrev_b32_e32 v18, 16, v12
	v_and_b32_e32 v13, 0xffff0000, v13
	v_and_b32_e32 v12, 0xffff0000, v12
	s_waitcnt lgkmcnt(0)
	v_pk_mul_f32 v[14:15], v[16:17], v[14:15] op_sel_hi:[0,1]
	v_pk_mul_f32 v[18:19], v[16:17], v[18:19] op_sel_hi:[0,1]
	v_pk_mul_f32 v[12:13], v[16:17], v[12:13] op_sel_hi:[0,1]
	v_pk_mul_f32 v[20:21], v[16:17], v[20:21] op_sel_hi:[0,1]
	v_cvt_pk_bf16_f32 v15, v15, v15
	v_cvt_pk_bf16_f32 v12, v12, v12
	v_cvt_pk_bf16_f32 v13, v13, v13
	v_cvt_pk_bf16_f32 v14, v14, v14
	v_cvt_pk_bf16_f32 v16, v18, v18
	v_cvt_pk_bf16_f32 v21, v21, v21
	v_cvt_pk_bf16_f32 v20, v20, v20
	v_cvt_pk_bf16_f32 v19, v19, v19
	v_lshrrev_b32_e32 v16, 16, v16
	v_lshlrev_b32_e32 v70, 7, v17
	v_lshl_add_u64 v[10:11], s[14:15], 0, v[4:5]
	v_lshrrev_b32_e32 v18, 16, v19
	v_lshrrev_b32_e32 v19, 16, v20
	v_lshrrev_b32_e32 v20, 16, v21
	v_and_or_b32 v12, v12, s74, v16
	v_ashrrev_i32_e32 v71, 31, v70
	v_and_or_b32 v15, v15, s74, v20
	v_and_or_b32 v14, v14, s74, v19
	v_and_or_b32 v13, v13, s74, v18
	v_lshl_add_u64 v[16:17], v[70:71], 1, v[10:11]
	global_store_dwordx4 v[16:17], v[12:15], off sc0 sc1
	s_nop 1
	v_lshl_add_u32 v12, v92, 2, 0
	v_mad_u32_u24 v33, v29, s72, v90
	v_mad_u32_u24 v13, v29, s72, v12
	v_add_u32_e32 v12, v12, v33
	ds_read_b32 v18, v12
	v_add_u32_e32 v12, 0x2200, v13
	v_lshl_add_u32 v14, v29, 2, 0
	ds_read2_b32 v[20:21], v12 offset0:68 offset1:200
	v_add_u32_e32 v12, 0x400, v13
	ds_read2_b32 v[16:17], v13 offset1:132
	v_add_u32_e32 v32, 0x27500, v14
	ds_read2_b32 v[22:23], v12 offset0:8 offset1:140
	ds_read_b32 v34, v13 offset:10032
	ds_read_b128 v[12:15], v32
	s_waitcnt lgkmcnt(4)
	v_mov_b32_e32 v19, v21
	v_and_b32_e32 v4, 56, v44
	s_waitcnt lgkmcnt(2)
	v_mov_b32_e32 v25, v22
	v_mov_b32_e32 v22, v17
	s_waitcnt lgkmcnt(0)
	v_mov_b32_e32 v27, v14
	v_mov_b32_e32 v14, v13
	v_mov_b32_e32 v24, v16
	v_mov_b32_e32 v26, v12
	v_pk_mul_f32 v[16:17], v[22:23], v[14:15]
	ds_read_b128 v[12:15], v32 offset:64
	v_mov_b32_e32 v21, v34
	v_pk_mul_f32 v[24:25], v[24:25], v[26:27]
	v_lshlrev_b32_e32 v4, 1, v4
	v_lshl_add_u64 v[8:9], s[16:17], 0, v[4:5]
	s_waitcnt lgkmcnt(0)
	v_mov_b32_e32 v23, v14
	v_mov_b32_e32 v14, v13
	v_mov_b32_e32 v22, v12
	v_pk_mul_f32 v[12:13], v[20:21], v[14:15]
	v_pk_mul_f32 v[18:19], v[18:19], v[22:23]
	v_cvt_pk_bf16_f32 v17, v17, v17
	v_cvt_pk_bf16_f32 v13, v13, v13
	v_cvt_pk_bf16_f32 v16, v16, v16
	v_cvt_pk_bf16_f32 v12, v12, v12
	v_cvt_pk_bf16_f32 v18, v18, v18
	v_cvt_pk_bf16_f32 v14, v24, v24
	v_cvt_pk_bf16_f32 v19, v19, v19
	v_cvt_pk_bf16_f32 v15, v25, v25
	v_lshrrev_b32_e32 v20, 16, v14
	v_lshrrev_b32_e32 v14, 16, v18
	v_lshrrev_b32_e32 v21, 16, v15
	v_lshrrev_b32_e32 v15, 16, v19
	v_and_or_b32 v14, v12, s74, v14
	v_and_or_b32 v12, v16, s74, v20
	v_lshlrev_b32_e32 v16, 6, v92
	v_and_or_b32 v15, v13, s74, v15
	v_and_or_b32 v13, v17, s74, v21
	v_ashrrev_i32_e32 v17, 31, v16
	v_lshl_add_u64 v[16:17], v[16:17], 1, v[8:9]
	global_store_dwordx4 v[16:17], v[12:15], off sc0 sc1
	s_nop 1
	v_ashrrev_i32_e32 v17, 4, v3
	v_mul_lo_u32 v100, v17, s73
	v_add3_u32 v12, v28, v100, v98
	ds_read2_b64 v[12:15], v12 offset1:4
	v_lshl_add_u32 v16, v17, 2, s85
	ds_read_b32 v16, v16
	v_lshlrev_b32_e32 v72, 7, v17
	v_ashrrev_i32_e32 v73, 31, v72
	s_waitcnt lgkmcnt(1)
	v_lshlrev_b32_e32 v19, 16, v13
	v_lshlrev_b32_e32 v18, 16, v12
	v_and_b32_e32 v13, 0xffff0000, v13
	v_and_b32_e32 v12, 0xffff0000, v12
	v_lshlrev_b32_e32 v21, 16, v15
	v_lshlrev_b32_e32 v20, 16, v14
	v_and_b32_e32 v15, 0xffff0000, v15
	v_and_b32_e32 v14, 0xffff0000, v14
	s_waitcnt lgkmcnt(0)
; __device__ __forceinline__ void gdn_local_item(const Params& P, LAS unsigned char* lds, int item, int tid, bool defer, int& pend, unsigned& pend_fb) {
;     ...
; #pragma unroll
;         for (int r = 0; r < 2; ++r) {
;             const int id = tid + 512 * r;
;             { const int c = id >> 4, gam = id & 15, s32 = gam >> 2, g = gam & 3;
;               const v2u lo = *(const LAS v2u*)(qb16 + c * 136 + 32 * s32 + 4 * g), hi = *(const LAS v2u*)(qb16 + c * 136 + 32 * s32 + 16 + 4 * g);
;               const float e = seg[c];
;               v4u o; o.x = pk2(bflo(lo.x) * e, bfhi(lo.x) * e); o.y = pk2(bflo(lo.y) * e, bfhi(lo.y) * e); o.z = pk2(bflo(hi.x) * e, bfhi(hi.x) * e); o.w = pk2(bflo(hi.y) * e, bfhi(hi.y) * e);
;               st16_wt(QD + c * 128 + 8 * gam, o); }
;             { const int dk = id >> 3, gam = id & 7, s32 = gam >> 2, g = gam & 3, c0 = 32 * s32 + 4 * g;
;               float v[8];
; #pragma unroll
;               for (int j = 0; j < 4; ++j) { v[j] = ks[(c0 + j) * 132 + dk] * sek[c0 + j]; v[4 + j] = ks[(c0 + 16 + j) * 132 + dk] * sek[c0 + 16 + j]; }
;               v4u o; o.x = pk2(v[0], v[1]); o.y = pk2(v[2], v[3]); o.z = pk2(v[4], v[5]); o.w = pk2(v[6], v[7]);
;               st16_wt(KD + dk * 64 + 8 * gam, o); }
;         }
;         { const int c = tid >> 3, gam = tid & 7, s32 = gam >> 2, g = gam & 3;
;           const v2u lo = *(const LAS v2u*)(atts + c * 64 + 32 * s32 + 4 * g), hi = *(const LAS v2u*)(atts + c * 64 + 32 * s32 + 16 + 4 * g);
;           v4u o; o.x = lo.x; o.y = lo.y; o.z = hi.x; o.w = hi.y;
;           st16_wt(ATT + c * 64 + 8 * gam, o); }
;     }
;     GL_BAR();
;     GL_REPF(5) {
;         LAS float* xcol = (LAS float*)(lds + GL_SOL);
;         LAS bf16* tinv = (LAS bf16*)(lds + GL_SOL + 17408);
;         const int j = tid >> 3, part = tid & 7, jb = j >> 4, jo = j & 15;
; #pragma unroll 1
;         for (int rb = jb; rb < 4; ++rb) {
;             float acc[16];
; #pragma unroll
;             for (int i = 0; i < 16; ++i) acc[i] = 0.f;
;             if (rb > jb) {
; #pragma unroll 2
;                 for (int s = 16 * jb + part; s < 16 * rb; s += 8) {
;                     const float sv = xcol[j * 68 + s];
;                     const LAS float* ar = AmT + s * 68 + 16 * rb;
; #pragma unroll
;                     for (int q = 0; q < 4; ++q) { const f32x4 A4 = *(const LAS f32x4*)(ar + 4 * q);
	v_pk_mul_f32 v[12:13], v[16:17], v[12:13] op_sel_hi:[0,1]
	v_pk_mul_f32 v[14:15], v[16:17], v[14:15] op_sel_hi:[0,1]
	v_pk_mul_f32 v[18:19], v[16:17], v[18:19] op_sel_hi:[0,1]
	v_pk_mul_f32 v[20:21], v[16:17], v[20:21] op_sel_hi:[0,1]
	v_cvt_pk_bf16_f32 v12, v12, v12
	v_cvt_pk_bf16_f32 v13, v13, v13
	v_cvt_pk_bf16_f32 v14, v14, v14
	v_cvt_pk_bf16_f32 v15, v15, v15
	v_cvt_pk_bf16_f32 v21, v21, v21
	v_cvt_pk_bf16_f32 v20, v20, v20
	v_cvt_pk_bf16_f32 v19, v19, v19
	v_cvt_pk_bf16_f32 v16, v18, v18
	v_lshrrev_b32_e32 v16, 16, v16
	v_lshrrev_b32_e32 v18, 16, v19
	v_lshrrev_b32_e32 v19, 16, v20
	v_lshrrev_b32_e32 v20, 16, v21
	v_lshl_add_u64 v[10:11], v[72:73], 1, v[10:11]
	v_ashrrev_i32_e32 v3, 3, v3
	v_and_or_b32 v15, v15, s74, v20
	v_and_or_b32 v14, v14, s74, v19
	v_and_or_b32 v13, v13, s74, v18
	v_and_or_b32 v12, v12, s74, v16
	global_store_dwordx4 v[10:11], v[12:15], off sc0 sc1
	s_nop 1
	v_lshl_add_u32 v10, v3, 2, 0
	v_mad_u32_u24 v11, v29, s72, v10
	v_add_u32_e32 v10, v10, v33
	ds_read_b32 v16, v10
	v_add_u32_e32 v10, 0x2200, v11
	ds_read2_b32 v[18:19], v10 offset0:68 offset1:200
	v_add_u32_e32 v10, 0x400, v11
	ds_read2_b32 v[14:15], v11 offset1:132
	ds_read2_b32 v[20:21], v10 offset0:8 offset1:140
	ds_read_b32 v26, v11 offset:10032
	ds_read_b128 v[10:13], v32
	v_and_b32_e32 v6, 0xffffffc0, v44
	s_waitcnt lgkmcnt(4)
	v_mov_b32_e32 v17, v19
	s_waitcnt lgkmcnt(2)
	v_mov_b32_e32 v23, v20
	v_mov_b32_e32 v20, v15
	s_waitcnt lgkmcnt(0)
	v_mov_b32_e32 v25, v12
	v_mov_b32_e32 v12, v11
	v_mov_b32_e32 v22, v14
	v_mov_b32_e32 v24, v10
	v_pk_mul_f32 v[14:15], v[20:21], v[12:13]
	ds_read_b128 v[10:13], v32 offset:64
	v_mov_b32_e32 v19, v26
	v_pk_mul_f32 v[22:23], v[22:23], v[24:25]
	s_add_u32 s0, s27, s0
	v_lshl_add_u32 v30, v6, 1, s30
	s_waitcnt lgkmcnt(0)
	v_mov_b32_e32 v21, v12
	v_mov_b32_e32 v12, v11
	v_mov_b32_e32 v20, v10
	v_pk_mul_f32 v[10:11], v[18:19], v[12:13]
	v_pk_mul_f32 v[16:17], v[16:17], v[20:21]
	v_cvt_pk_bf16_f32 v15, v15, v15
	v_cvt_pk_bf16_f32 v11, v11, v11
	v_cvt_pk_bf16_f32 v14, v14, v14
	v_cvt_pk_bf16_f32 v10, v10, v10
	v_bfe_u32 v19, v17, 16, 1
	v_cvt_pk_bf16_f32 v16, v16, v16
	v_cvt_pk_bf16_f32 v12, v22, v22
	v_add3_u32 v17, v17, v19, s75
	v_cvt_pk_bf16_f32 v13, v23, v23
	v_lshrrev_b32_e32 v18, 16, v12
	v_lshrrev_b32_e32 v12, 16, v16
	v_lshrrev_b32_e32 v19, 16, v13
	v_lshrrev_b32_e32 v13, 16, v17
	v_and_or_b32 v12, v10, s74, v12
	v_and_or_b32 v10, v14, s74, v18
	v_lshlrev_b32_e32 v14, 6, v3
	v_lshlrev_b32_e32 v31, 1, v7
	v_ashrrev_i32_e32 v7, 31, v6
	v_and_or_b32 v13, v11, s74, v13
	v_and_or_b32 v11, v15, s74, v19
	v_ashrrev_i32_e32 v15, 31, v14
	s_addc_u32 s1, s33, s1
	v_lshl_add_u64 v[8:9], v[14:15], 1, v[8:9]
	global_store_dwordx4 v[8:9], v[10:13], off sc0 sc1
	s_nop 1
	v_add3_u32 v3, v30, v31, v98
	v_lshl_add_u64 v[6:7], v[6:7], 1, s[0:1]
	v_lshl_add_u64 v[8:9], v[6:7], 0, v[4:5]
	ds_read2_b64 v[4:7], v3 offset1:4
	s_waitcnt lgkmcnt(0)
	global_store_dwordx4 v[8:9], v[4:7], off sc0 sc1
	s_nop 1
	s_waitcnt lgkmcnt(0)
	s_barrier
	v_ashrrev_i32_e32 v101, 7, v91
	v_cmp_gt_i32_e64 s[0:1], 4, v101
	v_cmp_eq_u32_e32 vcc, 0, v46
	s_and_saveexec_b64 s[14:15], s[0:1]
	s_cbranch_execz .LBB0_678
	v_bfe_u32 v4, v91, 3, 4
	v_cmp_eq_u32_e64 s[0:1], 0, v4
	v_lshlrev_b32_e32 v3, 4, v101
	v_or_b32_e32 v102, v3, v46
	v_cndmask_b32_e64 v104, 0, 1.0, s[0:1]
	v_cmp_eq_u32_e64 s[0:1], 1, v4
	v_add_u32_e32 v103, s96, v47
	v_lshl_add_u32 v74, v92, 1, s56
	v_cndmask_b32_e64 v105, 0, 1.0, s[0:1]
	v_cmp_eq_u32_e64 s[0:1], 2, v4
	s_mov_b32 s64, 0
	v_or_b32_e32 v121, 8, v102
	v_cndmask_b32_e64 v106, 0, 1.0, s[0:1]
	v_cmp_eq_u32_e64 s[0:1], 3, v4
	v_lshl_add_u32 v122, v102, 2, v103
	v_mul_lo_u32 v123, v102, s73
	v_cndmask_b32_e64 v107, 0, 1.0, s[0:1]
	v_cmp_eq_u32_e64 s[0:1], 4, v4
	v_lshl_add_u32 v124, v101, 6, s31
	s_mov_b64 s[16:17], 0
	v_cndmask_b32_e64 v108, 0, 1.0, s[0:1]
	v_cmp_eq_u32_e64 s[0:1], 5, v4
	v_mov_b32_e32 v125, v101
	s_nop 0
	v_cndmask_b32_e64 v109, 0, 1.0, s[0:1]
	v_cmp_eq_u32_e64 s[0:1], 6, v4
	s_nop 1
	v_cndmask_b32_e64 v110, 0, 1.0, s[0:1]
	v_cmp_eq_u32_e64 s[0:1], 7, v4
	s_nop 1
	v_cndmask_b32_e64 v111, 0, 1.0, s[0:1]
	v_cmp_eq_u32_e64 s[0:1], 8, v4
	s_nop 1
	v_cndmask_b32_e64 v112, 0, 1.0, s[0:1]
	v_cmp_eq_u32_e64 s[0:1], 9, v4
	s_nop 1
	v_cndmask_b32_e64 v113, 0, 1.0, s[0:1]
	v_cmp_eq_u32_e64 s[0:1], 10, v4
	s_nop 1
	v_cndmask_b32_e64 v114, 0, 1.0, s[0:1]
	v_cmp_eq_u32_e64 s[0:1], 11, v4
	s_nop 1
	v_cndmask_b32_e64 v115, 0, 1.0, s[0:1]
	v_cmp_eq_u32_e64 s[0:1], 12, v4
	s_nop 1
	v_cndmask_b32_e64 v116, 0, 1.0, s[0:1]
	v_cmp_eq_u32_e64 s[0:1], 13, v4
	s_nop 1
	v_cndmask_b32_e64 v117, 0, 1.0, s[0:1]
	v_cmp_eq_u32_e64 s[0:1], 14, v4
	s_nop 1
	v_cndmask_b32_e64 v118, 0, 1.0, s[0:1]
	v_cmp_eq_u32_e64 s[0:1], 15, v4
	v_not_b32_e32 v4, v46
	v_sub_u32_e32 v120, v4, v3
	v_cndmask_b32_e64 v119, 0, 1.0, s[0:1]
	s_branch .LBB0_666

; #define LAS __attribute__((address_space(3)))
; __device__ __forceinline__ void gdn_local_item(const Params& P, LAS unsigned char* lds, int item, int tid, bool defer, int& pend, unsigned& pend_fb) {
;     ...
; #pragma unroll
;             for (int i = 0; i < 16; ++i) {
;                 const float sv = acc[i];
;                 const LAS float* ar = AmT + (16 * rb + i) * 68 + 16 * rb;
; #pragma unroll
;                 for (int q = (i + 1) / 4; q < 4; ++q) { const f32x4 A4 = *(const LAS f32x4*)(ar + 4 * q);
;                     if (4 * q > i) acc[4 * q] -= A4.x * sv; if (4 * q + 1 > i) acc[4 * q + 1] -= A4.y * sv; if (4 * q + 2 > i) acc[4 * q + 2] -= A4.z * sv; if (4 * q + 3 > i) acc[4 * q + 3] -= A4.w * sv; }
;             }
.LBB0_676:
	s_or_b64 exec, exec, s[18:19]
	s_and_saveexec_b64 s[0:1], vcc
	s_cbranch_execz .LBB0_665
	v_lshlrev_b32_e32 v3, 2, v20
	v_add_u32_e32 v16, s31, v3
	s_movk_i32 s18, 0x1100
	v_mad_u64_u32 v[12:13], s[18:19], v125, s18, v[16:17]
	ds_read_b128 v[22:25], v12
	ds_read_b128 v[38:41], v12 offset:16
	ds_read_b128 v[44:47], v12 offset:32
	ds_read_b128 v[12:15], v12 offset:48
	v_add_u32_e32 v3, v103, v3
	s_waitcnt lgkmcnt(3)
	v_fma_f32 v6, -v4, v24, v6
	v_fma_f32 v7, -v4, v25, v7
	v_fma_f32 v5, -v4, v23, v5
	s_waitcnt lgkmcnt(0)
	v_fma_f32 v15, -v4, v15, v77
	v_or_b32_e32 v77, 1, v20
	v_mad_u64_u32 v[80:81], s[18:19], v77, s73, v[16:17]
	ds_read_b128 v[26:29], v80
	ds_read_b128 v[52:55], v80 offset:16
	ds_read_b128 v[48:51], v80 offset:32
	ds_read_b128 v[16:19], v80 offset:48
	s_waitcnt lgkmcnt(3)
	ds_read_b128 v[24:27], v80 offset:272
	ds_read_b128 v[56:59], v80 offset:288
	v_fma_f32 v6, -v5, v28, v6
	v_fma_f32 v7, -v5, v29, v7
	ds_read_b128 v[62:65], v80 offset:560
	s_waitcnt lgkmcnt(2)
	v_fma_f32 v7, -v6, v27, v7
	ds_read_b128 v[24:27], v80 offset:592
	ds_read_b128 v[66:69], v80 offset:832
	v_fma_f32 v8, -v4, v38, v8
	v_fma_f32 v9, -v4, v39, v9
	ds_read_b128 v[32:35], v80 offset:1136
	ds_read_b128 v[126:129], v80 offset:1104
	v_fma_f32 v10, -v4, v40, v10
	v_fma_f32 v11, -v4, v41, v11
	v_fma_f32 v8, -v5, v52, v8
	v_fma_f32 v9, -v5, v53, v9
	v_fma_f32 v10, -v5, v54, v10
	v_fma_f32 v11, -v5, v55, v11
	ds_read_b128 v[20:23], v80 offset:320
	s_waitcnt lgkmcnt(6)
	v_fma_f32 v8, -v6, v56, v8
	v_fma_f32 v9, -v6, v57, v9
	v_fma_f32 v10, -v6, v58, v10
	v_fma_f32 v11, -v6, v59, v11
	ds_read_b128 v[40:43], v80 offset:1376
	ds_read_b128 v[56:59], v80 offset:304
	s_waitcnt lgkmcnt(7)
	v_fma_f32 v8, -v7, v62, v8
	v_fma_f32 v9, -v7, v63, v9
	v_fma_f32 v10, -v7, v64, v10
	v_fma_f32 v11, -v7, v65, v11
	ds_read_b128 v[62:65], v80 offset:576
	ds_read_b128 v[28:31], v80 offset:864
	s_waitcnt lgkmcnt(7)
	v_fma_f32 v9, -v8, v67, v9
	v_fma_f32 v10, -v8, v68, v10
	v_fma_f32 v11, -v8, v69, v11
	ds_read_b128 v[66:69], v80 offset:848
	v_fma_f32 v15, -v19, v5, v15
	s_waitcnt lgkmcnt(6)
	v_fma_f32 v10, -v9, v128, v10
	v_fma_f32 v11, -v9, v129, v11
	v_fma_f32 v19, -v4, v44, v60
	ds_read_b128 v[126:129], v80 offset:1120
	ds_read_b128 v[36:39], v80 offset:1408
	ds_read_b128 v[130:133], v80 offset:1392
	v_fma_f32 v19, -v5, v48, v19
	s_waitcnt lgkmcnt(7)
	v_fma_f32 v11, -v10, v43, v11
	ds_read_b128 v[40:43], v80 offset:1680
	ds_read_b128 v[134:137], v80 offset:1664
	s_waitcnt lgkmcnt(8)
	v_fma_f32 v19, -v6, v56, v19
	s_waitcnt lgkmcnt(7)
	v_fma_f32 v19, -v7, v62, v19
	s_waitcnt lgkmcnt(5)
	v_fma_f32 v19, -v8, v66, v19
	s_waitcnt lgkmcnt(4)
	v_fma_f32 v19, -v9, v126, v19
	s_waitcnt lgkmcnt(2)
	v_fma_f32 v19, -v10, v130, v19
	s_waitcnt lgkmcnt(0)
	v_fma_f32 v44, -v11, v134, v19
	v_fma_f32 v19, -v4, v45, v61
	v_fma_f32 v19, -v5, v49, v19
	v_fma_f32 v19, -v6, v57, v19
	ds_read_b128 v[52:55], v80 offset:1952
	ds_read_b128 v[144:147], v80 offset:1936
	v_fma_f32 v19, -v7, v63, v19
	v_fma_f32 v19, -v8, v67, v19
	v_fma_f32 v19, -v9, v127, v19
	v_fma_f32 v19, -v10, v131, v19
	v_fma_f32 v19, -v11, v135, v19
	s_waitcnt lgkmcnt(0)
	v_fma_f32 v45, -v44, v145, v19
	v_fma_f32 v19, -v4, v46, v82
	v_fma_f32 v19, -v5, v50, v19
	v_fma_f32 v19, -v6, v58, v19
	v_fma_f32 v19, -v7, v64, v19
	ds_read_b128 v[60:63], v80 offset:2224
	ds_read_b128 v[148:151], v80 offset:2208
	v_fma_f32 v19, -v8, v68, v19
	v_fma_f32 v19, -v9, v128, v19
	v_fma_f32 v19, -v10, v132, v19
	v_fma_f32 v19, -v11, v136, v19
	v_fma_f32 v19, -v44, v146, v19
	s_waitcnt lgkmcnt(0)
; #define LAS __attribute__((address_space(3)))
; __device__ __forceinline__ unsigned f2bf(float f) { unsigned u = __builtin_bit_cast(unsigned, f); return (u + 0x7fffu + ((u >> 16) & 1u)) >> 16; }
; __device__ __forceinline__ void gdn_local_item(const Params& P, LAS unsigned char* lds, int item, int tid, bool defer, int& pend, unsigned& pend_fb) {
;     ...
;             for (int i = 0; i < 16; ++i) {
;                 const float sv = acc[i];
;                 const LAS float* ar = AmT + (16 * rb + i) * 68 + 16 * rb;
; #pragma unroll
;                 for (int q = (i + 1) / 4; q < 4; ++q) { const f32x4 A4 = *(const LAS f32x4*)(ar + 4 * q);
;                     if (4 * q > i) acc[4 * q] -= A4.x * sv; if (4 * q + 1 > i) acc[4 * q + 1] -= A4.y * sv; if (4 * q + 2 > i) acc[4 * q + 2] -= A4.z * sv; if (4 * q + 3 > i) acc[4 * q + 3] -= A4.w * sv; }
;             }
;             if (part == 0) {
; #pragma unroll
;                 for (int i = 0; i < 16; ++i) { xcol[j * 68 + 16 * rb + i] = acc[i]; tinv[(16 * rb + i) * 72 + j] = (bf16)f2bf(acc[i]); }
;             }
	v_fma_f32 v46, -v45, v150, v19
	v_fma_f32 v19, -v4, v47, v83
	v_fma_f32 v19, -v5, v51, v19
	v_fma_f32 v19, -v6, v59, v19
	v_fma_f32 v19, -v7, v65, v19
	v_fma_f32 v19, -v8, v69, v19
	v_fma_f32 v12, -v4, v12, v78
	v_fma_f32 v13, -v4, v13, v79
	v_fma_f32 v14, -v4, v14, v76
	ds_read_b128 v[152:155], v80 offset:2496
	ds_read_b128 v[48:51], v80 offset:2480
	v_fma_f32 v19, -v9, v129, v19
	v_fma_f32 v12, -v16, v5, v12
	v_fma_f32 v13, -v17, v5, v13
	v_fma_f32 v14, -v18, v5, v14
	v_fma_f32 v15, -v23, v6, v15
	v_fma_f32 v19, -v10, v133, v19
	v_fma_f32 v12, -v20, v6, v12
	v_fma_f32 v13, -v21, v6, v13
	v_fma_f32 v14, -v22, v6, v14
	v_fma_f32 v15, -v27, v7, v15
	v_fma_f32 v19, -v11, v137, v19
	v_fma_f32 v12, -v24, v7, v12
	v_fma_f32 v13, -v25, v7, v13
	v_fma_f32 v14, -v26, v7, v14
	v_fma_f32 v15, -v31, v8, v15
	v_fma_f32 v19, -v44, v147, v19
	v_fma_f32 v12, -v28, v8, v12
	v_fma_f32 v13, -v29, v8, v13
	v_fma_f32 v14, -v30, v8, v14
	v_fma_f32 v15, -v35, v9, v15
	v_fma_f32 v19, -v45, v151, v19
	v_fma_f32 v12, -v32, v9, v12
	v_fma_f32 v13, -v33, v9, v13
	v_fma_f32 v14, -v34, v9, v14
	v_fma_f32 v15, -v39, v10, v15
	s_waitcnt lgkmcnt(0)
	v_fma_f32 v47, -v46, v51, v19
	ds_read_b128 v[48:51], v80 offset:2768
	ds_read_b128 v[56:59], v80 offset:3040
	v_fma_f32 v12, -v36, v10, v12
	v_fma_f32 v13, -v37, v10, v13
	v_fma_f32 v14, -v38, v10, v14
	v_fma_f32 v15, -v43, v11, v15
	v_fma_f32 v12, -v40, v11, v12
	v_fma_f32 v13, -v41, v11, v13
	v_fma_f32 v14, -v42, v11, v14
	v_fma_f32 v15, -v55, v44, v15
	v_fma_f32 v12, -v52, v44, v12
	v_fma_f32 v13, -v53, v44, v13
	ds_read_b128 v[64:67], v80 offset:3312
	ds_read_b128 v[16:19], v80 offset:3584
	v_fma_f32 v14, -v54, v44, v14
	v_fma_f32 v15, -v63, v45, v15
	v_fma_f32 v12, -v60, v45, v12
	v_fma_f32 v13, -v61, v45, v13
	v_fma_f32 v14, -v62, v45, v14
	v_fma_f32 v15, -v155, v46, v15
	v_fma_f32 v12, -v152, v46, v12
	v_fma_f32 v13, -v153, v46, v13
	v_fma_f32 v14, -v154, v46, v14
	s_waitcnt lgkmcnt(3)
	v_fma_f32 v15, -v51, v47, v15
	v_fma_f32 v12, -v48, v47, v12
	v_fma_f32 v13, -v49, v47, v13
	v_fma_f32 v14, -v50, v47, v14
	s_waitcnt lgkmcnt(0)
	v_fma_f32 v15, -v59, v12, v15
	v_fma_f32 v13, -v57, v12, v13
	v_fma_f32 v14, -v58, v12, v14
	v_cvt_pk_bf16_f32 v18, v4, v4
	v_mad_u64_u32 v[16:17], s[18:19], v125, s29, v[74:75]
	v_fma_f32 v15, -v67, v13, v15
	v_fma_f32 v14, -v66, v13, v14
	v_fma_f32 v15, -v19, v14, v15
	ds_write_b16_d16_hi v16, v18
	v_cvt_pk_bf16_f32 v17, v5, v5
	v_mad_u64_u32 v[18:19], s[18:19], v77, s71, v[74:75]
	ds_write_b16_d16_hi v18, v17
	v_bfe_u32 v17, v6, 16, 1
	v_add3_u32 v17, v6, v17, s75
	ds_write_b16_d16_hi v18, v17 offset:144
	ds_write_b128 v3, v[4:7]
	v_cvt_pk_bf16_f32 v4, v7, v7
	ds_write_b16_d16_hi v18, v4 offset:288
	v_cvt_pk_bf16_f32 v4, v8, v8
	ds_write_b16_d16_hi v18, v4 offset:432
	v_cvt_pk_bf16_f32 v4, v9, v9
	ds_write_b16_d16_hi v18, v4 offset:576
	v_cvt_pk_bf16_f32 v4, v10, v10
	ds_write_b16_d16_hi v18, v4 offset:720
	ds_write_b128 v3, v[8:11] offset:16
	v_cvt_pk_bf16_f32 v4, v11, v11
	ds_write_b16_d16_hi v18, v4 offset:864
	v_cvt_pk_bf16_f32 v4, v44, v44
	ds_write_b16_d16_hi v18, v4 offset:1008
	v_cvt_pk_bf16_f32 v4, v45, v45
	ds_write_b16_d16_hi v18, v4 offset:1152
	v_cvt_pk_bf16_f32 v4, v46, v46
	ds_write_b16_d16_hi v18, v4 offset:1296
	ds_write_b128 v3, v[44:47] offset:32
	v_cvt_pk_bf16_f32 v4, v47, v47
	ds_write_b16_d16_hi v18, v4 offset:1440
	v_cvt_pk_bf16_f32 v4, v12, v12
	ds_write_b16_d16_hi v18, v4 offset:1584
	v_cvt_pk_bf16_f32 v4, v13, v13
	ds_write_b16_d16_hi v18, v4 offset:1728
	v_cvt_pk_bf16_f32 v4, v14, v14
	ds_write_b16_d16_hi v18, v4 offset:1872
	ds_write_b128 v3, v[12:15] offset:48
	v_cvt_pk_bf16_f32 v3, v15, v15
	ds_write_b16_d16_hi v16, v3 offset:2160
	s_branch .LBB0_665

; __device__ __forceinline__ void st16_wt(void* p, v4u v) { asm volatile("global_store_dwordx4 %0, %1, off sc0 sc1\n\ts_nop 1" :: "v"(p), "v"(v) : "memory"); }
; __device__ __forceinline__ unsigned f2bf(float f) { unsigned u = __builtin_bit_cast(unsigned, f); return (u + 0x7fffu + ((u >> 16) & 1u)) >> 16; }
; __device__ __forceinline__ unsigned pk2(float lo, float hi) { return f2bf(lo) | (f2bf(hi) << 16); }
; __device__ __forceinline__ void gdn_local_item(const Params& P, LAS unsigned char* lds, int item, int tid, bool defer, int& pend, unsigned& pend_fb) {
;     ...
;             for (int s2 = 0; s2 < 2; ++s2) {
;                 float v[8];
; #pragma unroll
;                 for (int e = 0; e < 8; ++e) { const int sidx = 32 * s2 + 8 * g + e; float x = src[sidx * 132] * sbeta[sidx]; if (isw) x *= seg[sidx]; v[e] = x; }
;                 v4u pk; pk.x = pk2(v[0], v[1]); pk.y = pk2(v[2], v[3]); pk.z = pk2(v[4], v[5]); pk.w = pk2(v[6], v[7]);
;                 bfr[s2] = __builtin_bit_cast(bf16x8, pk);
;             }
;             f32x4 acc[4];
; #pragma unroll
;             for (int rho = 0; rho < 4; ++rho) { acc[rho] = (f32x4){0.f, 0.f, 0.f, 0.f};
; #pragma unroll
;                 for (int s2 = 0; s2 < 2; ++s2) acc[rho] = __builtin_amdgcn_mfma_f32_16x16x32_bf16(af[rho][s2], bfr[s2], acc[rho], 0, 0, 0); }
;             if (!isw) {
;                 v4u o0, o1;
;                 o0.x = pk2(acc[0].x, acc[0].y); o0.y = pk2(acc[0].z, acc[0].w); o0.z = pk2(acc[1].x, acc[1].y); o0.w = pk2(acc[1].z, acc[1].w);
;                 o1.x = pk2(acc[2].x, acc[2].y); o1.y = pk2(acc[2].z, acc[2].w); o1.z = pk2(acc[3].x, acc[3].y); o1.w = pk2(acc[3].z, acc[3].w);
;                 v4u* d = (v4u*)(UF + (size_t)(2 * (wave & 3) + sig) * 1024 + lane * 16);
;                 st16_wt(d, o0); st16_wt(d + 1, o1);
;             } else {
; #pragma unroll
;                 for (int rho = 0; rho < 4; ++rho)
; #pragma unroll
;                     for (int i = 0; i < 4; ++i) wst[(16 * rho + 4 * g + i) * 136 + jj] = (bf16)f2bf(-acc[rho][i]);
;             }
.LBB0_723:
	v_cvt_pk_bf16_f32 v42, v42, v42
	v_cvt_pk_bf16_f32 v45, v45, v45
	v_cvt_pk_bf16_f32 v38, v38, v38
	v_cvt_pk_bf16_f32 v40, v40, v40
	v_cvt_pk_bf16_f32 v39, v39, v39
	v_cvt_pk_bf16_f32 v36, v36, v36
	v_cvt_pk_bf16_f32 v43, v43, v43
	v_cvt_pk_bf16_f32 v41, v41, v41
	v_lshrrev_b32_e32 v36, 16, v36
	v_lshrrev_b32_e32 v39, 16, v39
	v_lshrrev_b32_e32 v41, 16, v41
	v_lshrrev_b32_e32 v43, 16, v43
	v_and_or_b32 v109, v40, s74, v39
	v_and_or_b32 v108, v38, s74, v36
	v_and_or_b32 v111, v45, s74, v43
	v_and_or_b32 v110, v42, s74, v41
	v_cvt_pk_bf16_f32 v45, v46, v46
	v_cvt_pk_bf16_f32 v46, v48, v48
	v_cvt_pk_bf16_f32 v36, v37, v37
	v_cvt_pk_bf16_f32 v41, v51, v51
	v_cvt_pk_bf16_f32 v40, v49, v49
	v_cvt_pk_bf16_f32 v39, v47, v47
	v_cvt_pk_bf16_f32 v37, v44, v44
	v_lshrrev_b32_e32 v44, 16, v37
	v_lshrrev_b32_e32 v37, 16, v39
	v_lshrrev_b32_e32 v47, 16, v40
	v_lshrrev_b32_e32 v39, 16, v41
	v_mfma_f32_16x16x32_bf16 v[40:43], v[32:35], v[108:111], 0
	v_cvt_pk_bf16_f32 v38, v50, v50
	v_and_or_b32 v39, v36, s74, v39
	v_and_or_b32 v38, v38, s74, v47
	v_and_or_b32 v37, v46, s74, v37
	v_and_or_b32 v36, v45, s74, v44
	s_add_u32 s0, s82, s8
	s_addc_u32 s1, s83, s9
	v_mfma_f32_16x16x32_bf16 v[48:51], v[4:7], v[36:39], v[40:43]
	s_mov_b64 s[10:11], -1
	s_and_b64 vcc, exec, s[6:7]
	v_lshlrev_b32_e32 v105, 1, v53
	v_mfma_f32_16x16x32_bf16 v[40:43], v[8:11], v[108:111], 0
	v_mul_u32_u24_e32 v106, 0x440, v93
	v_mfma_f32_16x16x32_bf16 v[44:47], v[12:15], v[36:39], v[40:43]
	v_mfma_f32_16x16x32_bf16 v[40:43], v[16:19], v[108:111], 0
	v_mfma_f32_16x16x32_bf16 v[108:111], v[24:27], v[108:111], 0
	v_mfma_f32_16x16x32_bf16 v[40:43], v[20:23], v[36:39], v[40:43]
	v_mfma_f32_16x16x32_bf16 v[36:39], v[28:31], v[36:39], v[108:111]
	s_cbranch_vccnz .LBB0_725
	v_xor_b32_e32 v53, 0x80000000, v48
	s_nop 3
	v_cvt_pk_bf16_f32 v53, v53, v53
	v_add3_u32 v108, s54, v105, v106
	ds_write_b16_d16_hi v108, v53
	v_xor_b32_e32 v53, 0x80000000, v49
	v_cvt_pk_bf16_f32 v53, v53, v53
	ds_write_b16_d16_hi v108, v53 offset:272
	v_xor_b32_e32 v53, 0x80000000, v50
	v_cvt_pk_bf16_f32 v53, v53, v53
	ds_write_b16_d16_hi v108, v53 offset:544
	v_xor_b32_e32 v53, 0x80000000, v51
	v_cvt_pk_bf16_f32 v53, v53, v53
	ds_write_b16_d16_hi v108, v53 offset:816
	v_xor_b32_e32 v53, 0x80000000, v44
	v_cvt_pk_bf16_f32 v53, v53, v53
	ds_write_b16_d16_hi v108, v53 offset:4352
	v_xor_b32_e32 v53, 0x80000000, v45
	v_cvt_pk_bf16_f32 v53, v53, v53
	ds_write_b16_d16_hi v108, v53 offset:4624
	v_xor_b32_e32 v53, 0x80000000, v46
	v_cvt_pk_bf16_f32 v53, v53, v53
	ds_write_b16_d16_hi v108, v53 offset:4896
	v_xor_b32_e32 v53, 0x80000000, v47
	v_cvt_pk_bf16_f32 v53, v53, v53
	ds_write_b16_d16_hi v108, v53 offset:5168
	v_xor_b32_e32 v53, 0x80000000, v40
	v_cvt_pk_bf16_f32 v53, v53, v53
	ds_write_b16_d16_hi v108, v53 offset:8704
	v_xor_b32_e32 v53, 0x80000000, v41
	v_cvt_pk_bf16_f32 v53, v53, v53
	ds_write_b16_d16_hi v108, v53 offset:8976
	v_xor_b32_e32 v53, 0x80000000, v42
	v_cvt_pk_bf16_f32 v53, v53, v53
	ds_write_b16_d16_hi v108, v53 offset:9248
	v_xor_b32_e32 v53, 0x80000000, v43
	v_cvt_pk_bf16_f32 v53, v53, v53
	ds_write_b16_d16_hi v108, v53 offset:9520
	v_xor_b32_e32 v53, 0x80000000, v36
	v_cvt_pk_bf16_f32 v53, v53, v53
	ds_write_b16_d16_hi v108, v53 offset:13056
	v_xor_b32_e32 v53, 0x80000000, v37
	v_cvt_pk_bf16_f32 v53, v53, v53
	ds_write_b16_d16_hi v108, v53 offset:13328
	v_xor_b32_e32 v53, 0x80000000, v38
	v_cvt_pk_bf16_f32 v53, v53, v53
	ds_write_b16_d16_hi v108, v53 offset:13600
	v_xor_b32_e32 v53, 0x80000000, v39
	v_cvt_pk_bf16_f32 v53, v53, v53
	s_mov_b64 s[10:11], 0
	ds_write_b16_d16_hi v108, v53 offset:13872
.LBB0_725:
	s_lshl_b32 s12, s59, 5
	v_lshlrev_b32_e32 v52, 5, v52
	v_mov_b32_e32 v53, v2
	s_and_b32 s64, s12, 0xfffff800
	s_andn2_b64 vcc, exec, s[10:11]
	v_lshl_add_u64 v[52:53], s[0:1], 0, v[52:53]
	s_cbranch_vccnz .LBB0_727
	v_cvt_pk_bf16_f32 v48, v48, v49
	v_cvt_pk_bf16_f32 v49, v50, v51
	v_cvt_pk_bf16_f32 v50, v44, v45
	v_cvt_pk_bf16_f32 v51, v46, v47
	v_cvt_pk_bf16_f32 v40, v40, v41
	v_cvt_pk_bf16_f32 v41, v42, v43
	v_cvt_pk_bf16_f32 v42, v36, v37
	v_cvt_pk_bf16_f32 v43, v38, v39
	v_lshl_add_u64 v[36:37], s[64:65], 1, v[52:53]
	global_store_dwordx4 v[36:37], v[48:51], off sc0 sc1
	s_nop 1
	v_lshl_add_u64 v[36:37], v[36:37], 0, 16
	global_store_dwordx4 v[36:37], v[40:43], off sc0 sc1
	s_nop 1

; __device__ __forceinline__ void st16_wt(void* p, v4u v) { asm volatile("global_store_dwordx4 %0, %1, off sc0 sc1\n\ts_nop 1" :: "v"(p), "v"(v) : "memory"); }
; __device__ __forceinline__ unsigned f2bf(float f) { unsigned u = __builtin_bit_cast(unsigned, f); return (u + 0x7fffu + ((u >> 16) & 1u)) >> 16; }
; __device__ __forceinline__ unsigned pk2(float lo, float hi) { return f2bf(lo) | (f2bf(hi) << 16); }
; __device__ __forceinline__ void gdn_local_item(const Params& P, LAS unsigned char* lds, int item, int tid, bool defer, int& pend, unsigned& pend_fb) {
;     ...
;             for (int s2 = 0; s2 < 2; ++s2) {
;                 float v[8];
; #pragma unroll
;                 for (int e = 0; e < 8; ++e) { const int sidx = 32 * s2 + 8 * g + e; float x = src[sidx * 132] * sbeta[sidx]; if (isw) x *= seg[sidx]; v[e] = x; }
;                 v4u pk; pk.x = pk2(v[0], v[1]); pk.y = pk2(v[2], v[3]); pk.z = pk2(v[4], v[5]); pk.w = pk2(v[6], v[7]);
;                 bfr[s2] = __builtin_bit_cast(bf16x8, pk);
;             }
;             f32x4 acc[4];
; #pragma unroll
;             for (int rho = 0; rho < 4; ++rho) { acc[rho] = (f32x4){0.f, 0.f, 0.f, 0.f};
; #pragma unroll
;                 for (int s2 = 0; s2 < 2; ++s2) acc[rho] = __builtin_amdgcn_mfma_f32_16x16x32_bf16(af[rho][s2], bfr[s2], acc[rho], 0, 0, 0); }
;             if (!isw) {
;                 v4u o0, o1;
;                 o0.x = pk2(acc[0].x, acc[0].y); o0.y = pk2(acc[0].z, acc[0].w); o0.z = pk2(acc[1].x, acc[1].y); o0.w = pk2(acc[1].z, acc[1].w);
;                 o1.x = pk2(acc[2].x, acc[2].y); o1.y = pk2(acc[2].z, acc[2].w); o1.z = pk2(acc[3].x, acc[3].y); o1.w = pk2(acc[3].z, acc[3].w);
;                 v4u* d = (v4u*)(UF + (size_t)(2 * (wave & 3) + sig) * 1024 + lane * 16);
;                 st16_wt(d, o0); st16_wt(d + 1, o1);
;             } else {
; #pragma unroll
;                 for (int rho = 0; rho < 4; ++rho)
; #pragma unroll
;                     for (int i = 0; i < 4; ++i) wst[(16 * rho + 4 * g + i) * 136 + jj] = (bf16)f2bf(-acc[rho][i]);
;             }
.LBB0_759:
	v_cvt_pk_bf16_f32 v56, v37, v37
	v_cvt_pk_bf16_f32 v37, v39, v39
	v_cvt_pk_bf16_f32 v41, v41, v41
	v_cvt_pk_bf16_f32 v39, v44, v44
	v_cvt_pk_bf16_f32 v42, v42, v42
	v_cvt_pk_bf16_f32 v40, v40, v40
	v_cvt_pk_bf16_f32 v38, v38, v38
	v_cvt_pk_bf16_f32 v36, v36, v36
	v_lshrrev_b32_e32 v36, 16, v36
	v_lshrrev_b32_e32 v44, 16, v38
	v_lshrrev_b32_e32 v38, 16, v40
	v_lshrrev_b32_e32 v40, 16, v42
	v_and_or_b32 v39, v39, s74, v40
	v_and_or_b32 v38, v41, s74, v38
	v_and_or_b32 v37, v37, s74, v44
	v_and_or_b32 v36, v56, s74, v36
	v_cvt_pk_bf16_f32 v44, v45, v45
	v_cvt_pk_bf16_f32 v45, v47, v47
	v_cvt_pk_bf16_f32 v41, v49, v49
	v_cvt_pk_bf16_f32 v3, v3, v3
	v_mfma_f32_16x16x32_bf16 v[32:35], v[32:35], v[36:39], 0
	v_cvt_pk_bf16_f32 v49, v50, v50
	v_cvt_pk_bf16_f32 v47, v48, v48
	v_cvt_pk_bf16_f32 v42, v46, v46
	v_cvt_pk_bf16_f32 v40, v43, v43
	v_lshrrev_b32_e32 v40, 16, v40
	v_lshrrev_b32_e32 v46, 16, v42
	v_lshrrev_b32_e32 v42, 16, v47
	v_lshrrev_b32_e32 v43, 16, v49
	v_and_or_b32 v43, v3, s74, v43
	v_and_or_b32 v42, v41, s74, v42
	v_and_or_b32 v41, v45, s74, v46
	v_and_or_b32 v40, v44, s74, v40
	s_and_b64 vcc, exec, s[6:7]
	s_mov_b64 s[0:1], -1
	v_mfma_f32_16x16x32_bf16 v[32:35], v[4:7], v[40:43], v[32:35]
	v_mfma_f32_16x16x32_bf16 v[4:7], v[8:11], v[36:39], 0
	v_mfma_f32_16x16x32_bf16 v[12:15], v[12:15], v[40:43], v[4:7]
	v_mfma_f32_16x16x32_bf16 v[4:7], v[16:19], v[36:39], 0
	v_mfma_f32_16x16x32_bf16 v[8:11], v[20:23], v[40:43], v[4:7]
	v_mfma_f32_16x16x32_bf16 v[4:7], v[24:27], v[36:39], 0
	v_mfma_f32_16x16x32_bf16 v[4:7], v[28:31], v[40:43], v[4:7]
	s_cbranch_vccnz .LBB0_761
	s_nop 0
	v_xor_b32_e32 v3, 0x80000000, v32
	v_cvt_pk_bf16_f32 v3, v3, v3
	v_add3_u32 v16, s54, v106, v105
	ds_write_b16_d16_hi v16, v3 offset:32
	v_xor_b32_e32 v3, 0x80000000, v33
	v_cvt_pk_bf16_f32 v3, v3, v3
	ds_write_b16_d16_hi v16, v3 offset:304
	v_xor_b32_e32 v3, 0x80000000, v34
	v_cvt_pk_bf16_f32 v3, v3, v3
	ds_write_b16_d16_hi v16, v3 offset:576
	v_xor_b32_e32 v3, 0x80000000, v35
	v_cvt_pk_bf16_f32 v3, v3, v3
	ds_write_b16_d16_hi v16, v3 offset:848
	v_xor_b32_e32 v3, 0x80000000, v12
	v_cvt_pk_bf16_f32 v3, v3, v3
	ds_write_b16_d16_hi v16, v3 offset:4384
	v_xor_b32_e32 v3, 0x80000000, v13
	v_cvt_pk_bf16_f32 v3, v3, v3
	ds_write_b16_d16_hi v16, v3 offset:4656
	v_xor_b32_e32 v3, 0x80000000, v14
	v_cvt_pk_bf16_f32 v3, v3, v3
	ds_write_b16_d16_hi v16, v3 offset:4928
	v_xor_b32_e32 v3, 0x80000000, v15
	v_cvt_pk_bf16_f32 v3, v3, v3
	ds_write_b16_d16_hi v16, v3 offset:5200
	v_xor_b32_e32 v3, 0x80000000, v8
	v_cvt_pk_bf16_f32 v3, v3, v3
	ds_write_b16_d16_hi v16, v3 offset:8736
	v_xor_b32_e32 v3, 0x80000000, v9
	v_cvt_pk_bf16_f32 v3, v3, v3
	ds_write_b16_d16_hi v16, v3 offset:9008
	v_xor_b32_e32 v3, 0x80000000, v10
	v_cvt_pk_bf16_f32 v3, v3, v3
	ds_write_b16_d16_hi v16, v3 offset:9280
	v_xor_b32_e32 v3, 0x80000000, v11
	v_cvt_pk_bf16_f32 v3, v3, v3
	ds_write_b16_d16_hi v16, v3 offset:9552
	v_xor_b32_e32 v3, 0x80000000, v4
	v_cvt_pk_bf16_f32 v3, v3, v3
	ds_write_b16_d16_hi v16, v3 offset:13088
	v_xor_b32_e32 v3, 0x80000000, v5
	v_cvt_pk_bf16_f32 v3, v3, v3
	ds_write_b16_d16_hi v16, v3 offset:13360
	v_xor_b32_e32 v3, 0x80000000, v6
	v_cvt_pk_bf16_f32 v3, v3, v3
	ds_write_b16_d16_hi v16, v3 offset:13632
	v_xor_b32_e32 v3, 0x80000000, v7
	v_cvt_pk_bf16_f32 v3, v3, v3
	s_mov_b64 s[0:1], 0
	ds_write_b16_d16_hi v16, v3 offset:13904
.LBB0_761:
	s_andn2_b64 vcc, exec, s[0:1]
	s_cbranch_vccnz .LBB0_763
	v_cvt_pk_bf16_f32 v16, v32, v33
	v_cvt_pk_bf16_f32 v17, v34, v35
	v_cvt_pk_bf16_f32 v18, v12, v13
	v_cvt_pk_bf16_f32 v19, v14, v15
	v_cvt_pk_bf16_f32 v8, v8, v9
	v_cvt_pk_bf16_f32 v9, v10, v11
	v_cvt_pk_bf16_f32 v10, v4, v5
	v_cvt_pk_bf16_f32 v11, v6, v7
	v_lshl_add_u64 v[4:5], s[64:65], 1, v[52:53]
	s_mov_b64 s[0:1], 0x800
	v_lshl_add_u64 v[6:7], v[4:5], 0, s[0:1]
	global_store_dwordx4 v[6:7], v[16:19], off sc0 sc1
	s_nop 1
	s_mov_b64 s[0:1], 0x810
	v_lshl_add_u64 v[4:5], v[4:5], 0, s[0:1]
	global_store_dwordx4 v[4:5], v[8:11], off sc0 sc1
	s_nop 1

; #define LAS __attribute__((address_space(3)))
; __device__ __forceinline__ unsigned pk2(float lo, float hi) { return f2bf(lo) | (f2bf(hi) << 16); }
; __device__ __forceinline__ void gdn_local_item(const Params& P, LAS unsigned char* lds, int item, int tid, bool defer, int& pend, unsigned& pend_fb) {
;     ...
;             if (part <= 1) {
;                 LAS bf16* dst = (part == 0 ? qb16 : kb16) + c * 136 + grp * 16;
;                 v4u o0, o1; o0.x = pk2(y[0], y[1]); o0.y = pk2(y[2], y[3]); o0.z = pk2(y[4], y[5]); o0.w = pk2(y[6], y[7]);
;                 o1.x = pk2(y[8], y[9]); o1.y = pk2(y[10], y[11]); o1.z = pk2(y[12], y[13]); o1.w = pk2(y[14], y[15]);
;                 *(LAS v4u*)dst = o0; *(LAS v4u*)(dst + 8) = o1;
.LBB0_809:
	s_andn2_b64 vcc, exec, s[10:11]
	s_cbranch_vccnz .LBB0_804
	v_cvt_pk_bf16_f32 v2, v2, v3
	v_cvt_pk_bf16_f32 v3, v4, v5
	v_cvt_pk_bf16_f32 v4, v6, v7
	v_cvt_pk_bf16_f32 v5, v8, v9
	v_cvt_pk_bf16_f32 v6, v14, v15
	v_cvt_pk_bf16_f32 v7, v16, v17
	s_cmp_eq_u32 s12, 0
	s_mov_b32 s0, 0x14c00
	v_cvt_pk_bf16_f32 v8, v10, v11
	s_cselect_b32 s0, s0, 0x10800
	s_add_i32 s0, s0, 0
	v_add3_u32 v18, s0, v46, v50
	v_cvt_pk_bf16_f32 v9, v12, v13
	ds_write_b128 v18, v[2:5]
	ds_write_b128 v18, v[6:9] offset:16
	s_branch .LBB0_804

; __device__ __forceinline__ unsigned f2bf(float f) { unsigned u = __builtin_bit_cast(unsigned, f); return (u + 0x7fffu + ((u >> 16) & 1u)) >> 16; }
; __device__ __forceinline__ void gdn_local_item(const Params& P, LAS unsigned char* lds, int item, int tid, bool defer, int& pend, unsigned& pend_fb) {
;     ...
;             const int sidx = 16 * sig + col; const float gs = sgc[sidx];
; #pragma unroll
;             for (int i = 0; i < 4; ++i) {
;                 const int c = 16 * rho + 4 * g + i;
;                 const float dec = (c >= sidx) ? __expf(sgc[c] - gs) : 0.f;
;                 if (mat == 0) AmT[sidx * 68 + c] = (c > sidx) ? sbeta[c] * acc[i] * dec : 0.f;
;                 else atts[c * 64 + sidx] = (bf16)f2bf(acc[i] * dec);
;             }
.LBB0_818:
	s_or_b64 exec, exec, s[0:1]
	v_mul_u32_u24_e32 v27, 0x110, v86
	v_lshl_add_u32 v30, v86, 1, s30
	s_mov_b64 s[0:1], -1
	s_and_b64 vcc, exec, s[10:11]
	s_cbranch_vccz .LBB0_820
	v_mul_f32_e32 v24, v18, v23
	s_movk_i32 s0, 0x7fff
	v_cvt_pk_bf16_f32 v24, v24, v24
	v_lshl_add_u32 v25, v22, 7, v30
	ds_write_b16_d16_hi v25, v24
	s_mov_b64 s[0:1], 0

; __device__ __forceinline__ unsigned f2bf(float f) { unsigned u = __builtin_bit_cast(unsigned, f); return (u + 0x7fffu + ((u >> 16) & 1u)) >> 16; }
; __device__ __forceinline__ void gdn_local_item(const Params& P, LAS unsigned char* lds, int item, int tid, bool defer, int& pend, unsigned& pend_fb) {
;     ...
;             const int sidx = 16 * sig + col; const float gs = sgc[sidx];
; #pragma unroll
;             for (int i = 0; i < 4; ++i) {
;                 const int c = 16 * rho + 4 * g + i;
;                 const float dec = (c >= sidx) ? __expf(sgc[c] - gs) : 0.f;
;                 if (mat == 0) AmT[sidx * 68 + c] = (c > sidx) ? sbeta[c] * acc[i] * dec : 0.f;
;                 else atts[c * 64 + sidx] = (bf16)f2bf(acc[i] * dec);
;             }
.LBB0_826:
	s_or_b64 exec, exec, s[0:1]
	v_cndmask_b32_e64 v24, 0, 1, s[10:11]
	v_cmp_ne_u32_e64 s[6:7], 1, v24
	s_andn2_b64 vcc, exec, s[10:11]
	s_mov_b64 s[0:1], -1
	s_cbranch_vccnz .LBB0_828
	v_mul_f32_e32 v24, v19, v18
	s_movk_i32 s0, 0x7fff
	v_cvt_pk_bf16_f32 v24, v24, v24
	v_lshl_add_u32 v25, v23, 7, v30
	s_mov_b64 s[0:1], 0
	ds_write_b16_d16_hi v25, v24

; __device__ __forceinline__ unsigned f2bf(float f) { unsigned u = __builtin_bit_cast(unsigned, f); return (u + 0x7fffu + ((u >> 16) & 1u)) >> 16; }
; __device__ __forceinline__ void gdn_local_item(const Params& P, LAS unsigned char* lds, int item, int tid, bool defer, int& pend, unsigned& pend_fb) {
;     ...
;             const int sidx = 16 * sig + col; const float gs = sgc[sidx];
; #pragma unroll
;             for (int i = 0; i < 4; ++i) {
;                 const int c = 16 * rho + 4 * g + i;
;                 const float dec = (c >= sidx) ? __expf(sgc[c] - gs) : 0.f;
;                 if (mat == 0) AmT[sidx * 68 + c] = (c > sidx) ? sbeta[c] * acc[i] * dec : 0.f;
;                 else atts[c * 64 + sidx] = (bf16)f2bf(acc[i] * dec);
;             }
.LBB0_843:
	v_mul_f32_e32 v19, v20, v18
	s_movk_i32 s0, 0x7fff
	v_cvt_pk_bf16_f32 v19, v19, v19
	v_lshl_add_u32 v25, v24, 7, v30
	ds_write_b16_d16_hi v25, v19
	s_cbranch_execnz .LBB0_847

; __device__ __forceinline__ unsigned f2bf(float f) { unsigned u = __builtin_bit_cast(unsigned, f); return (u + 0x7fffu + ((u >> 16) & 1u)) >> 16; }
; __device__ __forceinline__ void gdn_local_item(const Params& P, LAS unsigned char* lds, int item, int tid, bool defer, int& pend, unsigned& pend_fb) {
;     ...
;             const int sidx = 16 * sig + col; const float gs = sgc[sidx];
; #pragma unroll
;             for (int i = 0; i < 4; ++i) {
;                 const int c = 16 * rho + 4 * g + i;
;                 const float dec = (c >= sidx) ? __expf(sgc[c] - gs) : 0.f;
;                 if (mat == 0) AmT[sidx * 68 + c] = (c > sidx) ? sbeta[c] * acc[i] * dec : 0.f;
;                 else atts[c * 64 + sidx] = (bf16)f2bf(acc[i] * dec);
;             }
.LBB0_851:
	v_mul_f32_e32 v19, v21, v18
	s_movk_i32 s0, 0x7fff
	v_cvt_pk_bf16_f32 v19, v19, v19
	v_lshl_add_u32 v20, v25, 7, v30
	ds_write_b16_d16_hi v20, v19
	s_cbranch_execnz .LBB0_855

; __device__ __forceinline__ unsigned f2bf(float f) { unsigned u = __builtin_bit_cast(unsigned, f); return (u + 0x7fffu + ((u >> 16) & 1u)) >> 16; }
; __device__ __forceinline__ void gdn_local_item(const Params& P, LAS unsigned char* lds, int item, int tid, bool defer, int& pend, unsigned& pend_fb) {
;     ...
;             const int sidx = 16 * sig + col; const float gs = sgc[sidx];
; #pragma unroll
;             for (int i = 0; i < 4; ++i) {
;                 const int c = 16 * rho + 4 * g + i;
;                 const float dec = (c >= sidx) ? __expf(sgc[c] - gs) : 0.f;
;                 if (mat == 0) AmT[sidx * 68 + c] = (c > sidx) ? sbeta[c] * acc[i] * dec : 0.f;
;                 else atts[c * 64 + sidx] = (bf16)f2bf(acc[i] * dec);
;             }
.LBB0_869:
	s_or_b64 exec, exec, s[0:1]
	s_mov_b64 s[0:1], -1
	s_and_b64 vcc, exec, s[6:7]
	s_waitcnt lgkmcnt(0)
	v_lshlrev_b32_e32 v28, 7, v25
	s_cbranch_vccnz .LBB0_871
	v_mul_f32_e32 v19, v21, v18
	s_movk_i32 s0, 0x7fff
	v_cvt_pk_bf16_f32 v19, v19, v19
	v_add3_u32 v20, s30, v28, v34
	s_mov_b64 s[0:1], 0
	ds_write_b16_d16_hi v20, v19

; __device__ __forceinline__ unsigned f2bf(float f) { unsigned u = __builtin_bit_cast(unsigned, f); return (u + 0x7fffu + ((u >> 16) & 1u)) >> 16; }
; __device__ __forceinline__ void gdn_local_item(const Params& P, LAS unsigned char* lds, int item, int tid, bool defer, int& pend, unsigned& pend_fb) {
;     ...
;             const int sidx = 16 * sig + col; const float gs = sgc[sidx];
; #pragma unroll
;             for (int i = 0; i < 4; ++i) {
;                 const int c = 16 * rho + 4 * g + i;
;                 const float dec = (c >= sidx) ? __expf(sgc[c] - gs) : 0.f;
;                 if (mat == 0) AmT[sidx * 68 + c] = (c > sidx) ? sbeta[c] * acc[i] * dec : 0.f;
;                 else atts[c * 64 + sidx] = (bf16)f2bf(acc[i] * dec);
;             }
.LBB0_888:
	v_mul_f32_e32 v30, v18, v29
	s_movk_i32 s0, 0x7fff
	v_cvt_pk_bf16_f32 v30, v30, v30
	v_add3_u32 v33, s30, v27, v34
	ds_write_b16_d16_hi v33, v30
	v_add_u32_e32 v33, s31, v31
	s_cbranch_execnz .LBB0_859

; __device__ __forceinline__ unsigned f2bf(float f) { unsigned u = __builtin_bit_cast(unsigned, f); return (u + 0x7fffu + ((u >> 16) & 1u)) >> 16; }
; __device__ __forceinline__ void gdn_local_item(const Params& P, LAS unsigned char* lds, int item, int tid, bool defer, int& pend, unsigned& pend_fb) {
;     ...
;             const int sidx = 16 * sig + col; const float gs = sgc[sidx];
; #pragma unroll
;             for (int i = 0; i < 4; ++i) {
;                 const int c = 16 * rho + 4 * g + i;
;                 const float dec = (c >= sidx) ? __expf(sgc[c] - gs) : 0.f;
;                 if (mat == 0) AmT[sidx * 68 + c] = (c > sidx) ? sbeta[c] * acc[i] * dec : 0.f;
;                 else atts[c * 64 + sidx] = (bf16)f2bf(acc[i] * dec);
;             }
.LBB0_892:
	v_mul_f32_e32 v29, v19, v18
	s_movk_i32 s0, 0x7fff
	v_cvt_pk_bf16_f32 v29, v29, v29
	v_add3_u32 v35, s30, v30, v34
	ds_write_b16_d16_hi v35, v29
	s_cbranch_execnz .LBB0_863

; __device__ __forceinline__ unsigned f2bf(float f) { unsigned u = __builtin_bit_cast(unsigned, f); return (u + 0x7fffu + ((u >> 16) & 1u)) >> 16; }
; __device__ __forceinline__ void gdn_local_item(const Params& P, LAS unsigned char* lds, int item, int tid, bool defer, int& pend, unsigned& pend_fb) {
;     ...
;             const int sidx = 16 * sig + col; const float gs = sgc[sidx];
; #pragma unroll
;             for (int i = 0; i < 4; ++i) {
;                 const int c = 16 * rho + 4 * g + i;
;                 const float dec = (c >= sidx) ? __expf(sgc[c] - gs) : 0.f;
;                 if (mat == 0) AmT[sidx * 68 + c] = (c > sidx) ? sbeta[c] * acc[i] * dec : 0.f;
;                 else atts[c * 64 + sidx] = (bf16)f2bf(acc[i] * dec);
;             }
.LBB0_896:
	v_mul_f32_e32 v19, v20, v18
	s_movk_i32 s0, 0x7fff
	v_cvt_pk_bf16_f32 v19, v19, v19
	v_add3_u32 v35, s30, v29, v34
	ds_write_b16_d16_hi v35, v19
	s_cbranch_execnz .LBB0_867

; __device__ __forceinline__ unsigned f2bf(float f) { unsigned u = __builtin_bit_cast(unsigned, f); return (u + 0x7fffu + ((u >> 16) & 1u)) >> 16; }
; __device__ __forceinline__ void gdn_local_item(const Params& P, LAS unsigned char* lds, int item, int tid, bool defer, int& pend, unsigned& pend_fb) {
;     ...
;             const int sidx = 16 * sig + col; const float gs = sgc[sidx];
; #pragma unroll
;             for (int i = 0; i < 4; ++i) {
;                 const int c = 16 * rho + 4 * g + i;
;                 const float dec = (c >= sidx) ? __expf(sgc[c] - gs) : 0.f;
;                 if (mat == 0) AmT[sidx * 68 + c] = (c > sidx) ? sbeta[c] * acc[i] * dec : 0.f;
;                 else atts[c * 64 + sidx] = (bf16)f2bf(acc[i] * dec);
;             }
.LBB0_900:
	s_nop 0
	v_mul_f32_e32 v33, v18, v36
	s_movk_i32 s0, 0x7fff
	v_cvt_pk_bf16_f32 v33, v33, v33
	v_add3_u32 v37, s30, v27, v35
	ds_write_b16_d16_hi v37, v33
	v_add_u32_e32 v33, s31, v31
	s_cbranch_execnz .LBB0_879

; __device__ __forceinline__ unsigned f2bf(float f) { unsigned u = __builtin_bit_cast(unsigned, f); return (u + 0x7fffu + ((u >> 16) & 1u)) >> 16; }
; __device__ __forceinline__ void gdn_local_item(const Params& P, LAS unsigned char* lds, int item, int tid, bool defer, int& pend, unsigned& pend_fb) {
;     ...
;             const int sidx = 16 * sig + col; const float gs = sgc[sidx];
; #pragma unroll
;             for (int i = 0; i < 4; ++i) {
;                 const int c = 16 * rho + 4 * g + i;
;                 const float dec = (c >= sidx) ? __expf(sgc[c] - gs) : 0.f;
;                 if (mat == 0) AmT[sidx * 68 + c] = (c > sidx) ? sbeta[c] * acc[i] * dec : 0.f;
;                 else atts[c * 64 + sidx] = (bf16)f2bf(acc[i] * dec);
;             }
.LBB0_910:
	v_mul_f32_e32 v19, v20, v18
	s_movk_i32 s0, 0x7fff
	v_cvt_pk_bf16_f32 v19, v19, v19
	v_add3_u32 v36, s30, v29, v35
	ds_write_b16_d16_hi v36, v19
	s_cbranch_execnz .LBB0_885

; __device__ __forceinline__ unsigned f2bf(float f) { unsigned u = __builtin_bit_cast(unsigned, f); return (u + 0x7fffu + ((u >> 16) & 1u)) >> 16; }
; __device__ __forceinline__ void gdn_local_item(const Params& P, LAS unsigned char* lds, int item, int tid, bool defer, int& pend, unsigned& pend_fb) {
;     ...
;             const int sidx = 16 * sig + col; const float gs = sgc[sidx];
; #pragma unroll
;             for (int i = 0; i < 4; ++i) {
;                 const int c = 16 * rho + 4 * g + i;
;                 const float dec = (c >= sidx) ? __expf(sgc[c] - gs) : 0.f;
;                 if (mat == 0) AmT[sidx * 68 + c] = (c > sidx) ? sbeta[c] * acc[i] * dec : 0.f;
;                 else atts[c * 64 + sidx] = (bf16)f2bf(acc[i] * dec);
;             }
.LBB0_915:
	v_mul_f32_e32 v19, v21, v18
	s_movk_i32 s0, 0x7fff
	v_cvt_pk_bf16_f32 v19, v19, v19
	v_add3_u32 v20, s30, v28, v35
	ds_write_b16_d16_hi v20, v19
	s_cbranch_execnz .LBB0_919

; __device__ __forceinline__ unsigned f2bf(float f) { unsigned u = __builtin_bit_cast(unsigned, f); return (u + 0x7fffu + ((u >> 16) & 1u)) >> 16; }
; __device__ __forceinline__ void gdn_local_item(const Params& P, LAS unsigned char* lds, int item, int tid, bool defer, int& pend, unsigned& pend_fb) {
;     ...
;             const int sidx = 16 * sig + col; const float gs = sgc[sidx];
; #pragma unroll
;             for (int i = 0; i < 4; ++i) {
;                 const int c = 16 * rho + 4 * g + i;
;                 const float dec = (c >= sidx) ? __expf(sgc[c] - gs) : 0.f;
;                 if (mat == 0) AmT[sidx * 68 + c] = (c > sidx) ? sbeta[c] * acc[i] * dec : 0.f;
;                 else atts[c * 64 + sidx] = (bf16)f2bf(acc[i] * dec);
;             }
.LBB0_932:
	v_mul_f32_e32 v6, v2, v19
	s_movk_i32 s0, 0x7fff
	v_cvt_pk_bf16_f32 v6, v6, v6
	v_add3_u32 v9, s30, v27, v8
	ds_write_b16_d16_hi v9, v6
	v_add_u32_e32 v6, s31, v20
	s_cbranch_execnz .LBB0_923

; __device__ __forceinline__ unsigned f2bf(float f) { unsigned u = __builtin_bit_cast(unsigned, f); return (u + 0x7fffu + ((u >> 16) & 1u)) >> 16; }
; __device__ __forceinline__ void gdn_local_item(const Params& P, LAS unsigned char* lds, int item, int tid, bool defer, int& pend, unsigned& pend_fb) {
;     ...
;             const int sidx = 16 * sig + col; const float gs = sgc[sidx];
; #pragma unroll
;             for (int i = 0; i < 4; ++i) {
;                 const int c = 16 * rho + 4 * g + i;
;                 const float dec = (c >= sidx) ? __expf(sgc[c] - gs) : 0.f;
;                 if (mat == 0) AmT[sidx * 68 + c] = (c > sidx) ? sbeta[c] * acc[i] * dec : 0.f;
;                 else atts[c * 64 + sidx] = (bf16)f2bf(acc[i] * dec);
;             }
.LBB0_937:
	v_mul_f32_e32 v9, v3, v2
	s_movk_i32 s0, 0x7fff
	v_cvt_pk_bf16_f32 v9, v9, v9
	v_add3_u32 v10, s30, v30, v8
	ds_write_b16_d16_hi v10, v9
	s_cbranch_execnz .LBB0_926

; __device__ __forceinline__ unsigned f2bf(float f) { unsigned u = __builtin_bit_cast(unsigned, f); return (u + 0x7fffu + ((u >> 16) & 1u)) >> 16; }
; __device__ __forceinline__ void gdn_local_item(const Params& P, LAS unsigned char* lds, int item, int tid, bool defer, int& pend, unsigned& pend_fb) {
;     ...
;             const int sidx = 16 * sig + col; const float gs = sgc[sidx];
; #pragma unroll
;             for (int i = 0; i < 4; ++i) {
;                 const int c = 16 * rho + 4 * g + i;
;                 const float dec = (c >= sidx) ? __expf(sgc[c] - gs) : 0.f;
;                 if (mat == 0) AmT[sidx * 68 + c] = (c > sidx) ? sbeta[c] * acc[i] * dec : 0.f;
;                 else atts[c * 64 + sidx] = (bf16)f2bf(acc[i] * dec);
;             }
.LBB0_942:
	v_mul_f32_e32 v3, v4, v2
	s_movk_i32 s0, 0x7fff
	v_cvt_pk_bf16_f32 v3, v3, v3
	v_add3_u32 v9, s30, v29, v8
	ds_write_b16_d16_hi v9, v3
	s_cbranch_execnz .LBB0_929

; __device__ __forceinline__ unsigned f2bf(float f) { unsigned u = __builtin_bit_cast(unsigned, f); return (u + 0x7fffu + ((u >> 16) & 1u)) >> 16; }
; __device__ __forceinline__ void gdn_local_item(const Params& P, LAS unsigned char* lds, int item, int tid, bool defer, int& pend, unsigned& pend_fb) {
;     ...
;             const int sidx = 16 * sig + col; const float gs = sgc[sidx];
; #pragma unroll
;             for (int i = 0; i < 4; ++i) {
;                 const int c = 16 * rho + 4 * g + i;
;                 const float dec = (c >= sidx) ? __expf(sgc[c] - gs) : 0.f;
;                 if (mat == 0) AmT[sidx * 68 + c] = (c > sidx) ? sbeta[c] * acc[i] * dec : 0.f;
;                 else atts[c * 64 + sidx] = (bf16)f2bf(acc[i] * dec);
;             }
.LBB0_947:
	v_mul_f32_e32 v3, v5, v2
	s_movk_i32 s0, 0x7fff
	v_cvt_pk_bf16_f32 v3, v3, v3
	v_add3_u32 v4, s30, v28, v8
	ds_write_b16_d16_hi v4, v3
	s_cbranch_execnz .LBB0_951

; #define LAS __attribute__((address_space(3)))
; __device__ __forceinline__ void st16_wt(void* p, v4u v) { asm volatile("global_store_dwordx4 %0, %1, off sc0 sc1\n\ts_nop 1" :: "v"(p), "v"(v) : "memory"); }
; __device__ __forceinline__ unsigned pk2(float lo, float hi) { return f2bf(lo) | (f2bf(hi) << 16); }
; #define GL_REPF(k) for (int rr_ = 0; rr_ < ((GL_REP_STEP == (k)) ? 2 : 1); ++rr_)
; __device__ __forceinline__ void gdn_local_item(const Params& P, LAS unsigned char* lds, int item, int tid, bool defer, int& pend, unsigned& pend_fb) {
;     ...
;     GL_REPF(4) {
;         bf16* QD = (bf16*)(ws + WS_QD) + (size_t)item * 8192;
;         bf16* KD = (bf16*)(ws + WS_KD) + (size_t)item * 8192;
;         bf16* ATT = (bf16*)(ws + WS_ATT) + (size_t)item * 4096;
; #pragma unroll
;         for (int r = 0; r < 2; ++r) {
;             const int id = tid + 512 * r;
;             { const int c = id >> 4, gam = id & 15, s32 = gam >> 2, g = gam & 3;
;               const v2u lo = *(const LAS v2u*)(qb16 + c * 136 + 32 * s32 + 4 * g), hi = *(const LAS v2u*)(qb16 + c * 136 + 32 * s32 + 16 + 4 * g);
;               const float e = seg[c];
;               v4u o; o.x = pk2(bflo(lo.x) * e, bfhi(lo.x) * e); o.y = pk2(bflo(lo.y) * e, bfhi(lo.y) * e); o.z = pk2(bflo(hi.x) * e, bfhi(hi.x) * e); o.w = pk2(bflo(hi.y) * e, bfhi(hi.y) * e);
;               st16_wt(QD + c * 128 + 8 * gam, o); }
;             { const int dk = id >> 3, gam = id & 7, s32 = gam >> 2, g = gam & 3, c0 = 32 * s32 + 4 * g;
;               float v[8];
; #pragma unroll
;               for (int j = 0; j < 4; ++j) { v[j] = ks[(c0 + j) * 132 + dk] * sek[c0 + j]; v[4 + j] = ks[(c0 + 16 + j) * 132 + dk] * sek[c0 + 16 + j]; }
;               v4u o; o.x = pk2(v[0], v[1]); o.y = pk2(v[2], v[3]); o.z = pk2(v[4], v[5]); o.w = pk2(v[6], v[7]);
;               st16_wt(KD + dk * 64 + 8 * gam, o); }
;         }
.LBB0_951:
	v_lshlrev_b32_e32 v88, 3, v86
	v_and_b32_e32 v89, 0x60, v88
	v_and_b32_e32 v12, 12, v44
	v_ashrrev_i32_e32 v17, 4, v84
	s_movk_i32 s58, 0x110
	v_lshl_add_u32 v3, v89, 1, s56
	s_waitcnt lgkmcnt(0)
	v_and_b32_e32 v7, 32, v43
	v_mul_lo_u32 v91, v17, s58
	v_lshlrev_b32_e32 v90, 1, v12
	s_waitcnt lgkmcnt(0)
	s_barrier
	v_or_b32_e32 v28, v7, v12
	v_add3_u32 v12, v3, v91, v90
	ds_read2_b64 v[12:15], v12 offset1:4
	v_lshl_add_u32 v16, v17, 2, s85
	ds_read_b32 v16, v16
	s_mov_b32 s65, 0
	s_lshl_b64 s[0:1], s[64:65], 13
	s_waitcnt lgkmcnt(1)
	v_lshlrev_b32_e32 v19, 16, v13
	v_lshlrev_b32_e32 v18, 16, v12
	v_and_b32_e32 v13, 0xffff0000, v13
	v_and_b32_e32 v12, 0xffff0000, v12
	v_lshlrev_b32_e32 v21, 16, v15
	v_lshlrev_b32_e32 v20, 16, v14
	v_and_b32_e32 v15, 0xffff0000, v15
	v_and_b32_e32 v14, 0xffff0000, v14
	s_waitcnt lgkmcnt(0)
	v_pk_mul_f32 v[12:13], v[16:17], v[12:13] op_sel_hi:[0,1]
	v_pk_mul_f32 v[14:15], v[16:17], v[14:15] op_sel_hi:[0,1]
	s_lshl_b64 s[8:9], s[64:65], 14
	v_pk_mul_f32 v[18:19], v[16:17], v[18:19] op_sel_hi:[0,1]
	v_pk_mul_f32 v[20:21], v[16:17], v[20:21] op_sel_hi:[0,1]
	s_movk_i32 s59, 0x7fff
	s_add_u32 s14, s53, s8
	v_mov_b32_e32 v2, 0
	v_cvt_pk_bf16_f32 v13, v13, v13
	v_cvt_pk_bf16_f32 v14, v14, v14
	s_addc_u32 s15, s97, s9
	v_lshlrev_b32_e32 v4, 4, v86
	v_mov_b32_e32 v5, v2
	v_cvt_pk_bf16_f32 v12, v12, v12
	v_cvt_pk_bf16_f32 v15, v15, v15
	v_cvt_pk_bf16_f32 v20, v20, v20
	v_cvt_pk_bf16_f32 v19, v19, v19
	v_lshl_add_u64 v[10:11], s[14:15], 0, v[4:5]
	s_mov_b32 s14, 0xffff0000
	v_cvt_pk_bf16_f32 v21, v21, v21
	v_cvt_pk_bf16_f32 v16, v18, v18
	v_lshrrev_b32_e32 v18, 16, v19
	v_lshrrev_b32_e32 v19, 16, v20
	v_lshlrev_b32_e32 v70, 7, v17
	v_lshrrev_b32_e32 v16, 16, v16
	v_lshrrev_b32_e32 v20, 16, v21
	v_and_or_b32 v14, v14, s14, v19
	v_ashrrev_i32_e32 v71, 31, v70
	v_and_or_b32 v15, v15, s14, v20
	v_and_or_b32 v13, v13, s14, v18
	v_and_or_b32 v12, v12, s14, v16
	v_lshl_add_u64 v[16:17], v[70:71], 1, v[10:11]
	global_store_dwordx4 v[16:17], v[12:15], off sc0 sc1
	s_nop 1
	v_lshl_add_u32 v14, v28, 2, 0
	s_movk_i32 s15, 0x210
	v_add_u32_e32 v31, 0x27500, v14
	v_mov_b32_e32 v14, 0x2100
	v_lshl_add_u32 v12, v85, 2, 0
	v_mad_u32_u24 v32, v28, s15, v14
	v_mad_u32_u24 v13, v28, s15, v12
	v_add_u32_e32 v12, v12, v32
	ds_read_b32 v18, v12
	v_add_u32_e32 v12, 0x2200, v13
	ds_read2_b32 v[20:21], v12 offset0:68 offset1:200
	v_add_u32_e32 v12, 0x400, v13
	ds_read2_b32 v[16:17], v13 offset1:132
	ds_read2_b32 v[22:23], v12 offset0:8 offset1:140
	ds_read_b32 v33, v13 offset:10032
	ds_read_b128 v[12:15], v31
	s_add_u32 s16, s86, s8
	s_waitcnt lgkmcnt(4)
	v_mov_b32_e32 v19, v21
	s_waitcnt lgkmcnt(2)
	v_mov_b32_e32 v25, v22
	v_mov_b32_e32 v22, v17
	s_waitcnt lgkmcnt(0)
	v_mov_b32_e32 v27, v14
	v_mov_b32_e32 v14, v13
	v_mov_b32_e32 v24, v16
	v_mov_b32_e32 v26, v12
	v_pk_mul_f32 v[16:17], v[22:23], v[14:15]
	ds_read_b128 v[12:15], v31 offset:64
	v_mov_b32_e32 v21, v33
	v_pk_mul_f32 v[24:25], v[24:25], v[26:27]
	v_and_b32_e32 v4, 56, v43
	s_addc_u32 s17, s52, s9
	s_waitcnt lgkmcnt(0)
	v_mov_b32_e32 v23, v14
	v_mov_b32_e32 v14, v13
	v_mov_b32_e32 v22, v12
	v_pk_mul_f32 v[12:13], v[20:21], v[14:15]
	v_pk_mul_f32 v[18:19], v[18:19], v[22:23]
	v_cvt_pk_bf16_f32 v17, v17, v17
	v_cvt_pk_bf16_f32 v13, v13, v13
	v_cvt_pk_bf16_f32 v16, v16, v16
	v_cvt_pk_bf16_f32 v12, v12, v12
	v_cvt_pk_bf16_f32 v18, v18, v18
	v_cvt_pk_bf16_f32 v14, v24, v24
	v_cvt_pk_bf16_f32 v19, v19, v19
	v_cvt_pk_bf16_f32 v15, v25, v25
	v_lshrrev_b32_e32 v20, 16, v14
	v_lshrrev_b32_e32 v14, 16, v18
	v_lshlrev_b32_e32 v4, 1, v4
	v_lshrrev_b32_e32 v21, 16, v15
	v_lshrrev_b32_e32 v15, 16, v19
	v_and_or_b32 v14, v12, s14, v14
	v_and_or_b32 v12, v16, s14, v20
	v_lshlrev_b32_e32 v16, 6, v85
	v_lshl_add_u64 v[8:9], s[16:17], 0, v[4:5]
	v_and_or_b32 v15, v13, s14, v15
	v_and_or_b32 v13, v17, s14, v21
	v_ashrrev_i32_e32 v17, 31, v16
	v_lshl_add_u64 v[16:17], v[16:17], 1, v[8:9]
	global_store_dwordx4 v[16:17], v[12:15], off sc0 sc1
	s_nop 1
	v_ashrrev_i32_e32 v17, 4, v42
	v_mul_lo_u32 v92, v17, s58
	v_add3_u32 v3, v3, v92, v90
	ds_read2_b64 v[12:15], v3 offset1:4
	v_lshl_add_u32 v3, v17, 2, s85
	ds_read_b32 v16, v3
	v_lshlrev_b32_e32 v72, 7, v17
	v_ashrrev_i32_e32 v73, 31, v72
	s_waitcnt lgkmcnt(1)
	v_lshlrev_b32_e32 v19, 16, v13
	v_lshlrev_b32_e32 v18, 16, v12
	v_and_b32_e32 v13, 0xffff0000, v13
	v_and_b32_e32 v12, 0xffff0000, v12
	v_lshlrev_b32_e32 v21, 16, v15
	v_lshlrev_b32_e32 v20, 16, v14
	v_and_b32_e32 v15, 0xffff0000, v15
	v_and_b32_e32 v14, 0xffff0000, v14
	s_waitcnt lgkmcnt(0)
; #define LAS __attribute__((address_space(3)))
; #define GL_REPF(k) for (int rr_ = 0; rr_ < ((GL_REP_STEP == (k)) ? 2 : 1); ++rr_)
; __device__ __forceinline__ void gdn_local_item(const Params& P, LAS unsigned char* lds, int item, int tid, bool defer, int& pend, unsigned& pend_fb) {
;     ...
;             { const int c = id >> 4, gam = id & 15, s32 = gam >> 2, g = gam & 3;
;               const v2u lo = *(const LAS v2u*)(qb16 + c * 136 + 32 * s32 + 4 * g), hi = *(const LAS v2u*)(qb16 + c * 136 + 32 * s32 + 16 + 4 * g);
;               const float e = seg[c];
;               v4u o; o.x = pk2(bflo(lo.x) * e, bfhi(lo.x) * e); o.y = pk2(bflo(lo.y) * e, bfhi(lo.y) * e); o.z = pk2(bflo(hi.x) * e, bfhi(hi.x) * e); o.w = pk2(bflo(hi.y) * e, bfhi(hi.y) * e);
;               st16_wt(QD + c * 128 + 8 * gam, o); }
;             { const int dk = id >> 3, gam = id & 7, s32 = gam >> 2, g = gam & 3, c0 = 32 * s32 + 4 * g;
;               float v[8];
; #pragma unroll
;               for (int j = 0; j < 4; ++j) { v[j] = ks[(c0 + j) * 132 + dk] * sek[c0 + j]; v[4 + j] = ks[(c0 + 16 + j) * 132 + dk] * sek[c0 + 16 + j]; }
;               v4u o; o.x = pk2(v[0], v[1]); o.y = pk2(v[2], v[3]); o.z = pk2(v[4], v[5]); o.w = pk2(v[6], v[7]);
;               st16_wt(KD + dk * 64 + 8 * gam, o); }
;         }
;         { const int c = tid >> 3, gam = tid & 7, s32 = gam >> 2, g = gam & 3;
;           const v2u lo = *(const LAS v2u*)(atts + c * 64 + 32 * s32 + 4 * g), hi = *(const LAS v2u*)(atts + c * 64 + 32 * s32 + 16 + 4 * g);
;           v4u o; o.x = lo.x; o.y = lo.y; o.z = hi.x; o.w = hi.y;
;           st16_wt(ATT + c * 64 + 8 * gam, o); }
;     }
;     GL_BAR();
;     GL_REPF(5) {
;         LAS float* xcol = (LAS float*)(lds + GL_SOL);
;         LAS bf16* tinv = (LAS bf16*)(lds + GL_SOL + 17408);
;         const int j = tid >> 3, part = tid & 7, jb = j >> 4, jo = j & 15;
; #pragma unroll 1
;         for (int rb = jb; rb < 4; ++rb) {
;             float acc[16];
; #pragma unroll
;             for (int i = 0; i < 16; ++i) acc[i] = 0.f;
;             if (rb > jb) {
; #pragma unroll 2
;                 for (int s = 16 * jb + part; s < 16 * rb; s += 8) {
;                     const float sv = xcol[j * 68 + s];
;                     const LAS float* ar = AmT + s * 68 + 16 * rb;
; #pragma unroll
;                     for (int q = 0; q < 4; ++q) { const f32x4 A4 = *(const LAS f32x4*)(ar + 4 * q);
	v_pk_mul_f32 v[12:13], v[16:17], v[12:13] op_sel_hi:[0,1]
	v_pk_mul_f32 v[14:15], v[16:17], v[14:15] op_sel_hi:[0,1]
	v_pk_mul_f32 v[18:19], v[16:17], v[18:19] op_sel_hi:[0,1]
	v_pk_mul_f32 v[20:21], v[16:17], v[20:21] op_sel_hi:[0,1]
	v_cvt_pk_bf16_f32 v12, v12, v12
	v_cvt_pk_bf16_f32 v3, v15, v15
	v_cvt_pk_bf16_f32 v13, v13, v13
	v_cvt_pk_bf16_f32 v14, v14, v14
	v_cvt_pk_bf16_f32 v21, v21, v21
	v_cvt_pk_bf16_f32 v15, v18, v18
	v_cvt_pk_bf16_f32 v20, v20, v20
	v_cvt_pk_bf16_f32 v16, v19, v19
	v_lshrrev_b32_e32 v18, 16, v15
	v_lshrrev_b32_e32 v15, 16, v21
	v_lshrrev_b32_e32 v16, 16, v16
	v_lshrrev_b32_e32 v19, 16, v20
	v_and_or_b32 v15, v3, s14, v15
	v_lshl_add_u64 v[10:11], v[72:73], 1, v[10:11]
	v_ashrrev_i32_e32 v3, 3, v42
	v_and_or_b32 v14, v14, s14, v19
	v_and_or_b32 v13, v13, s14, v16
	v_and_or_b32 v12, v12, s14, v18
	global_store_dwordx4 v[10:11], v[12:15], off sc0 sc1
	s_nop 1
	v_lshl_add_u32 v10, v3, 2, 0
	v_mad_u32_u24 v11, v28, s15, v10
	v_add_u32_e32 v10, v10, v32
	ds_read_b32 v16, v10
	v_add_u32_e32 v10, 0x2200, v11
	ds_read2_b32 v[18:19], v10 offset0:68 offset1:200
	v_add_u32_e32 v10, 0x400, v11
	ds_read2_b32 v[14:15], v11 offset1:132
	ds_read2_b32 v[20:21], v10 offset0:8 offset1:140
	ds_read_b32 v26, v11 offset:10032
	ds_read_b128 v[10:13], v31
	s_add_u32 s0, s27, s0
	s_waitcnt lgkmcnt(4)
	v_mov_b32_e32 v17, v19
	s_waitcnt lgkmcnt(2)
	v_mov_b32_e32 v23, v20
	v_mov_b32_e32 v20, v15
	s_waitcnt lgkmcnt(0)
	v_mov_b32_e32 v25, v12
	v_mov_b32_e32 v12, v11
	v_mov_b32_e32 v22, v14
	v_mov_b32_e32 v24, v10
	v_pk_mul_f32 v[14:15], v[20:21], v[12:13]
	ds_read_b128 v[10:13], v31 offset:64
	v_mov_b32_e32 v19, v26
	v_pk_mul_f32 v[22:23], v[22:23], v[24:25]
	v_and_b32_e32 v6, 0xffffffc0, v43
	s_addc_u32 s1, s33, s1
	s_waitcnt lgkmcnt(0)
	v_mov_b32_e32 v21, v12
	v_mov_b32_e32 v12, v11
	v_mov_b32_e32 v20, v10
	v_pk_mul_f32 v[10:11], v[18:19], v[12:13]
	v_pk_mul_f32 v[16:17], v[16:17], v[20:21]
	v_cvt_pk_bf16_f32 v15, v15, v15
	v_cvt_pk_bf16_f32 v11, v11, v11
	v_cvt_pk_bf16_f32 v14, v14, v14
	v_cvt_pk_bf16_f32 v10, v10, v10
	v_bfe_u32 v19, v17, 16, 1
	v_cvt_pk_bf16_f32 v16, v16, v16
	v_cvt_pk_bf16_f32 v12, v22, v22
	v_add3_u32 v17, v17, v19, s59
	v_cvt_pk_bf16_f32 v13, v23, v23
	v_lshrrev_b32_e32 v18, 16, v12
	v_lshrrev_b32_e32 v12, 16, v16
	v_lshrrev_b32_e32 v19, 16, v13
	v_lshrrev_b32_e32 v13, 16, v17
	v_and_or_b32 v12, v10, s14, v12
	v_and_or_b32 v10, v14, s14, v18
	v_lshlrev_b32_e32 v14, 6, v3
	v_lshl_add_u32 v29, v6, 1, s30
	v_lshlrev_b32_e32 v30, 1, v7
	v_ashrrev_i32_e32 v7, 31, v6
	v_and_or_b32 v13, v11, s14, v13
	v_and_or_b32 v11, v15, s14, v19
	v_ashrrev_i32_e32 v15, 31, v14
	v_lshl_add_u64 v[8:9], v[14:15], 1, v[8:9]
	global_store_dwordx4 v[8:9], v[10:13], off sc0 sc1
	s_nop 1
	v_add3_u32 v3, v29, v30, v90
	v_lshl_add_u64 v[6:7], v[6:7], 1, s[0:1]
	v_lshl_add_u64 v[8:9], v[6:7], 0, v[4:5]
	ds_read2_b64 v[4:7], v3 offset1:4
	s_waitcnt lgkmcnt(0)
	global_store_dwordx4 v[8:9], v[4:7], off sc0 sc1
	s_nop 1
	s_waitcnt lgkmcnt(0)
	s_barrier
	v_ashrrev_i32_e32 v93, 7, v84
	v_cmp_gt_i32_e64 s[0:1], 4, v93
	v_cmp_eq_u32_e32 vcc, 0, v45
	s_and_saveexec_b64 s[14:15], s[0:1]
	s_cbranch_execz .LBB0_966
	v_bfe_u32 v4, v84, 3, 4
	v_cmp_eq_u32_e64 s[0:1], 0, v4
	v_lshlrev_b32_e32 v3, 4, v93
	v_or_b32_e32 v94, v3, v45
	v_cndmask_b32_e64 v96, 0, 1.0, s[0:1]
	v_cmp_eq_u32_e64 s[0:1], 1, v4
	v_add_u32_e32 v95, s96, v46
	v_lshl_add_u32 v74, v85, 1, s56
	v_cndmask_b32_e64 v97, 0, 1.0, s[0:1]
	v_cmp_eq_u32_e64 s[0:1], 2, v4
	v_or_b32_e32 v113, 8, v94
	v_lshl_add_u32 v114, v94, 2, v95
	v_cndmask_b32_e64 v98, 0, 1.0, s[0:1]
	v_cmp_eq_u32_e64 s[0:1], 3, v4
	v_mul_lo_u32 v115, v94, s58
	s_mov_b64 s[16:17], 0
	v_cndmask_b32_e64 v99, 0, 1.0, s[0:1]
	v_cmp_eq_u32_e64 s[0:1], 4, v4
	v_mov_b32_e32 v118, v93
	s_nop 0
	v_cndmask_b32_e64 v100, 0, 1.0, s[0:1]
	v_cmp_eq_u32_e64 s[0:1], 5, v4
	s_nop 1
	v_cndmask_b32_e64 v101, 0, 1.0, s[0:1]
	v_cmp_eq_u32_e64 s[0:1], 6, v4
	s_nop 1
	v_cndmask_b32_e64 v102, 0, 1.0, s[0:1]
	v_cmp_eq_u32_e64 s[0:1], 7, v4
	s_nop 1
	v_cndmask_b32_e64 v103, 0, 1.0, s[0:1]
	v_cmp_eq_u32_e64 s[0:1], 8, v4
	s_nop 1
	v_cndmask_b32_e64 v104, 0, 1.0, s[0:1]
	v_cmp_eq_u32_e64 s[0:1], 9, v4
	s_nop 1
	v_cndmask_b32_e64 v105, 0, 1.0, s[0:1]
	v_cmp_eq_u32_e64 s[0:1], 10, v4
	s_nop 1
	v_cndmask_b32_e64 v106, 0, 1.0, s[0:1]
	v_cmp_eq_u32_e64 s[0:1], 11, v4
	s_nop 1
	v_cndmask_b32_e64 v107, 0, 1.0, s[0:1]
	v_cmp_eq_u32_e64 s[0:1], 12, v4
	s_nop 1
	v_cndmask_b32_e64 v108, 0, 1.0, s[0:1]
	v_cmp_eq_u32_e64 s[0:1], 13, v4
	s_nop 1
	v_cndmask_b32_e64 v109, 0, 1.0, s[0:1]
	v_cmp_eq_u32_e64 s[0:1], 14, v4
	s_nop 1
	v_cndmask_b32_e64 v110, 0, 1.0, s[0:1]
	v_cmp_eq_u32_e64 s[0:1], 15, v4
	v_not_b32_e32 v4, v45
	v_sub_u32_e32 v112, v4, v3
	v_add_u32_e32 v3, 0, v46
	v_add_u32_e32 v116, 0x10800, v3
	v_lshl_add_u32 v3, v93, 6, 0
	v_cndmask_b32_e64 v111, 0, 1.0, s[0:1]
	v_add_u32_e32 v117, 0x20800, v3
	s_branch .LBB0_954

; #define LAS __attribute__((address_space(3)))
; __device__ __forceinline__ void gdn_local_item(const Params& P, LAS unsigned char* lds, int item, int tid, bool defer, int& pend, unsigned& pend_fb) {
;     ...
; #pragma unroll
;             for (int i = 0; i < 16; ++i) {
;                 const float sv = acc[i];
;                 const LAS float* ar = AmT + (16 * rb + i) * 68 + 16 * rb;
; #pragma unroll
;                 for (int q = (i + 1) / 4; q < 4; ++q) { const f32x4 A4 = *(const LAS f32x4*)(ar + 4 * q);
;                     if (4 * q > i) acc[4 * q] -= A4.x * sv; if (4 * q + 1 > i) acc[4 * q + 1] -= A4.y * sv; if (4 * q + 2 > i) acc[4 * q + 2] -= A4.z * sv; if (4 * q + 3 > i) acc[4 * q + 3] -= A4.w * sv; }
;             }
.LBB0_964:
	s_or_b64 exec, exec, s[18:19]
	s_and_saveexec_b64 s[0:1], vcc
	s_cbranch_execz .LBB0_953
	v_lshlrev_b32_e32 v3, 2, v20
	v_add_u32_e32 v16, s31, v3
	s_movk_i32 s18, 0x1100
	v_mad_u64_u32 v[12:13], s[18:19], v118, s18, v[16:17]
	ds_read_b128 v[22:25], v12
	ds_read_b128 v[38:41], v12 offset:16
	ds_read_b128 v[44:47], v12 offset:32
	ds_read_b128 v[12:15], v12 offset:48
	v_add_u32_e32 v3, v95, v3
	s_waitcnt lgkmcnt(3)
	v_fma_f32 v6, -v4, v24, v6
	v_fma_f32 v7, -v4, v25, v7
	v_fma_f32 v5, -v4, v23, v5
	s_waitcnt lgkmcnt(0)
	v_fma_f32 v15, -v4, v15, v77
	v_or_b32_e32 v77, 1, v20
	v_mad_u64_u32 v[80:81], s[18:19], v77, s58, v[16:17]
	ds_read_b128 v[26:29], v80
	ds_read_b128 v[52:55], v80 offset:16
	ds_read_b128 v[48:51], v80 offset:32
	ds_read_b128 v[16:19], v80 offset:48
	s_waitcnt lgkmcnt(3)
	ds_read_b128 v[24:27], v80 offset:272
	ds_read_b128 v[56:59], v80 offset:288
	v_fma_f32 v6, -v5, v28, v6
	v_fma_f32 v7, -v5, v29, v7
	ds_read_b128 v[62:65], v80 offset:560
	s_waitcnt lgkmcnt(2)
	v_fma_f32 v7, -v6, v27, v7
	ds_read_b128 v[24:27], v80 offset:592
	ds_read_b128 v[66:69], v80 offset:832
	v_fma_f32 v8, -v4, v38, v8
	v_fma_f32 v9, -v4, v39, v9
	ds_read_b128 v[32:35], v80 offset:1136
	ds_read_b128 v[120:123], v80 offset:1104
	v_fma_f32 v10, -v4, v40, v10
	v_fma_f32 v11, -v4, v41, v11
	v_fma_f32 v8, -v5, v52, v8
	v_fma_f32 v9, -v5, v53, v9
	v_fma_f32 v10, -v5, v54, v10
	v_fma_f32 v11, -v5, v55, v11
	ds_read_b128 v[20:23], v80 offset:320
	s_waitcnt lgkmcnt(6)
	v_fma_f32 v8, -v6, v56, v8
	v_fma_f32 v9, -v6, v57, v9
	v_fma_f32 v10, -v6, v58, v10
	v_fma_f32 v11, -v6, v59, v11
	ds_read_b128 v[40:43], v80 offset:1376
	ds_read_b128 v[56:59], v80 offset:304
	s_waitcnt lgkmcnt(7)
	v_fma_f32 v8, -v7, v62, v8
	v_fma_f32 v9, -v7, v63, v9
	v_fma_f32 v10, -v7, v64, v10
	v_fma_f32 v11, -v7, v65, v11
	ds_read_b128 v[62:65], v80 offset:576
	ds_read_b128 v[28:31], v80 offset:864
	s_waitcnt lgkmcnt(7)
	v_fma_f32 v9, -v8, v67, v9
	v_fma_f32 v10, -v8, v68, v10
	v_fma_f32 v11, -v8, v69, v11
	ds_read_b128 v[66:69], v80 offset:848
	v_fma_f32 v15, -v19, v5, v15
	s_waitcnt lgkmcnt(6)
	v_fma_f32 v10, -v9, v122, v10
	v_fma_f32 v11, -v9, v123, v11
	v_fma_f32 v19, -v4, v44, v60
	ds_read_b128 v[120:123], v80 offset:1120
	ds_read_b128 v[36:39], v80 offset:1408
	ds_read_b128 v[124:127], v80 offset:1392
	v_fma_f32 v19, -v5, v48, v19
	s_waitcnt lgkmcnt(7)
	v_fma_f32 v11, -v10, v43, v11
	ds_read_b128 v[40:43], v80 offset:1680
	ds_read_b128 v[128:131], v80 offset:1664
	s_waitcnt lgkmcnt(8)
	v_fma_f32 v19, -v6, v56, v19
	s_waitcnt lgkmcnt(7)
	v_fma_f32 v19, -v7, v62, v19
	s_waitcnt lgkmcnt(5)
	v_fma_f32 v19, -v8, v66, v19
	s_waitcnt lgkmcnt(4)
	v_fma_f32 v19, -v9, v120, v19
	s_waitcnt lgkmcnt(2)
	v_fma_f32 v19, -v10, v124, v19
	s_waitcnt lgkmcnt(0)
	v_fma_f32 v44, -v11, v128, v19
	v_fma_f32 v19, -v4, v45, v61
	v_fma_f32 v19, -v5, v49, v19
	v_fma_f32 v19, -v6, v57, v19
	ds_read_b128 v[52:55], v80 offset:1952
	ds_read_b128 v[132:135], v80 offset:1936
	v_fma_f32 v19, -v7, v63, v19
	v_fma_f32 v19, -v8, v67, v19
	v_fma_f32 v19, -v9, v121, v19
	v_fma_f32 v19, -v10, v125, v19
	v_fma_f32 v19, -v11, v129, v19
	s_waitcnt lgkmcnt(0)
	v_fma_f32 v45, -v44, v133, v19
	v_fma_f32 v19, -v4, v46, v82
	v_fma_f32 v19, -v5, v50, v19
	v_fma_f32 v19, -v6, v58, v19
	v_fma_f32 v19, -v7, v64, v19
	ds_read_b128 v[60:63], v80 offset:2224
	ds_read_b128 v[136:139], v80 offset:2208
	v_fma_f32 v19, -v8, v68, v19
	v_fma_f32 v19, -v9, v122, v19
	v_fma_f32 v19, -v10, v126, v19
	v_fma_f32 v19, -v11, v130, v19
	v_fma_f32 v19, -v44, v134, v19
	s_waitcnt lgkmcnt(0)
; #define LAS __attribute__((address_space(3)))
; __device__ __forceinline__ unsigned f2bf(float f) { unsigned u = __builtin_bit_cast(unsigned, f); return (u + 0x7fffu + ((u >> 16) & 1u)) >> 16; }
; __device__ __forceinline__ void gdn_local_item(const Params& P, LAS unsigned char* lds, int item, int tid, bool defer, int& pend, unsigned& pend_fb) {
;     ...
; #pragma unroll
;             for (int i = 0; i < 16; ++i) {
;                 const float sv = acc[i];
;                 const LAS float* ar = AmT + (16 * rb + i) * 68 + 16 * rb;
; #pragma unroll
;                 for (int q = (i + 1) / 4; q < 4; ++q) { const f32x4 A4 = *(const LAS f32x4*)(ar + 4 * q);
;                     if (4 * q > i) acc[4 * q] -= A4.x * sv; if (4 * q + 1 > i) acc[4 * q + 1] -= A4.y * sv; if (4 * q + 2 > i) acc[4 * q + 2] -= A4.z * sv; if (4 * q + 3 > i) acc[4 * q + 3] -= A4.w * sv; }
;             }
;             if (part == 0) {
; #pragma unroll
;                 for (int i = 0; i < 16; ++i) { xcol[j * 68 + 16 * rb + i] = acc[i]; tinv[(16 * rb + i) * 72 + j] = (bf16)f2bf(acc[i]); }
;             }
	v_fma_f32 v46, -v45, v138, v19
	v_fma_f32 v19, -v4, v47, v83
	v_fma_f32 v19, -v5, v51, v19
	v_fma_f32 v19, -v6, v59, v19
	v_fma_f32 v19, -v7, v65, v19
	v_fma_f32 v19, -v8, v69, v19
	v_fma_f32 v12, -v4, v12, v78
	v_fma_f32 v13, -v4, v13, v79
	v_fma_f32 v14, -v4, v14, v76
	ds_read_b128 v[144:147], v80 offset:2496
	ds_read_b128 v[48:51], v80 offset:2480
	v_fma_f32 v19, -v9, v123, v19
	v_fma_f32 v12, -v16, v5, v12
	v_fma_f32 v13, -v17, v5, v13
	v_fma_f32 v14, -v18, v5, v14
	v_fma_f32 v15, -v23, v6, v15
	v_fma_f32 v19, -v10, v127, v19
	v_fma_f32 v12, -v20, v6, v12
	v_fma_f32 v13, -v21, v6, v13
	v_fma_f32 v14, -v22, v6, v14
	v_fma_f32 v15, -v27, v7, v15
	v_fma_f32 v19, -v11, v131, v19
	v_fma_f32 v12, -v24, v7, v12
	v_fma_f32 v13, -v25, v7, v13
	v_fma_f32 v14, -v26, v7, v14
	v_fma_f32 v15, -v31, v8, v15
	v_fma_f32 v19, -v44, v135, v19
	v_fma_f32 v12, -v28, v8, v12
	v_fma_f32 v13, -v29, v8, v13
	v_fma_f32 v14, -v30, v8, v14
	v_fma_f32 v15, -v35, v9, v15
	v_fma_f32 v19, -v45, v139, v19
	v_fma_f32 v12, -v32, v9, v12
	v_fma_f32 v13, -v33, v9, v13
	v_fma_f32 v14, -v34, v9, v14
	v_fma_f32 v15, -v39, v10, v15
	s_waitcnt lgkmcnt(0)
	v_fma_f32 v47, -v46, v51, v19
	ds_read_b128 v[48:51], v80 offset:2768
	ds_read_b128 v[56:59], v80 offset:3040
	v_fma_f32 v12, -v36, v10, v12
	v_fma_f32 v13, -v37, v10, v13
	v_fma_f32 v14, -v38, v10, v14
	v_fma_f32 v15, -v43, v11, v15
	v_fma_f32 v12, -v40, v11, v12
	v_fma_f32 v13, -v41, v11, v13
	v_fma_f32 v14, -v42, v11, v14
	v_fma_f32 v15, -v55, v44, v15
	v_fma_f32 v12, -v52, v44, v12
	v_fma_f32 v13, -v53, v44, v13
	ds_read_b128 v[64:67], v80 offset:3312
	ds_read_b128 v[16:19], v80 offset:3584
	v_fma_f32 v14, -v54, v44, v14
	v_fma_f32 v15, -v63, v45, v15
	v_fma_f32 v12, -v60, v45, v12
	v_fma_f32 v13, -v61, v45, v13
	v_fma_f32 v14, -v62, v45, v14
	v_fma_f32 v15, -v147, v46, v15
	v_fma_f32 v12, -v144, v46, v12
	v_fma_f32 v13, -v145, v46, v13
	v_fma_f32 v14, -v146, v46, v14
	s_waitcnt lgkmcnt(3)
	v_fma_f32 v15, -v51, v47, v15
	v_fma_f32 v12, -v48, v47, v12
	v_fma_f32 v13, -v49, v47, v13
	v_fma_f32 v14, -v50, v47, v14
	s_waitcnt lgkmcnt(0)
	s_movk_i32 s18, 0x900
	v_fma_f32 v15, -v59, v12, v15
	v_fma_f32 v13, -v57, v12, v13
	v_fma_f32 v14, -v58, v12, v14
	v_cvt_pk_bf16_f32 v18, v4, v4
	v_mad_u64_u32 v[16:17], s[18:19], v118, s18, v[74:75]
	v_fma_f32 v15, -v67, v13, v15
	v_fma_f32 v14, -v66, v13, v14
	s_movk_i32 s18, 0x90
	v_fma_f32 v15, -v19, v14, v15
	ds_write_b16_d16_hi v16, v18
	v_cvt_pk_bf16_f32 v17, v5, v5
	v_mad_u64_u32 v[18:19], s[18:19], v77, s18, v[74:75]
	ds_write_b16_d16_hi v18, v17
	v_bfe_u32 v17, v6, 16, 1
	v_add3_u32 v17, v6, v17, s59
	ds_write_b16_d16_hi v18, v17 offset:144
	ds_write_b128 v3, v[4:7]
	v_cvt_pk_bf16_f32 v4, v7, v7
	ds_write_b16_d16_hi v18, v4 offset:288
	v_cvt_pk_bf16_f32 v4, v8, v8
	ds_write_b16_d16_hi v18, v4 offset:432
	v_cvt_pk_bf16_f32 v4, v9, v9
	ds_write_b16_d16_hi v18, v4 offset:576
	v_cvt_pk_bf16_f32 v4, v10, v10
	ds_write_b16_d16_hi v18, v4 offset:720
	ds_write_b128 v3, v[8:11] offset:16
	v_cvt_pk_bf16_f32 v4, v11, v11
	ds_write_b16_d16_hi v18, v4 offset:864
	v_cvt_pk_bf16_f32 v4, v44, v44
	ds_write_b16_d16_hi v18, v4 offset:1008
	v_cvt_pk_bf16_f32 v4, v45, v45
	ds_write_b16_d16_hi v18, v4 offset:1152
	v_cvt_pk_bf16_f32 v4, v46, v46
	ds_write_b16_d16_hi v18, v4 offset:1296
	ds_write_b128 v3, v[44:47] offset:32
	v_cvt_pk_bf16_f32 v4, v47, v47
	ds_write_b16_d16_hi v18, v4 offset:1440
	v_cvt_pk_bf16_f32 v4, v12, v12
	ds_write_b16_d16_hi v18, v4 offset:1584
	v_cvt_pk_bf16_f32 v4, v13, v13
	ds_write_b16_d16_hi v18, v4 offset:1728
	v_cvt_pk_bf16_f32 v4, v14, v14
	ds_write_b16_d16_hi v18, v4 offset:1872
	ds_write_b128 v3, v[12:15] offset:48
	v_cvt_pk_bf16_f32 v3, v15, v15
	ds_write_b16_d16_hi v16, v3 offset:2160
	s_branch .LBB0_953

; __device__ __forceinline__ void st16_wt(void* p, v4u v) { asm volatile("global_store_dwordx4 %0, %1, off sc0 sc1\n\ts_nop 1" :: "v"(p), "v"(v) : "memory"); }
; __device__ __forceinline__ unsigned f2bf(float f) { unsigned u = __builtin_bit_cast(unsigned, f); return (u + 0x7fffu + ((u >> 16) & 1u)) >> 16; }
; __device__ __forceinline__ unsigned pk2(float lo, float hi) { return f2bf(lo) | (f2bf(hi) << 16); }
; __device__ __forceinline__ void gdn_local_item(const Params& P, LAS unsigned char* lds, int item, int tid, bool defer, int& pend, unsigned& pend_fb) {
;     ...
;             for (int s2 = 0; s2 < 2; ++s2) {
;                 float v[8];
; #pragma unroll
;                 for (int e = 0; e < 8; ++e) { const int sidx = 32 * s2 + 8 * g + e; float x = src[sidx * 132] * sbeta[sidx]; if (isw) x *= seg[sidx]; v[e] = x; }
;                 v4u pk; pk.x = pk2(v[0], v[1]); pk.y = pk2(v[2], v[3]); pk.z = pk2(v[4], v[5]); pk.w = pk2(v[6], v[7]);
;                 bfr[s2] = __builtin_bit_cast(bf16x8, pk);
;             }
;             f32x4 acc[4];
; #pragma unroll
;             for (int rho = 0; rho < 4; ++rho) { acc[rho] = (f32x4){0.f, 0.f, 0.f, 0.f};
; #pragma unroll
;                 for (int s2 = 0; s2 < 2; ++s2) acc[rho] = __builtin_amdgcn_mfma_f32_16x16x32_bf16(af[rho][s2], bfr[s2], acc[rho], 0, 0, 0); }
;             if (!isw) {
;                 v4u o0, o1;
;                 o0.x = pk2(acc[0].x, acc[0].y); o0.y = pk2(acc[0].z, acc[0].w); o0.z = pk2(acc[1].x, acc[1].y); o0.w = pk2(acc[1].z, acc[1].w);
;                 o1.x = pk2(acc[2].x, acc[2].y); o1.y = pk2(acc[2].z, acc[2].w); o1.z = pk2(acc[3].x, acc[3].y); o1.w = pk2(acc[3].z, acc[3].w);
;                 v4u* d = (v4u*)(UF + (size_t)(2 * (wave & 3) + sig) * 1024 + lane * 16);
;                 st16_wt(d, o0); st16_wt(d + 1, o1);
;             } else {
; #pragma unroll
;                 for (int rho = 0; rho < 4; ++rho)
; #pragma unroll
;                     for (int i = 0; i < 4; ++i) wst[(16 * rho + 4 * g + i) * 136 + jj] = (bf16)f2bf(-acc[rho][i]);
;             }
.LBB0_1011:
	s_movk_i32 s0, 0x7fff
	v_cvt_pk_bf16_f32 v41, v41, v41
	v_cvt_pk_bf16_f32 v44, v44, v44
	v_cvt_pk_bf16_f32 v39, v39, v39
	v_cvt_pk_bf16_f32 v38, v38, v38
	v_cvt_pk_bf16_f32 v35, v35, v35
	v_cvt_pk_bf16_f32 v37, v37, v37
	v_cvt_pk_bf16_f32 v40, v40, v40
	v_lshrrev_b32_e32 v35, 16, v35
	v_lshrrev_b32_e32 v38, 16, v38
	s_mov_b32 s1, 0xffff0000
	v_cvt_pk_bf16_f32 v43, v43, v43
	v_lshrrev_b32_e32 v40, 16, v40
	v_and_or_b32 v99, v39, s1, v38
	v_and_or_b32 v98, v37, s1, v35
	v_lshrrev_b32_e32 v43, 16, v43
	v_and_or_b32 v100, v41, s1, v40
	v_cvt_pk_bf16_f32 v40, v45, v45
	v_cvt_pk_bf16_f32 v35, v36, v36
	v_and_or_b32 v101, v44, s1, v43
	v_cvt_pk_bf16_f32 v41, v47, v47
	v_cvt_pk_bf16_f32 v43, v49, v49
	v_cvt_pk_bf16_f32 v39, v50, v50
	v_cvt_pk_bf16_f32 v36, v42, v42
	v_cvt_pk_bf16_f32 v38, v48, v48
	v_cvt_pk_bf16_f32 v37, v46, v46
	v_lshrrev_b32_e32 v42, 16, v36
	v_lshrrev_b32_e32 v36, 16, v39
	v_lshrrev_b32_e32 v44, 16, v37
	v_lshrrev_b32_e32 v45, 16, v38
	v_and_or_b32 v105, v35, s1, v36
	v_mfma_f32_16x16x32_bf16 v[36:39], v[30:33], v[98:101], 0
	v_and_or_b32 v104, v43, s1, v45
	v_and_or_b32 v103, v41, s1, v44
	v_and_or_b32 v102, v40, s1, v42
	v_lshlrev_b32_e32 v50, 5, v34
	s_add_u32 s10, s82, s8
	v_mfma_f32_16x16x32_bf16 v[46:49], v[2:5], v[102:105], v[36:39]
	s_addc_u32 s11, s83, s9
	s_lshl_b32 s1, s28, 5
	v_mov_b32_e32 v51, 0
	v_mfma_f32_16x16x32_bf16 v[36:39], v[6:9], v[98:101], 0
	s_mov_b64 s[12:13], -1
	s_and_b64 vcc, exec, s[6:7]
	v_lshlrev_b32_e32 v96, 1, v96
	v_mfma_f32_16x16x32_bf16 v[42:45], v[10:13], v[102:105], v[36:39]
	v_mfma_f32_16x16x32_bf16 v[36:39], v[14:17], v[98:101], 0
	v_mfma_f32_16x16x32_bf16 v[98:101], v[22:25], v[98:101], 0
	v_mfma_f32_16x16x32_bf16 v[38:41], v[18:21], v[102:105], v[36:39]
	v_mfma_f32_16x16x32_bf16 v[34:37], v[26:29], v[102:105], v[98:101]
	s_cbranch_vccnz .LBB0_1013
	v_xor_b32_e32 v97, 0x80000000, v46
	s_nop 3
	v_cvt_pk_bf16_f32 v97, v97, v97
	v_mul_u32_u24_e32 v98, 0x440, v1
	v_add3_u32 v98, s54, v96, v98
	ds_write_b16_d16_hi v98, v97
	v_xor_b32_e32 v97, 0x80000000, v47
	v_cvt_pk_bf16_f32 v97, v97, v97
	ds_write_b16_d16_hi v98, v97 offset:272
	v_xor_b32_e32 v97, 0x80000000, v48
	v_cvt_pk_bf16_f32 v97, v97, v97
	ds_write_b16_d16_hi v98, v97 offset:544
	v_xor_b32_e32 v97, 0x80000000, v49
	v_cvt_pk_bf16_f32 v97, v97, v97
	ds_write_b16_d16_hi v98, v97 offset:816
	v_xor_b32_e32 v97, 0x80000000, v42
	v_cvt_pk_bf16_f32 v97, v97, v97
	ds_write_b16_d16_hi v98, v97 offset:4352
	v_xor_b32_e32 v97, 0x80000000, v43
	v_cvt_pk_bf16_f32 v97, v97, v97
	ds_write_b16_d16_hi v98, v97 offset:4624
	v_xor_b32_e32 v97, 0x80000000, v44
	v_cvt_pk_bf16_f32 v97, v97, v97
	ds_write_b16_d16_hi v98, v97 offset:4896
	v_xor_b32_e32 v97, 0x80000000, v45
	v_cvt_pk_bf16_f32 v97, v97, v97
	ds_write_b16_d16_hi v98, v97 offset:5168
	v_xor_b32_e32 v97, 0x80000000, v38
	v_cvt_pk_bf16_f32 v97, v97, v97
	ds_write_b16_d16_hi v98, v97 offset:8704
	v_xor_b32_e32 v97, 0x80000000, v39
	v_cvt_pk_bf16_f32 v97, v97, v97
	ds_write_b16_d16_hi v98, v97 offset:8976
	v_xor_b32_e32 v97, 0x80000000, v40
	v_cvt_pk_bf16_f32 v97, v97, v97
	ds_write_b16_d16_hi v98, v97 offset:9248
	v_xor_b32_e32 v97, 0x80000000, v41
	v_cvt_pk_bf16_f32 v97, v97, v97
	ds_write_b16_d16_hi v98, v97 offset:9520
	v_xor_b32_e32 v97, 0x80000000, v34
	v_cvt_pk_bf16_f32 v97, v97, v97
	ds_write_b16_d16_hi v98, v97 offset:13056
	v_xor_b32_e32 v97, 0x80000000, v35
	v_cvt_pk_bf16_f32 v97, v97, v97
	ds_write_b16_d16_hi v98, v97 offset:13328
	v_xor_b32_e32 v97, 0x80000000, v36
	v_cvt_pk_bf16_f32 v97, v97, v97
	ds_write_b16_d16_hi v98, v97 offset:13600
	v_xor_b32_e32 v97, 0x80000000, v37
	v_cvt_pk_bf16_f32 v97, v97, v97
	s_mov_b64 s[12:13], 0
	ds_write_b16_d16_hi v98, v97 offset:13872
.LBB0_1013:
	v_mul_u32_u24_e32 v97, 0x1080, v1
	s_and_b32 s0, s1, 0xfffff800
	s_andn2_b64 vcc, exec, s[12:13]
	v_lshl_add_u64 v[50:51], s[10:11], 0, v[50:51]
	s_cbranch_vccnz .LBB0_1015
	s_movk_i32 s1, 0x7fff
	v_cvt_pk_bf16_f32 v46, v46, v47
	s_mov_b32 s10, 0xffff0000
	v_cvt_pk_bf16_f32 v47, v48, v49
	v_cvt_pk_bf16_f32 v48, v42, v43
	v_cvt_pk_bf16_f32 v49, v44, v45
	v_cvt_pk_bf16_f32 v38, v38, v39
	v_cvt_pk_bf16_f32 v39, v40, v41
	v_cvt_pk_bf16_f32 v40, v34, v35
	v_cvt_pk_bf16_f32 v41, v36, v37
	s_mov_b32 s1, 0
	v_lshl_add_u64 v[34:35], s[0:1], 1, v[50:51]
	global_store_dwordx4 v[34:35], v[46:49], off sc0 sc1
	s_nop 1
	v_lshl_add_u64 v[34:35], v[34:35], 0, 16
	global_store_dwordx4 v[34:35], v[38:41], off sc0 sc1
	s_nop 1

; __device__ __forceinline__ void st16_wt(void* p, v4u v) { asm volatile("global_store_dwordx4 %0, %1, off sc0 sc1\n\ts_nop 1" :: "v"(p), "v"(v) : "memory"); }
; __device__ __forceinline__ unsigned f2bf(float f) { unsigned u = __builtin_bit_cast(unsigned, f); return (u + 0x7fffu + ((u >> 16) & 1u)) >> 16; }
; __device__ __forceinline__ unsigned pk2(float lo, float hi) { return f2bf(lo) | (f2bf(hi) << 16); }
; __device__ __forceinline__ void gdn_local_item(const Params& P, LAS unsigned char* lds, int item, int tid, bool defer, int& pend, unsigned& pend_fb) {
;     ...
;             for (int s2 = 0; s2 < 2; ++s2) {
;                 float v[8];
; #pragma unroll
;                 for (int e = 0; e < 8; ++e) { const int sidx = 32 * s2 + 8 * g + e; float x = src[sidx * 132] * sbeta[sidx]; if (isw) x *= seg[sidx]; v[e] = x; }
;                 v4u pk; pk.x = pk2(v[0], v[1]); pk.y = pk2(v[2], v[3]); pk.z = pk2(v[4], v[5]); pk.w = pk2(v[6], v[7]);
;                 bfr[s2] = __builtin_bit_cast(bf16x8, pk);
;             }
;             f32x4 acc[4];
; #pragma unroll
;             for (int rho = 0; rho < 4; ++rho) { acc[rho] = (f32x4){0.f, 0.f, 0.f, 0.f};
; #pragma unroll
;                 for (int s2 = 0; s2 < 2; ++s2) acc[rho] = __builtin_amdgcn_mfma_f32_16x16x32_bf16(af[rho][s2], bfr[s2], acc[rho], 0, 0, 0); }
;             if (!isw) {
;                 v4u o0, o1;
;                 o0.x = pk2(acc[0].x, acc[0].y); o0.y = pk2(acc[0].z, acc[0].w); o0.z = pk2(acc[1].x, acc[1].y); o0.w = pk2(acc[1].z, acc[1].w);
;                 o1.x = pk2(acc[2].x, acc[2].y); o1.y = pk2(acc[2].z, acc[2].w); o1.z = pk2(acc[3].x, acc[3].y); o1.w = pk2(acc[3].z, acc[3].w);
;                 v4u* d = (v4u*)(UF + (size_t)(2 * (wave & 3) + sig) * 1024 + lane * 16);
;                 st16_wt(d, o0); st16_wt(d + 1, o1);
;             } else {
; #pragma unroll
;                 for (int rho = 0; rho < 4; ++rho)
; #pragma unroll
;                     for (int i = 0; i < 4; ++i) wst[(16 * rho + 4 * g + i) * 136 + jj] = (bf16)f2bf(-acc[rho][i]);
;             }
.LBB0_1047:
	s_movk_i32 s1, 0x7fff
	v_cvt_pk_bf16_f32 v55, v35, v35
	v_cvt_pk_bf16_f32 v35, v37, v37
	v_cvt_pk_bf16_f32 v39, v39, v39
	v_cvt_pk_bf16_f32 v37, v42, v42
	v_cvt_pk_bf16_f32 v41, v41, v41
	v_cvt_pk_bf16_f32 v38, v38, v38
	v_cvt_pk_bf16_f32 v36, v36, v36
	v_cvt_pk_bf16_f32 v34, v34, v34
	v_lshrrev_b32_e32 v34, 16, v34
	v_lshrrev_b32_e32 v42, 16, v36
	v_lshrrev_b32_e32 v36, 16, v38
	v_lshrrev_b32_e32 v38, 16, v41
	s_mov_b32 s10, 0xffff0000
	v_and_or_b32 v37, v37, s10, v38
	v_and_or_b32 v36, v39, s10, v36
	v_and_or_b32 v35, v35, s10, v42
	v_and_or_b32 v34, v55, s10, v34
	v_cvt_pk_bf16_f32 v42, v43, v43
	v_cvt_pk_bf16_f32 v43, v45, v45
	v_cvt_pk_bf16_f32 v39, v47, v47
	v_cvt_pk_bf16_f32 v38, v49, v49
	v_mfma_f32_16x16x32_bf16 v[30:33], v[30:33], v[34:37], 0
	v_cvt_pk_bf16_f32 v48, v48, v48
	v_cvt_pk_bf16_f32 v46, v46, v46
	v_cvt_pk_bf16_f32 v44, v44, v44
	v_cvt_pk_bf16_f32 v40, v40, v40
	v_lshrrev_b32_e32 v45, 16, v40
	v_lshrrev_b32_e32 v44, 16, v44
	v_lshrrev_b32_e32 v40, 16, v46
	v_lshrrev_b32_e32 v41, 16, v48
	v_and_or_b32 v41, v38, s10, v41
	v_and_or_b32 v40, v39, s10, v40
	v_and_or_b32 v39, v43, s10, v44
	v_and_or_b32 v38, v42, s10, v45
	s_and_b64 vcc, exec, s[6:7]
	s_mov_b64 s[6:7], -1
	v_mfma_f32_16x16x32_bf16 v[30:33], v[2:5], v[38:41], v[30:33]
	v_mfma_f32_16x16x32_bf16 v[2:5], v[6:9], v[34:37], 0
	v_mfma_f32_16x16x32_bf16 v[10:13], v[10:13], v[38:41], v[2:5]
	v_mfma_f32_16x16x32_bf16 v[2:5], v[14:17], v[34:37], 0
	v_mfma_f32_16x16x32_bf16 v[6:9], v[18:21], v[38:41], v[2:5]
	v_mfma_f32_16x16x32_bf16 v[2:5], v[22:25], v[34:37], 0
	v_mfma_f32_16x16x32_bf16 v[2:5], v[26:29], v[38:41], v[2:5]
	s_cbranch_vccnz .LBB0_1049
	s_nop 0
	v_xor_b32_e32 v14, 0x80000000, v30
	v_mul_u32_u24_e32 v1, 0x440, v1
	v_cvt_pk_bf16_f32 v14, v14, v14
	v_add3_u32 v1, s54, v1, v96
	ds_write_b16_d16_hi v1, v14 offset:32
	v_xor_b32_e32 v14, 0x80000000, v31
	v_cvt_pk_bf16_f32 v14, v14, v14
	ds_write_b16_d16_hi v1, v14 offset:304
	v_xor_b32_e32 v14, 0x80000000, v32
	v_cvt_pk_bf16_f32 v14, v14, v14
	ds_write_b16_d16_hi v1, v14 offset:576
	v_xor_b32_e32 v14, 0x80000000, v33
	v_cvt_pk_bf16_f32 v14, v14, v14
	ds_write_b16_d16_hi v1, v14 offset:848
	v_xor_b32_e32 v14, 0x80000000, v10
	v_cvt_pk_bf16_f32 v14, v14, v14
	ds_write_b16_d16_hi v1, v14 offset:4384
	v_xor_b32_e32 v14, 0x80000000, v11
	v_cvt_pk_bf16_f32 v14, v14, v14
	ds_write_b16_d16_hi v1, v14 offset:4656
	v_xor_b32_e32 v14, 0x80000000, v12
	v_cvt_pk_bf16_f32 v14, v14, v14
	ds_write_b16_d16_hi v1, v14 offset:4928
	v_xor_b32_e32 v14, 0x80000000, v13
	v_cvt_pk_bf16_f32 v14, v14, v14
	ds_write_b16_d16_hi v1, v14 offset:5200
	v_xor_b32_e32 v14, 0x80000000, v6
	v_cvt_pk_bf16_f32 v14, v14, v14
	ds_write_b16_d16_hi v1, v14 offset:8736
	v_xor_b32_e32 v14, 0x80000000, v7
	v_cvt_pk_bf16_f32 v14, v14, v14
	ds_write_b16_d16_hi v1, v14 offset:9008
	v_xor_b32_e32 v14, 0x80000000, v8
	v_cvt_pk_bf16_f32 v14, v14, v14
	ds_write_b16_d16_hi v1, v14 offset:9280
	v_xor_b32_e32 v14, 0x80000000, v9
	v_cvt_pk_bf16_f32 v14, v14, v14
	ds_write_b16_d16_hi v1, v14 offset:9552
	v_xor_b32_e32 v14, 0x80000000, v2
	v_cvt_pk_bf16_f32 v14, v14, v14
	ds_write_b16_d16_hi v1, v14 offset:13088
	v_xor_b32_e32 v14, 0x80000000, v3
	v_cvt_pk_bf16_f32 v14, v14, v14
	ds_write_b16_d16_hi v1, v14 offset:13360
	v_xor_b32_e32 v14, 0x80000000, v4
	v_cvt_pk_bf16_f32 v14, v14, v14
	ds_write_b16_d16_hi v1, v14 offset:13632
	v_xor_b32_e32 v14, 0x80000000, v5
	v_cvt_pk_bf16_f32 v14, v14, v14
	s_mov_b64 s[6:7], 0
	ds_write_b16_d16_hi v1, v14 offset:13904
.LBB0_1049:
	s_andn2_b64 vcc, exec, s[6:7]
	s_cbranch_vccnz .LBB0_1051
	v_cvt_pk_bf16_f32 v14, v30, v31
	s_mov_b32 s6, 0xffff0000
	v_cvt_pk_bf16_f32 v15, v32, v33
	v_cvt_pk_bf16_f32 v16, v10, v11
	v_cvt_pk_bf16_f32 v17, v12, v13
	v_cvt_pk_bf16_f32 v6, v6, v7
	v_cvt_pk_bf16_f32 v7, v8, v9
	v_cvt_pk_bf16_f32 v8, v2, v3
	v_cvt_pk_bf16_f32 v9, v4, v5
	s_mov_b32 s1, 0
	v_lshl_add_u64 v[2:3], s[0:1], 1, v[50:51]
	s_mov_b64 s[0:1], 0x800
	v_lshl_add_u64 v[4:5], v[2:3], 0, s[0:1]
	global_store_dwordx4 v[4:5], v[14:17], off sc0 sc1
	s_nop 1
	s_mov_b64 s[0:1], 0x810
	v_lshl_add_u64 v[2:3], v[2:3], 0, s[0:1]
	global_store_dwordx4 v[2:3], v[6:9], off sc0 sc1
	s_nop 1

; #define LAS __attribute__((address_space(3)))
; __device__ __forceinline__ unsigned pk2(float lo, float hi) { return f2bf(lo) | (f2bf(hi) << 16); }
; __device__ __forceinline__ void gdn_local_item(const Params& P, LAS unsigned char* lds, int item, int tid, bool defer, int& pend, unsigned& pend_fb) {
;     ...
;             if (part <= 1) {
;                 LAS bf16* dst = (part == 0 ? qb16 : kb16) + c * 136 + grp * 16;
;                 v4u o0, o1; o0.x = pk2(y[0], y[1]); o0.y = pk2(y[2], y[3]); o0.z = pk2(y[4], y[5]); o0.w = pk2(y[6], y[7]);
;                 o1.x = pk2(y[8], y[9]); o1.y = pk2(y[10], y[11]); o1.z = pk2(y[12], y[13]); o1.w = pk2(y[14], y[15]);
;                 *(LAS v4u*)dst = o0; *(LAS v4u*)(dst + 8) = o1;
.LBB0_1091:
	s_andn2_b64 vcc, exec, s[10:11]
	s_cbranch_vccnz .LBB0_1086
	v_cvt_pk_bf16_f32 v2, v2, v3
	v_cvt_pk_bf16_f32 v3, v4, v5
	v_cvt_pk_bf16_f32 v4, v6, v7
	v_cvt_pk_bf16_f32 v5, v8, v9
	v_cvt_pk_bf16_f32 v6, v14, v15
	v_cvt_pk_bf16_f32 v7, v16, v17
	s_cmp_eq_u32 s12, 0
	v_cvt_pk_bf16_f32 v8, v10, v11
	s_cselect_b32 s0, s15, 0x10800
	s_add_i32 s0, s0, 0
	v_add3_u32 v18, s0, v46, v50
	v_cvt_pk_bf16_f32 v9, v12, v13
	ds_write_b128 v18, v[2:5]
	ds_write_b128 v18, v[6:9] offset:16
	s_branch .LBB0_1086

; __device__ __forceinline__ unsigned f2bf(float f) { unsigned u = __builtin_bit_cast(unsigned, f); return (u + 0x7fffu + ((u >> 16) & 1u)) >> 16; }
; __device__ __forceinline__ void gdn_local_item(const Params& P, LAS unsigned char* lds, int item, int tid, bool defer, int& pend, unsigned& pend_fb) {
;     ...
;             const int sidx = 16 * sig + col; const float gs = sgc[sidx];
; #pragma unroll
;             for (int i = 0; i < 4; ++i) {
;                 const int c = 16 * rho + 4 * g + i;
;                 const float dec = (c >= sidx) ? __expf(sgc[c] - gs) : 0.f;
;                 if (mat == 0) AmT[sidx * 68 + c] = (c > sidx) ? sbeta[c] * acc[i] * dec : 0.f;
;                 else atts[c * 64 + sidx] = (bf16)f2bf(acc[i] * dec);
;             }
.LBB0_1098:
	s_or_b64 exec, exec, s[0:1]
	v_mul_u32_u24_e32 v27, 0x110, v75
	v_lshl_add_u32 v30, v75, 1, s30
	s_mov_b64 s[0:1], -1
	s_and_b64 vcc, exec, s[10:11]
	s_cbranch_vccz .LBB0_1100
	v_mul_f32_e32 v24, v18, v23
	s_movk_i32 s0, 0x7fff
	v_cvt_pk_bf16_f32 v24, v24, v24
	v_lshl_add_u32 v25, v22, 7, v30
	ds_write_b16_d16_hi v25, v24
	s_mov_b64 s[0:1], 0

; __device__ __forceinline__ unsigned f2bf(float f) { unsigned u = __builtin_bit_cast(unsigned, f); return (u + 0x7fffu + ((u >> 16) & 1u)) >> 16; }
; __device__ __forceinline__ void gdn_local_item(const Params& P, LAS unsigned char* lds, int item, int tid, bool defer, int& pend, unsigned& pend_fb) {
;     ...
;             const int sidx = 16 * sig + col; const float gs = sgc[sidx];
; #pragma unroll
;             for (int i = 0; i < 4; ++i) {
;                 const int c = 16 * rho + 4 * g + i;
;                 const float dec = (c >= sidx) ? __expf(sgc[c] - gs) : 0.f;
;                 if (mat == 0) AmT[sidx * 68 + c] = (c > sidx) ? sbeta[c] * acc[i] * dec : 0.f;
;                 else atts[c * 64 + sidx] = (bf16)f2bf(acc[i] * dec);
;             }
.LBB0_1185:
	v_mul_f32_e32 v36, v19, v18
	s_movk_i32 s0, 0x7fff
	v_cvt_pk_bf16_f32 v36, v36, v36
	v_add3_u32 v37, s30, v30, v35
	ds_write_b16_d16_hi v37, v36
	s_cbranch_execnz .LBB0_1162

; __device__ __forceinline__ unsigned f2bf(float f) { unsigned u = __builtin_bit_cast(unsigned, f); return (u + 0x7fffu + ((u >> 16) & 1u)) >> 16; }
; __device__ __forceinline__ void gdn_local_item(const Params& P, LAS unsigned char* lds, int item, int tid, bool defer, int& pend, unsigned& pend_fb) {
;     ...
;             const int sidx = 16 * sig + col; const float gs = sgc[sidx];
; #pragma unroll
;             for (int i = 0; i < 4; ++i) {
;                 const int c = 16 * rho + 4 * g + i;
;                 const float dec = (c >= sidx) ? __expf(sgc[c] - gs) : 0.f;
;                 if (mat == 0) AmT[sidx * 68 + c] = (c > sidx) ? sbeta[c] * acc[i] * dec : 0.f;
;                 else atts[c * 64 + sidx] = (bf16)f2bf(acc[i] * dec);
;             }
.LBB0_1212:
	s_nop 0
	v_mul_f32_e32 v7, v2, v19
	s_movk_i32 s0, 0x7fff
	v_cvt_pk_bf16_f32 v7, v7, v7
	v_add3_u32 v10, s30, v27, v9
	ds_write_b16_d16_hi v10, v7
	v_add_u32_e32 v7, s31, v18
	s_cbranch_execnz .LBB0_1203

; __device__ __forceinline__ unsigned f2bf(float f) { unsigned u = __builtin_bit_cast(unsigned, f); return (u + 0x7fffu + ((u >> 16) & 1u)) >> 16; }
; __device__ __forceinline__ void gdn_local_item(const Params& P, LAS unsigned char* lds, int item, int tid, bool defer, int& pend, unsigned& pend_fb) {
;     ...
;             const int sidx = 16 * sig + col; const float gs = sgc[sidx];
; #pragma unroll
;             for (int i = 0; i < 4; ++i) {
;                 const int c = 16 * rho + 4 * g + i;
;                 const float dec = (c >= sidx) ? __expf(sgc[c] - gs) : 0.f;
;                 if (mat == 0) AmT[sidx * 68 + c] = (c > sidx) ? sbeta[c] * acc[i] * dec : 0.f;
;                 else atts[c * 64 + sidx] = (bf16)f2bf(acc[i] * dec);
;             }
.LBB0_1217:
	v_mul_f32_e32 v10, v3, v2
	s_movk_i32 s0, 0x7fff
	v_cvt_pk_bf16_f32 v10, v10, v10
	v_add3_u32 v11, s30, v30, v9
	ds_write_b16_d16_hi v11, v10
	s_cbranch_execnz .LBB0_1206

; __device__ __forceinline__ unsigned f2bf(float f) { unsigned u = __builtin_bit_cast(unsigned, f); return (u + 0x7fffu + ((u >> 16) & 1u)) >> 16; }
; __device__ __forceinline__ void gdn_local_item(const Params& P, LAS unsigned char* lds, int item, int tid, bool defer, int& pend, unsigned& pend_fb) {
;     ...
;             const int sidx = 16 * sig + col; const float gs = sgc[sidx];
; #pragma unroll
;             for (int i = 0; i < 4; ++i) {
;                 const int c = 16 * rho + 4 * g + i;
;                 const float dec = (c >= sidx) ? __expf(sgc[c] - gs) : 0.f;
;                 if (mat == 0) AmT[sidx * 68 + c] = (c > sidx) ? sbeta[c] * acc[i] * dec : 0.f;
;                 else atts[c * 64 + sidx] = (bf16)f2bf(acc[i] * dec);
;             }
.LBB0_1222:
	v_mul_f32_e32 v3, v4, v2
	s_movk_i32 s0, 0x7fff
	v_cvt_pk_bf16_f32 v3, v3, v3
	v_add3_u32 v10, s30, v29, v9
	ds_write_b16_d16_hi v10, v3
	s_cbranch_execnz .LBB0_1209

; __device__ __forceinline__ unsigned f2bf(float f) { unsigned u = __builtin_bit_cast(unsigned, f); return (u + 0x7fffu + ((u >> 16) & 1u)) >> 16; }
; __device__ __forceinline__ void gdn_local_item(const Params& P, LAS unsigned char* lds, int item, int tid, bool defer, int& pend, unsigned& pend_fb) {
;     ...
;             const int sidx = 16 * sig + col; const float gs = sgc[sidx];
; #pragma unroll
;             for (int i = 0; i < 4; ++i) {
;                 const int c = 16 * rho + 4 * g + i;
;                 const float dec = (c >= sidx) ? __expf(sgc[c] - gs) : 0.f;
;                 if (mat == 0) AmT[sidx * 68 + c] = (c > sidx) ? sbeta[c] * acc[i] * dec : 0.f;
;                 else atts[c * 64 + sidx] = (bf16)f2bf(acc[i] * dec);
;             }
.LBB0_1227:
	v_mul_f32_e32 v3, v5, v2
	s_movk_i32 s0, 0x7fff
	v_cvt_pk_bf16_f32 v3, v3, v3
	v_add3_u32 v4, s30, v28, v9
	ds_write_b16_d16_hi v4, v3
	s_cbranch_execnz .LBB0_1231

; #define LAS __attribute__((address_space(3)))
; __device__ __forceinline__ void st16_wt(void* p, v4u v) { asm volatile("global_store_dwordx4 %0, %1, off sc0 sc1\n\ts_nop 1" :: "v"(p), "v"(v) : "memory"); }
; __device__ __forceinline__ unsigned pk2(float lo, float hi) { return f2bf(lo) | (f2bf(hi) << 16); }
; #define GL_REPF(k) for (int rr_ = 0; rr_ < ((GL_REP_STEP == (k)) ? 2 : 1); ++rr_)
; __device__ __forceinline__ void gdn_local_item(const Params& P, LAS unsigned char* lds, int item, int tid, bool defer, int& pend, unsigned& pend_fb) {
;     ...
;     GL_REPF(4) {
;         bf16* QD = (bf16*)(ws + WS_QD) + (size_t)item * 8192;
;         bf16* KD = (bf16*)(ws + WS_KD) + (size_t)item * 8192;
;         bf16* ATT = (bf16*)(ws + WS_ATT) + (size_t)item * 4096;
; #pragma unroll
;         for (int r = 0; r < 2; ++r) {
;             const int id = tid + 512 * r;
;             { const int c = id >> 4, gam = id & 15, s32 = gam >> 2, g = gam & 3;
;               const v2u lo = *(const LAS v2u*)(qb16 + c * 136 + 32 * s32 + 4 * g), hi = *(const LAS v2u*)(qb16 + c * 136 + 32 * s32 + 16 + 4 * g);
;               const float e = seg[c];
;               v4u o; o.x = pk2(bflo(lo.x) * e, bfhi(lo.x) * e); o.y = pk2(bflo(lo.y) * e, bfhi(lo.y) * e); o.z = pk2(bflo(hi.x) * e, bfhi(hi.x) * e); o.w = pk2(bflo(hi.y) * e, bfhi(hi.y) * e);
;               st16_wt(QD + c * 128 + 8 * gam, o); }
;             { const int dk = id >> 3, gam = id & 7, s32 = gam >> 2, g = gam & 3, c0 = 32 * s32 + 4 * g;
;               float v[8];
; #pragma unroll
;               for (int j = 0; j < 4; ++j) { v[j] = ks[(c0 + j) * 132 + dk] * sek[c0 + j]; v[4 + j] = ks[(c0 + 16 + j) * 132 + dk] * sek[c0 + 16 + j]; }
;               v4u o; o.x = pk2(v[0], v[1]); o.y = pk2(v[2], v[3]); o.z = pk2(v[4], v[5]); o.w = pk2(v[6], v[7]);
;               st16_wt(KD + dk * 64 + 8 * gam, o); }
;         }
.LBB0_1231:
	v_lshlrev_b32_e32 v87, 3, v75
	v_and_b32_e32 v88, 0x60, v87
	v_and_b32_e32 v6, 12, v44
	v_ashrrev_i32_e32 v15, 4, v84
	s_movk_i32 s42, 0x110
	v_lshl_add_u32 v3, v88, 1, s56
	v_and_b32_e32 v7, 32, v43
	v_mul_lo_u32 v90, v15, s42
	v_lshlrev_b32_e32 v89, 1, v6
	s_waitcnt lgkmcnt(0)
	s_barrier
	v_or_b32_e32 v28, v7, v6
	v_add3_u32 v6, v3, v90, v89
	ds_read2_b64 v[10:13], v6 offset1:4
	v_lshl_add_u32 v6, v15, 2, s85
	ds_read_b32 v14, v6
	s_mov_b32 s63, 0
	s_lshl_b64 s[0:1], s[62:63], 13
	s_waitcnt lgkmcnt(1)
	v_lshlrev_b32_e32 v21, 16, v13
	v_lshlrev_b32_e32 v20, 16, v12
	v_and_b32_e32 v13, 0xffff0000, v13
	v_and_b32_e32 v12, 0xffff0000, v12
	v_lshlrev_b32_e32 v17, 16, v11
	v_lshlrev_b32_e32 v16, 16, v10
	v_and_b32_e32 v11, 0xffff0000, v11
	v_and_b32_e32 v10, 0xffff0000, v10
	s_waitcnt lgkmcnt(0)
	v_pk_mul_f32 v[12:13], v[14:15], v[12:13] op_sel_hi:[0,1]
	s_lshl_b64 s[8:9], s[62:63], 14
	v_pk_mul_f32 v[16:17], v[14:15], v[16:17] op_sel_hi:[0,1]
	v_pk_mul_f32 v[10:11], v[14:15], v[10:11] op_sel_hi:[0,1]
	s_movk_i32 s43, 0x7fff
	s_add_u32 s14, s53, s8
	v_mov_b32_e32 v2, 0
	v_pk_mul_f32 v[20:21], v[14:15], v[20:21] op_sel_hi:[0,1]
	v_cvt_pk_bf16_f32 v12, v12, v12
	s_addc_u32 s15, s97, s9
	v_lshlrev_b32_e32 v4, 4, v75
	v_mov_b32_e32 v5, v2
	v_cvt_pk_bf16_f32 v10, v10, v10
	v_cvt_pk_bf16_f32 v11, v11, v11
	v_cvt_pk_bf16_f32 v13, v13, v13
	v_cvt_pk_bf16_f32 v17, v17, v17
	v_lshl_add_u64 v[18:19], s[14:15], 0, v[4:5]
	s_mov_b32 s14, 0xffff0000
	v_cvt_pk_bf16_f32 v21, v21, v21
	v_cvt_pk_bf16_f32 v20, v20, v20
	v_cvt_pk_bf16_f32 v14, v16, v16
	v_lshrrev_b32_e32 v16, 16, v17
	v_lshlrev_b32_e32 v70, 7, v15
	v_lshrrev_b32_e32 v14, 16, v14
	v_lshrrev_b32_e32 v17, 16, v20
	v_lshrrev_b32_e32 v20, 16, v21
	v_and_or_b32 v11, v11, s14, v16
	v_ashrrev_i32_e32 v71, 31, v70
	v_and_or_b32 v13, v13, s14, v20
	v_and_or_b32 v12, v12, s14, v17
	v_and_or_b32 v10, v10, s14, v14
	v_lshl_add_u64 v[14:15], v[70:71], 1, v[18:19]
	global_store_dwordx4 v[14:15], v[10:13], off sc0 sc1
	s_nop 1
	v_lshl_add_u32 v11, v28, 2, 0
	v_lshl_add_u32 v10, v85, 2, 0
	s_movk_i32 s15, 0x210
	v_add_u32_e32 v29, 0x27500, v11
	v_mov_b32_e32 v11, 0x2100
	v_mad_u32_u24 v14, v28, s15, v10
	v_mad_u32_u24 v30, v28, s15, v11
	v_add_u32_e32 v31, v10, v30
	v_add_u32_e32 v10, 0x400, v14
	ds_read2_b32 v[20:21], v14 offset1:132
	ds_read2_b32 v[22:23], v10 offset0:8 offset1:140
	ds_read_b32 v32, v14 offset:10032
	ds_read_b128 v[10:13], v29
	v_add_u32_e32 v14, 0x2200, v14
	ds_read2_b32 v[24:25], v14 offset0:68 offset1:200
	s_waitcnt lgkmcnt(3)
	v_mov_b32_e32 v15, v22
	v_mov_b32_e32 v14, v20
	s_waitcnt lgkmcnt(1)
	v_mov_b32_e32 v16, v10
	v_mov_b32_e32 v17, v12
	v_pk_mul_f32 v[26:27], v[14:15], v[16:17]
	ds_read_b32 v10, v31
	ds_read_b128 v[14:17], v29 offset:64
	v_mov_b32_e32 v22, v21
	v_mov_b32_e32 v12, v11
	s_waitcnt lgkmcnt(2)
	v_mov_b32_e32 v11, v25
	v_mov_b32_e32 v25, v32
	s_waitcnt lgkmcnt(0)
	v_mov_b32_e32 v21, v16
	v_mov_b32_e32 v16, v15
	v_pk_mul_f32 v[12:13], v[22:23], v[12:13]
	v_mov_b32_e32 v20, v14
	v_pk_mul_f32 v[14:15], v[24:25], v[16:17]
	v_pk_mul_f32 v[10:11], v[10:11], v[20:21]
	v_cvt_pk_bf16_f32 v21, v12, v12
	v_cvt_pk_bf16_f32 v20, v13, v13
	v_cvt_pk_bf16_f32 v12, v14, v14
	v_cvt_pk_bf16_f32 v13, v15, v15
	v_cvt_pk_bf16_f32 v10, v10, v10
	v_cvt_pk_bf16_f32 v14, v26, v26
	s_add_u32 s16, s86, s8
	v_and_b32_e32 v4, 56, v43
	v_cvt_pk_bf16_f32 v11, v11, v11
	v_cvt_pk_bf16_f32 v15, v27, v27
	v_lshrrev_b32_e32 v14, 16, v14
	v_lshrrev_b32_e32 v10, 16, v10
	s_addc_u32 s17, s52, s9
	v_lshlrev_b32_e32 v4, 1, v4
	v_lshrrev_b32_e32 v15, 16, v15
	v_lshrrev_b32_e32 v11, 16, v11
	v_and_or_b32 v12, v12, s14, v10
	v_and_or_b32 v10, v21, s14, v14
	v_lshlrev_b32_e32 v14, 6, v85
	v_lshl_add_u64 v[8:9], s[16:17], 0, v[4:5]
	v_and_or_b32 v13, v13, s14, v11
	v_and_or_b32 v11, v20, s14, v15
	v_ashrrev_i32_e32 v15, 31, v14
	v_lshl_add_u64 v[14:15], v[14:15], 1, v[8:9]
	global_store_dwordx4 v[14:15], v[10:13], off sc0 sc1
	s_nop 1
	v_ashrrev_i32_e32 v15, 4, v42
	v_mul_lo_u32 v91, v15, s42
	v_add3_u32 v3, v3, v91, v89
	ds_read2_b64 v[10:13], v3 offset1:4
	v_lshl_add_u32 v3, v15, 2, s85
	ds_read_b32 v14, v3
	v_lshlrev_b32_e32 v72, 7, v15
	v_ashrrev_i32_e32 v73, 31, v72
	s_waitcnt lgkmcnt(1)
	v_lshlrev_b32_e32 v21, 16, v13
	v_lshlrev_b32_e32 v20, 16, v12
	v_and_b32_e32 v13, 0xffff0000, v13
	v_and_b32_e32 v12, 0xffff0000, v12
	v_lshlrev_b32_e32 v17, 16, v11
	v_lshlrev_b32_e32 v16, 16, v10
	v_and_b32_e32 v11, 0xffff0000, v11
	v_and_b32_e32 v10, 0xffff0000, v10
	s_waitcnt lgkmcnt(0)
; #define LAS __attribute__((address_space(3)))
; #define GL_REPF(k) for (int rr_ = 0; rr_ < ((GL_REP_STEP == (k)) ? 2 : 1); ++rr_)
; __device__ __forceinline__ void gdn_local_item(const Params& P, LAS unsigned char* lds, int item, int tid, bool defer, int& pend, unsigned& pend_fb) {
;     ...
;             { const int c = id >> 4, gam = id & 15, s32 = gam >> 2, g = gam & 3;
;               const v2u lo = *(const LAS v2u*)(qb16 + c * 136 + 32 * s32 + 4 * g), hi = *(const LAS v2u*)(qb16 + c * 136 + 32 * s32 + 16 + 4 * g);
;               const float e = seg[c];
;               v4u o; o.x = pk2(bflo(lo.x) * e, bfhi(lo.x) * e); o.y = pk2(bflo(lo.y) * e, bfhi(lo.y) * e); o.z = pk2(bflo(hi.x) * e, bfhi(hi.x) * e); o.w = pk2(bflo(hi.y) * e, bfhi(hi.y) * e);
;               st16_wt(QD + c * 128 + 8 * gam, o); }
;             { const int dk = id >> 3, gam = id & 7, s32 = gam >> 2, g = gam & 3, c0 = 32 * s32 + 4 * g;
;               float v[8];
; #pragma unroll
;               for (int j = 0; j < 4; ++j) { v[j] = ks[(c0 + j) * 132 + dk] * sek[c0 + j]; v[4 + j] = ks[(c0 + 16 + j) * 132 + dk] * sek[c0 + 16 + j]; }
;               v4u o; o.x = pk2(v[0], v[1]); o.y = pk2(v[2], v[3]); o.z = pk2(v[4], v[5]); o.w = pk2(v[6], v[7]);
;               st16_wt(KD + dk * 64 + 8 * gam, o); }
;         }
;         { const int c = tid >> 3, gam = tid & 7, s32 = gam >> 2, g = gam & 3;
;           const v2u lo = *(const LAS v2u*)(atts + c * 64 + 32 * s32 + 4 * g), hi = *(const LAS v2u*)(atts + c * 64 + 32 * s32 + 16 + 4 * g);
;           v4u o; o.x = lo.x; o.y = lo.y; o.z = hi.x; o.w = hi.y;
;           st16_wt(ATT + c * 64 + 8 * gam, o); }
;     }
;     GL_BAR();
;     GL_REPF(5) {
;         LAS float* xcol = (LAS float*)(lds + GL_SOL);
;         LAS bf16* tinv = (LAS bf16*)(lds + GL_SOL + 17408);
;         const int j = tid >> 3, part = tid & 7, jb = j >> 4, jo = j & 15;
; #pragma unroll 1
;         for (int rb = jb; rb < 4; ++rb) {
;             float acc[16];
; #pragma unroll
;             for (int i = 0; i < 16; ++i) acc[i] = 0.f;
;             if (rb > jb) {
; #pragma unroll 2
;                 for (int s = 16 * jb + part; s < 16 * rb; s += 8) {
;                     const float sv = xcol[j * 68 + s];
;                     const LAS float* ar = AmT + s * 68 + 16 * rb;
; #pragma unroll
;                     for (int q = 0; q < 4; ++q) { const f32x4 A4 = *(const LAS f32x4*)(ar + 4 * q);
	v_pk_mul_f32 v[12:13], v[14:15], v[12:13] op_sel_hi:[0,1]
	v_pk_mul_f32 v[16:17], v[14:15], v[16:17] op_sel_hi:[0,1]
	v_pk_mul_f32 v[10:11], v[14:15], v[10:11] op_sel_hi:[0,1]
	v_pk_mul_f32 v[20:21], v[14:15], v[20:21] op_sel_hi:[0,1]
	v_cvt_pk_bf16_f32 v13, v13, v13
	v_cvt_pk_bf16_f32 v10, v10, v10
	v_cvt_pk_bf16_f32 v11, v11, v11
	v_cvt_pk_bf16_f32 v12, v12, v12
	v_cvt_pk_bf16_f32 v14, v16, v16
	v_cvt_pk_bf16_f32 v21, v21, v21
	v_cvt_pk_bf16_f32 v20, v20, v20
	v_cvt_pk_bf16_f32 v17, v17, v17
	v_lshrrev_b32_e32 v14, 16, v14
	v_lshrrev_b32_e32 v16, 16, v17
	v_lshrrev_b32_e32 v17, 16, v20
	v_lshrrev_b32_e32 v20, 16, v21
	v_and_or_b32 v10, v10, s14, v14
	v_ashrrev_i32_e32 v31, 3, v42
	v_and_or_b32 v13, v13, s14, v20
	v_and_or_b32 v12, v12, s14, v17
	v_and_or_b32 v11, v11, s14, v16
	v_lshl_add_u64 v[14:15], v[72:73], 1, v[18:19]
	global_store_dwordx4 v[14:15], v[10:13], off sc0 sc1
	s_nop 1
	v_lshl_add_u32 v10, v31, 2, 0
	v_mad_u32_u24 v14, v28, s15, v10
	v_add_u32_e32 v15, v10, v30
	v_add_u32_e32 v10, 0x2200, v14
	ds_read2_b32 v[18:19], v14 offset1:132
	ds_read2_b32 v[20:21], v10 offset0:68 offset1:200
	v_add_u32_e32 v10, 0x400, v14
	ds_read2_b32 v[22:23], v10 offset0:8 offset1:140
	ds_read_b128 v[10:13], v29
	ds_read_b32 v24, v15
	ds_read_b32 v30, v14 offset:10032
	ds_read_b128 v[14:17], v29 offset:64
	s_waitcnt lgkmcnt(4)
	v_mov_b32_e32 v27, v22
	s_waitcnt lgkmcnt(3)
	v_mov_b32_e32 v29, v12
	v_mov_b32_e32 v22, v19
	v_mov_b32_e32 v12, v11
	v_mov_b32_e32 v28, v10
	v_pk_mul_f32 v[10:11], v[22:23], v[12:13]
	v_mov_b32_e32 v25, v21
	s_waitcnt lgkmcnt(0)
	v_mov_b32_e32 v12, v14
	v_mov_b32_e32 v13, v16
	v_mov_b32_e32 v26, v18
	v_pk_mul_f32 v[12:13], v[24:25], v[12:13]
	v_mov_b32_e32 v21, v30
	v_mov_b32_e32 v16, v15
	v_pk_mul_f32 v[14:15], v[20:21], v[16:17]
	v_cvt_pk_bf16_f32 v11, v11, v11
	v_pk_mul_f32 v[26:27], v[26:27], v[28:29]
	v_cvt_pk_bf16_f32 v10, v10, v10
	v_cvt_pk_bf16_f32 v12, v12, v12
	v_and_b32_e32 v6, 0xffffffc0, v43
	v_cvt_pk_bf16_f32 v14, v14, v14
	v_cvt_pk_bf16_f32 v15, v15, v15
	v_cvt_pk_bf16_f32 v13, v13, v13
	v_lshrrev_b32_e32 v12, 16, v12
	s_add_u32 s0, s27, s0
	v_lshl_add_u32 v3, v6, 1, s30
	v_lshlrev_b32_e32 v7, 1, v7
	v_cvt_pk_bf16_f32 v17, v27, v27
	v_cvt_pk_bf16_f32 v16, v26, v26
	v_lshrrev_b32_e32 v13, 16, v13
	v_and_or_b32 v12, v14, s14, v12
	v_lshlrev_b32_e32 v14, 6, v31
	v_lshrrev_b32_e32 v16, 16, v16
	v_lshrrev_b32_e32 v17, 16, v17
	v_and_or_b32 v13, v15, s14, v13
	v_ashrrev_i32_e32 v15, 31, v14
	v_add3_u32 v3, v3, v7, v89
	s_addc_u32 s1, s33, s1
	v_ashrrev_i32_e32 v7, 31, v6
	v_and_or_b32 v11, v11, s14, v17
	v_and_or_b32 v10, v10, s14, v16
	v_lshl_add_u64 v[8:9], v[14:15], 1, v[8:9]
	global_store_dwordx4 v[8:9], v[10:13], off sc0 sc1
	s_nop 1
	v_lshl_add_u64 v[6:7], v[6:7], 1, s[0:1]
	ds_read2_b64 v[8:11], v3 offset1:4
	v_lshl_add_u64 v[4:5], v[6:7], 0, v[4:5]
	s_waitcnt lgkmcnt(0)
	global_store_dwordx4 v[4:5], v[8:11], off sc0 sc1
	s_nop 1
	s_waitcnt lgkmcnt(0)
	s_barrier
	v_ashrrev_i32_e32 v92, 7, v84
	v_cmp_gt_i32_e64 s[0:1], 4, v92
	v_cmp_eq_u32_e32 vcc, 0, v45
	s_and_saveexec_b64 s[14:15], s[0:1]
	s_cbranch_execz .LBB0_1246
	v_bfe_u32 v4, v84, 3, 4
	v_cmp_eq_u32_e64 s[0:1], 0, v4
	v_lshlrev_b32_e32 v3, 4, v92
	v_or_b32_e32 v93, v3, v45
	v_cndmask_b32_e64 v95, 0, 1.0, s[0:1]
	v_cmp_eq_u32_e64 s[0:1], 1, v4
	v_add_u32_e32 v94, s96, v46
	v_lshl_add_u32 v74, v85, 1, s56
	v_cndmask_b32_e64 v96, 0, 1.0, s[0:1]
	v_cmp_eq_u32_e64 s[0:1], 2, v4
	v_or_b32_e32 v112, 8, v93
	v_lshl_add_u32 v113, v93, 2, v94
	v_cndmask_b32_e64 v97, 0, 1.0, s[0:1]
	v_cmp_eq_u32_e64 s[0:1], 3, v4
	v_mul_lo_u32 v114, v93, s42
	s_mov_b64 s[16:17], 0
	v_cndmask_b32_e64 v98, 0, 1.0, s[0:1]
	v_cmp_eq_u32_e64 s[0:1], 4, v4
	v_mov_b32_e32 v117, v92
	s_nop 0
	v_cndmask_b32_e64 v99, 0, 1.0, s[0:1]
	v_cmp_eq_u32_e64 s[0:1], 5, v4
	s_nop 1
	v_cndmask_b32_e64 v100, 0, 1.0, s[0:1]
	v_cmp_eq_u32_e64 s[0:1], 6, v4
	s_nop 1
	v_cndmask_b32_e64 v101, 0, 1.0, s[0:1]
	v_cmp_eq_u32_e64 s[0:1], 7, v4
	s_nop 1
	v_cndmask_b32_e64 v102, 0, 1.0, s[0:1]
	v_cmp_eq_u32_e64 s[0:1], 8, v4
	s_nop 1
	v_cndmask_b32_e64 v103, 0, 1.0, s[0:1]
	v_cmp_eq_u32_e64 s[0:1], 9, v4
	s_nop 1
	v_cndmask_b32_e64 v104, 0, 1.0, s[0:1]
	v_cmp_eq_u32_e64 s[0:1], 10, v4
	s_nop 1
	v_cndmask_b32_e64 v105, 0, 1.0, s[0:1]
	v_cmp_eq_u32_e64 s[0:1], 11, v4
	s_nop 1
	v_cndmask_b32_e64 v106, 0, 1.0, s[0:1]
	v_cmp_eq_u32_e64 s[0:1], 12, v4
	s_nop 1
	v_cndmask_b32_e64 v107, 0, 1.0, s[0:1]
	v_cmp_eq_u32_e64 s[0:1], 13, v4
	s_nop 1
	v_cndmask_b32_e64 v108, 0, 1.0, s[0:1]
	v_cmp_eq_u32_e64 s[0:1], 14, v4
	s_nop 1
	v_cndmask_b32_e64 v109, 0, 1.0, s[0:1]
	v_cmp_eq_u32_e64 s[0:1], 15, v4
	v_not_b32_e32 v4, v45
	v_sub_u32_e32 v111, v4, v3
	v_add_u32_e32 v3, 0, v46
	v_add_u32_e32 v115, 0x10800, v3
	v_lshl_add_u32 v3, v92, 6, 0
	v_cndmask_b32_e64 v110, 0, 1.0, s[0:1]
	v_add_u32_e32 v116, 0x20800, v3
	s_branch .LBB0_1234

; #define LAS __attribute__((address_space(3)))
; __device__ __forceinline__ void gdn_local_item(const Params& P, LAS unsigned char* lds, int item, int tid, bool defer, int& pend, unsigned& pend_fb) {
;     ...
; #pragma unroll
;             for (int i = 0; i < 16; ++i) {
;                 const float sv = acc[i];
;                 const LAS float* ar = AmT + (16 * rb + i) * 68 + 16 * rb;
; #pragma unroll
;                 for (int q = (i + 1) / 4; q < 4; ++q) { const f32x4 A4 = *(const LAS f32x4*)(ar + 4 * q);
;                     if (4 * q > i) acc[4 * q] -= A4.x * sv; if (4 * q + 1 > i) acc[4 * q + 1] -= A4.y * sv; if (4 * q + 2 > i) acc[4 * q + 2] -= A4.z * sv; if (4 * q + 3 > i) acc[4 * q + 3] -= A4.w * sv; }
;             }
.LBB0_1244:
	s_or_b64 exec, exec, s[18:19]
	s_and_saveexec_b64 s[0:1], vcc
	s_cbranch_execz .LBB0_1233
	v_lshlrev_b32_e32 v3, 2, v20
	v_add_u32_e32 v16, s31, v3
	s_movk_i32 s18, 0x1100
	v_mad_u64_u32 v[12:13], s[18:19], v117, s18, v[16:17]
	ds_read_b128 v[22:25], v12
	ds_read_b128 v[38:41], v12 offset:16
	ds_read_b128 v[44:47], v12 offset:32
	ds_read_b128 v[12:15], v12 offset:48
	v_add_u32_e32 v3, v94, v3
	s_waitcnt lgkmcnt(3)
	v_fma_f32 v6, -v4, v24, v6
	v_fma_f32 v7, -v4, v25, v7
	v_fma_f32 v5, -v4, v23, v5
	s_waitcnt lgkmcnt(0)
	v_fma_f32 v15, -v4, v15, v77
	v_or_b32_e32 v77, 1, v20
	v_mad_u64_u32 v[80:81], s[18:19], v77, s42, v[16:17]
	ds_read_b128 v[26:29], v80
	ds_read_b128 v[52:55], v80 offset:16
	ds_read_b128 v[48:51], v80 offset:32
	ds_read_b128 v[16:19], v80 offset:48
	s_waitcnt lgkmcnt(3)
	ds_read_b128 v[24:27], v80 offset:272
	ds_read_b128 v[56:59], v80 offset:288
	v_fma_f32 v6, -v5, v28, v6
	v_fma_f32 v7, -v5, v29, v7
	ds_read_b128 v[62:65], v80 offset:560
	s_waitcnt lgkmcnt(2)
	v_fma_f32 v7, -v6, v27, v7
	ds_read_b128 v[24:27], v80 offset:592
	ds_read_b128 v[66:69], v80 offset:832
	v_fma_f32 v8, -v4, v38, v8
	v_fma_f32 v9, -v4, v39, v9
	ds_read_b128 v[32:35], v80 offset:1136
	ds_read_b128 v[118:121], v80 offset:1104
	v_fma_f32 v10, -v4, v40, v10
	v_fma_f32 v11, -v4, v41, v11
	v_fma_f32 v8, -v5, v52, v8
	v_fma_f32 v9, -v5, v53, v9
	v_fma_f32 v10, -v5, v54, v10
	v_fma_f32 v11, -v5, v55, v11
	ds_read_b128 v[20:23], v80 offset:320
	s_waitcnt lgkmcnt(6)
	v_fma_f32 v8, -v6, v56, v8
	v_fma_f32 v9, -v6, v57, v9
	v_fma_f32 v10, -v6, v58, v10
	v_fma_f32 v11, -v6, v59, v11
	ds_read_b128 v[40:43], v80 offset:1376
	ds_read_b128 v[56:59], v80 offset:304
	s_waitcnt lgkmcnt(7)
	v_fma_f32 v8, -v7, v62, v8
	v_fma_f32 v9, -v7, v63, v9
	v_fma_f32 v10, -v7, v64, v10
	v_fma_f32 v11, -v7, v65, v11
	ds_read_b128 v[62:65], v80 offset:576
	ds_read_b128 v[28:31], v80 offset:864
	s_waitcnt lgkmcnt(7)
	v_fma_f32 v9, -v8, v67, v9
	v_fma_f32 v10, -v8, v68, v10
	v_fma_f32 v11, -v8, v69, v11
	ds_read_b128 v[66:69], v80 offset:848
	v_fma_f32 v15, -v19, v5, v15
	s_waitcnt lgkmcnt(6)
	v_fma_f32 v10, -v9, v120, v10
	v_fma_f32 v11, -v9, v121, v11
	v_fma_f32 v19, -v4, v44, v60
	ds_read_b128 v[118:121], v80 offset:1120
	ds_read_b128 v[36:39], v80 offset:1408
	ds_read_b128 v[122:125], v80 offset:1392
	v_fma_f32 v19, -v5, v48, v19
	s_waitcnt lgkmcnt(7)
	v_fma_f32 v11, -v10, v43, v11
	ds_read_b128 v[40:43], v80 offset:1680
	ds_read_b128 v[126:129], v80 offset:1664
	s_waitcnt lgkmcnt(8)
	v_fma_f32 v19, -v6, v56, v19
	s_waitcnt lgkmcnt(7)
	v_fma_f32 v19, -v7, v62, v19
	s_waitcnt lgkmcnt(5)
	v_fma_f32 v19, -v8, v66, v19
	s_waitcnt lgkmcnt(4)
	v_fma_f32 v19, -v9, v118, v19
	s_waitcnt lgkmcnt(2)
	v_fma_f32 v19, -v10, v122, v19
	s_waitcnt lgkmcnt(0)
	v_fma_f32 v44, -v11, v126, v19
	v_fma_f32 v19, -v4, v45, v61
	v_fma_f32 v19, -v5, v49, v19
	v_fma_f32 v19, -v6, v57, v19
	ds_read_b128 v[52:55], v80 offset:1952
	ds_read_b128 v[130:133], v80 offset:1936
	v_fma_f32 v19, -v7, v63, v19
	v_fma_f32 v19, -v8, v67, v19
	v_fma_f32 v19, -v9, v119, v19
	v_fma_f32 v19, -v10, v123, v19
	v_fma_f32 v19, -v11, v127, v19
	s_waitcnt lgkmcnt(0)
	v_fma_f32 v45, -v44, v131, v19
	v_fma_f32 v19, -v4, v46, v82
	v_fma_f32 v19, -v5, v50, v19
	v_fma_f32 v19, -v6, v58, v19
	v_fma_f32 v19, -v7, v64, v19
	ds_read_b128 v[60:63], v80 offset:2224
	ds_read_b128 v[134:137], v80 offset:2208
	v_fma_f32 v19, -v8, v68, v19
	v_fma_f32 v19, -v9, v120, v19
	v_fma_f32 v19, -v10, v124, v19
	v_fma_f32 v19, -v11, v128, v19
	v_fma_f32 v19, -v44, v132, v19
	s_waitcnt lgkmcnt(0)
; #define LAS __attribute__((address_space(3)))
; __device__ __forceinline__ unsigned f2bf(float f) { unsigned u = __builtin_bit_cast(unsigned, f); return (u + 0x7fffu + ((u >> 16) & 1u)) >> 16; }
; __device__ __forceinline__ void gdn_local_item(const Params& P, LAS unsigned char* lds, int item, int tid, bool defer, int& pend, unsigned& pend_fb) {
;     ...
; #pragma unroll
;             for (int i = 0; i < 16; ++i) {
;                 const float sv = acc[i];
;                 const LAS float* ar = AmT + (16 * rb + i) * 68 + 16 * rb;
; #pragma unroll
;                 for (int q = (i + 1) / 4; q < 4; ++q) { const f32x4 A4 = *(const LAS f32x4*)(ar + 4 * q);
;                     if (4 * q > i) acc[4 * q] -= A4.x * sv; if (4 * q + 1 > i) acc[4 * q + 1] -= A4.y * sv; if (4 * q + 2 > i) acc[4 * q + 2] -= A4.z * sv; if (4 * q + 3 > i) acc[4 * q + 3] -= A4.w * sv; }
;             }
;             if (part == 0) {
; #pragma unroll
;                 for (int i = 0; i < 16; ++i) { xcol[j * 68 + 16 * rb + i] = acc[i]; tinv[(16 * rb + i) * 72 + j] = (bf16)f2bf(acc[i]); }
;             }
	v_fma_f32 v46, -v45, v136, v19
	v_fma_f32 v19, -v4, v47, v83
	v_fma_f32 v19, -v5, v51, v19
	v_fma_f32 v19, -v6, v59, v19
	v_fma_f32 v19, -v7, v65, v19
	v_fma_f32 v19, -v8, v69, v19
	v_fma_f32 v12, -v4, v12, v78
	v_fma_f32 v13, -v4, v13, v79
	v_fma_f32 v14, -v4, v14, v76
	ds_read_b128 v[144:147], v80 offset:2496
	ds_read_b128 v[48:51], v80 offset:2480
	v_fma_f32 v19, -v9, v121, v19
	v_fma_f32 v12, -v16, v5, v12
	v_fma_f32 v13, -v17, v5, v13
	v_fma_f32 v14, -v18, v5, v14
	v_fma_f32 v15, -v23, v6, v15
	v_fma_f32 v19, -v10, v125, v19
	v_fma_f32 v12, -v20, v6, v12
	v_fma_f32 v13, -v21, v6, v13
	v_fma_f32 v14, -v22, v6, v14
	v_fma_f32 v15, -v27, v7, v15
	v_fma_f32 v19, -v11, v129, v19
	v_fma_f32 v12, -v24, v7, v12
	v_fma_f32 v13, -v25, v7, v13
	v_fma_f32 v14, -v26, v7, v14
	v_fma_f32 v15, -v31, v8, v15
	v_fma_f32 v19, -v44, v133, v19
	v_fma_f32 v12, -v28, v8, v12
	v_fma_f32 v13, -v29, v8, v13
	v_fma_f32 v14, -v30, v8, v14
	v_fma_f32 v15, -v35, v9, v15
	v_fma_f32 v19, -v45, v137, v19
	v_fma_f32 v12, -v32, v9, v12
	v_fma_f32 v13, -v33, v9, v13
	v_fma_f32 v14, -v34, v9, v14
	v_fma_f32 v15, -v39, v10, v15
	s_waitcnt lgkmcnt(0)
	v_fma_f32 v47, -v46, v51, v19
	ds_read_b128 v[48:51], v80 offset:2768
	ds_read_b128 v[56:59], v80 offset:3040
	v_fma_f32 v12, -v36, v10, v12
	v_fma_f32 v13, -v37, v10, v13
	v_fma_f32 v14, -v38, v10, v14
	v_fma_f32 v15, -v43, v11, v15
	v_fma_f32 v12, -v40, v11, v12
	v_fma_f32 v13, -v41, v11, v13
	v_fma_f32 v14, -v42, v11, v14
	v_fma_f32 v15, -v55, v44, v15
	v_fma_f32 v12, -v52, v44, v12
	v_fma_f32 v13, -v53, v44, v13
	ds_read_b128 v[64:67], v80 offset:3312
	ds_read_b128 v[16:19], v80 offset:3584
	v_fma_f32 v14, -v54, v44, v14
	v_fma_f32 v15, -v63, v45, v15
	v_fma_f32 v12, -v60, v45, v12
	v_fma_f32 v13, -v61, v45, v13
	v_fma_f32 v14, -v62, v45, v14
	v_fma_f32 v15, -v147, v46, v15
	v_fma_f32 v12, -v144, v46, v12
	v_fma_f32 v13, -v145, v46, v13
	v_fma_f32 v14, -v146, v46, v14
	s_waitcnt lgkmcnt(3)
	v_fma_f32 v15, -v51, v47, v15
	v_fma_f32 v12, -v48, v47, v12
	v_fma_f32 v13, -v49, v47, v13
	v_fma_f32 v14, -v50, v47, v14
	s_waitcnt lgkmcnt(0)
	s_movk_i32 s18, 0x900
	v_fma_f32 v15, -v59, v12, v15
	v_fma_f32 v13, -v57, v12, v13
	v_fma_f32 v14, -v58, v12, v14
	v_cvt_pk_bf16_f32 v18, v4, v4
	v_mad_u64_u32 v[16:17], s[18:19], v117, s18, v[74:75]
	v_fma_f32 v15, -v67, v13, v15
	v_fma_f32 v14, -v66, v13, v14
	s_movk_i32 s18, 0x90
	v_fma_f32 v15, -v19, v14, v15
	ds_write_b16_d16_hi v16, v18
	v_cvt_pk_bf16_f32 v17, v5, v5
	v_mad_u64_u32 v[18:19], s[18:19], v77, s18, v[74:75]
	ds_write_b16_d16_hi v18, v17
	v_bfe_u32 v17, v6, 16, 1
	v_add3_u32 v17, v6, v17, s43
	ds_write_b16_d16_hi v18, v17 offset:144
	ds_write_b128 v3, v[4:7]
	v_cvt_pk_bf16_f32 v4, v7, v7
	ds_write_b16_d16_hi v18, v4 offset:288
	v_cvt_pk_bf16_f32 v4, v8, v8
	ds_write_b16_d16_hi v18, v4 offset:432
	v_cvt_pk_bf16_f32 v4, v9, v9
	ds_write_b16_d16_hi v18, v4 offset:576
	v_cvt_pk_bf16_f32 v4, v10, v10
	ds_write_b16_d16_hi v18, v4 offset:720
	ds_write_b128 v3, v[8:11] offset:16
	v_cvt_pk_bf16_f32 v4, v11, v11
	ds_write_b16_d16_hi v18, v4 offset:864
	v_cvt_pk_bf16_f32 v4, v44, v44
	ds_write_b16_d16_hi v18, v4 offset:1008
	v_cvt_pk_bf16_f32 v4, v45, v45
	ds_write_b16_d16_hi v18, v4 offset:1152
	v_cvt_pk_bf16_f32 v4, v46, v46
	ds_write_b16_d16_hi v18, v4 offset:1296
	ds_write_b128 v3, v[44:47] offset:32
	v_cvt_pk_bf16_f32 v4, v47, v47
	ds_write_b16_d16_hi v18, v4 offset:1440
	v_cvt_pk_bf16_f32 v4, v12, v12
	ds_write_b16_d16_hi v18, v4 offset:1584
	v_cvt_pk_bf16_f32 v4, v13, v13
	ds_write_b16_d16_hi v18, v4 offset:1728
	v_cvt_pk_bf16_f32 v4, v14, v14
	ds_write_b16_d16_hi v18, v4 offset:1872
	ds_write_b128 v3, v[12:15] offset:48
	v_cvt_pk_bf16_f32 v3, v15, v15
	ds_write_b16_d16_hi v16, v3 offset:2160
	s_branch .LBB0_1233

; __device__ __forceinline__ void st16_wt(void* p, v4u v) { asm volatile("global_store_dwordx4 %0, %1, off sc0 sc1\n\ts_nop 1" :: "v"(p), "v"(v) : "memory"); }
; __device__ __forceinline__ unsigned f2bf(float f) { unsigned u = __builtin_bit_cast(unsigned, f); return (u + 0x7fffu + ((u >> 16) & 1u)) >> 16; }
; __device__ __forceinline__ unsigned pk2(float lo, float hi) { return f2bf(lo) | (f2bf(hi) << 16); }
; __device__ __forceinline__ void gdn_local_item(const Params& P, LAS unsigned char* lds, int item, int tid, bool defer, int& pend, unsigned& pend_fb) {
;     ...
;             for (int s2 = 0; s2 < 2; ++s2) {
;                 float v[8];
; #pragma unroll
;                 for (int e = 0; e < 8; ++e) { const int sidx = 32 * s2 + 8 * g + e; float x = src[sidx * 132] * sbeta[sidx]; if (isw) x *= seg[sidx]; v[e] = x; }
;                 v4u pk; pk.x = pk2(v[0], v[1]); pk.y = pk2(v[2], v[3]); pk.z = pk2(v[4], v[5]); pk.w = pk2(v[6], v[7]);
;                 bfr[s2] = __builtin_bit_cast(bf16x8, pk);
;             }
;             f32x4 acc[4];
; #pragma unroll
;             for (int rho = 0; rho < 4; ++rho) { acc[rho] = (f32x4){0.f, 0.f, 0.f, 0.f};
; #pragma unroll
;                 for (int s2 = 0; s2 < 2; ++s2) acc[rho] = __builtin_amdgcn_mfma_f32_16x16x32_bf16(af[rho][s2], bfr[s2], acc[rho], 0, 0, 0); }
;             if (!isw) {
;                 v4u o0, o1;
;                 o0.x = pk2(acc[0].x, acc[0].y); o0.y = pk2(acc[0].z, acc[0].w); o0.z = pk2(acc[1].x, acc[1].y); o0.w = pk2(acc[1].z, acc[1].w);
;                 o1.x = pk2(acc[2].x, acc[2].y); o1.y = pk2(acc[2].z, acc[2].w); o1.z = pk2(acc[3].x, acc[3].y); o1.w = pk2(acc[3].z, acc[3].w);
;                 v4u* d = (v4u*)(UF + (size_t)(2 * (wave & 3) + sig) * 1024 + lane * 16);
;                 st16_wt(d, o0); st16_wt(d + 1, o1);
;             } else {
; #pragma unroll
;                 for (int rho = 0; rho < 4; ++rho)
; #pragma unroll
;                     for (int i = 0; i < 4; ++i) wst[(16 * rho + 4 * g + i) * 136 + jj] = (bf16)f2bf(-acc[rho][i]);
;             }
.LBB0_1291:
	s_movk_i32 s0, 0x7fff
	v_cvt_pk_bf16_f32 v41, v41, v41
	v_cvt_pk_bf16_f32 v44, v44, v44
	v_cvt_pk_bf16_f32 v39, v39, v39
	v_cvt_pk_bf16_f32 v38, v38, v38
	v_cvt_pk_bf16_f32 v35, v35, v35
	v_cvt_pk_bf16_f32 v37, v37, v37
	v_cvt_pk_bf16_f32 v40, v40, v40
	v_lshrrev_b32_e32 v35, 16, v35
	v_lshrrev_b32_e32 v38, 16, v38
	s_mov_b32 s1, 0xffff0000
	v_cvt_pk_bf16_f32 v43, v43, v43
	v_lshrrev_b32_e32 v40, 16, v40
	v_and_or_b32 v97, v39, s1, v38
	v_and_or_b32 v96, v37, s1, v35
	v_lshrrev_b32_e32 v43, 16, v43
	v_and_or_b32 v98, v41, s1, v40
	v_cvt_pk_bf16_f32 v40, v45, v45
	v_cvt_pk_bf16_f32 v35, v36, v36
	v_and_or_b32 v99, v44, s1, v43
	v_cvt_pk_bf16_f32 v41, v47, v47
	v_cvt_pk_bf16_f32 v43, v49, v49
	v_cvt_pk_bf16_f32 v39, v50, v50
	v_cvt_pk_bf16_f32 v36, v42, v42
	v_cvt_pk_bf16_f32 v38, v48, v48
	v_cvt_pk_bf16_f32 v37, v46, v46
	v_lshrrev_b32_e32 v42, 16, v36
	v_lshrrev_b32_e32 v36, 16, v39
	v_lshrrev_b32_e32 v44, 16, v37
	v_lshrrev_b32_e32 v45, 16, v38
	v_and_or_b32 v103, v35, s1, v36
	v_mfma_f32_16x16x32_bf16 v[36:39], v[30:33], v[96:99], 0
	v_and_or_b32 v102, v43, s1, v45
	v_and_or_b32 v101, v41, s1, v44
	v_and_or_b32 v100, v40, s1, v42
	v_lshlrev_b32_e32 v50, 5, v34
	s_add_u32 s10, s82, s8
	v_mfma_f32_16x16x32_bf16 v[46:49], v[2:5], v[100:103], v[36:39]
	s_addc_u32 s11, s83, s9
	s_lshl_b32 s1, s28, 5
	v_mov_b32_e32 v51, 0
	v_mfma_f32_16x16x32_bf16 v[36:39], v[6:9], v[96:99], 0
	s_mov_b64 s[12:13], -1
	s_and_b64 vcc, exec, s[6:7]
	v_lshlrev_b32_e32 v95, 1, v95
	v_mfma_f32_16x16x32_bf16 v[42:45], v[10:13], v[100:103], v[36:39]
	v_mfma_f32_16x16x32_bf16 v[36:39], v[14:17], v[96:99], 0
	v_mfma_f32_16x16x32_bf16 v[96:99], v[22:25], v[96:99], 0
	v_mfma_f32_16x16x32_bf16 v[38:41], v[18:21], v[100:103], v[36:39]
	v_mfma_f32_16x16x32_bf16 v[34:37], v[26:29], v[100:103], v[96:99]
	s_cbranch_vccnz .LBB0_1293
	s_nop 4
	v_xor_b32_e32 v96, 0x80000000, v46
	v_cvt_pk_bf16_f32 v96, v96, v96
	v_mul_u32_u24_e32 v97, 0x440, v1
	v_add3_u32 v97, s54, v95, v97
	ds_write_b16_d16_hi v97, v96
	v_xor_b32_e32 v96, 0x80000000, v47
	v_cvt_pk_bf16_f32 v96, v96, v96
	ds_write_b16_d16_hi v97, v96 offset:272
	v_xor_b32_e32 v96, 0x80000000, v48
	v_cvt_pk_bf16_f32 v96, v96, v96
	ds_write_b16_d16_hi v97, v96 offset:544
	v_xor_b32_e32 v96, 0x80000000, v49
	v_cvt_pk_bf16_f32 v96, v96, v96
	ds_write_b16_d16_hi v97, v96 offset:816
	v_xor_b32_e32 v96, 0x80000000, v42
	v_cvt_pk_bf16_f32 v96, v96, v96
	ds_write_b16_d16_hi v97, v96 offset:4352
	v_xor_b32_e32 v96, 0x80000000, v43
	v_cvt_pk_bf16_f32 v96, v96, v96
	ds_write_b16_d16_hi v97, v96 offset:4624
	v_xor_b32_e32 v96, 0x80000000, v44
	v_cvt_pk_bf16_f32 v96, v96, v96
	ds_write_b16_d16_hi v97, v96 offset:4896
	v_xor_b32_e32 v96, 0x80000000, v45
	v_cvt_pk_bf16_f32 v96, v96, v96
	ds_write_b16_d16_hi v97, v96 offset:5168
	v_xor_b32_e32 v96, 0x80000000, v38
	v_cvt_pk_bf16_f32 v96, v96, v96
	ds_write_b16_d16_hi v97, v96 offset:8704
	v_xor_b32_e32 v96, 0x80000000, v39
	v_cvt_pk_bf16_f32 v96, v96, v96
	ds_write_b16_d16_hi v97, v96 offset:8976
	v_xor_b32_e32 v96, 0x80000000, v40
	v_cvt_pk_bf16_f32 v96, v96, v96
	ds_write_b16_d16_hi v97, v96 offset:9248
	v_xor_b32_e32 v96, 0x80000000, v41
	v_cvt_pk_bf16_f32 v96, v96, v96
	ds_write_b16_d16_hi v97, v96 offset:9520
	v_xor_b32_e32 v96, 0x80000000, v34
	v_cvt_pk_bf16_f32 v96, v96, v96
	ds_write_b16_d16_hi v97, v96 offset:13056
	v_xor_b32_e32 v96, 0x80000000, v35
	v_cvt_pk_bf16_f32 v96, v96, v96
	ds_write_b16_d16_hi v97, v96 offset:13328
	v_xor_b32_e32 v96, 0x80000000, v36
	v_cvt_pk_bf16_f32 v96, v96, v96
	ds_write_b16_d16_hi v97, v96 offset:13600
	v_xor_b32_e32 v96, 0x80000000, v37
	v_cvt_pk_bf16_f32 v96, v96, v96
	s_mov_b64 s[12:13], 0
	ds_write_b16_d16_hi v97, v96 offset:13872
.LBB0_1293:
	s_nop 4
	v_mul_u32_u24_e32 v96, 0x1080, v1
	s_and_b32 s0, s1, 0xfffff800
	s_andn2_b64 vcc, exec, s[12:13]
	v_lshl_add_u64 v[50:51], s[10:11], 0, v[50:51]
	s_cbranch_vccnz .LBB0_1295
	s_movk_i32 s1, 0x7fff
	v_cvt_pk_bf16_f32 v46, v46, v47
	s_mov_b32 s10, 0xffff0000
	v_cvt_pk_bf16_f32 v47, v48, v49
	v_cvt_pk_bf16_f32 v48, v42, v43
	v_cvt_pk_bf16_f32 v49, v44, v45
	v_cvt_pk_bf16_f32 v38, v38, v39
	v_cvt_pk_bf16_f32 v39, v40, v41
	v_cvt_pk_bf16_f32 v40, v34, v35
	v_cvt_pk_bf16_f32 v41, v36, v37
	s_mov_b32 s1, 0
	v_lshl_add_u64 v[34:35], s[0:1], 1, v[50:51]
	global_store_dwordx4 v[34:35], v[46:49], off sc0 sc1
	s_nop 1
	v_lshl_add_u64 v[34:35], v[34:35], 0, 16
	global_store_dwordx4 v[34:35], v[38:41], off sc0 sc1
	s_nop 1

; __device__ __forceinline__ void st16_wt(void* p, v4u v) { asm volatile("global_store_dwordx4 %0, %1, off sc0 sc1\n\ts_nop 1" :: "v"(p), "v"(v) : "memory"); }
; __device__ __forceinline__ unsigned f2bf(float f) { unsigned u = __builtin_bit_cast(unsigned, f); return (u + 0x7fffu + ((u >> 16) & 1u)) >> 16; }
; __device__ __forceinline__ unsigned pk2(float lo, float hi) { return f2bf(lo) | (f2bf(hi) << 16); }
; __device__ __forceinline__ void gdn_local_item(const Params& P, LAS unsigned char* lds, int item, int tid, bool defer, int& pend, unsigned& pend_fb) {
;     ...
;             for (int s2 = 0; s2 < 2; ++s2) {
;                 float v[8];
; #pragma unroll
;                 for (int e = 0; e < 8; ++e) { const int sidx = 32 * s2 + 8 * g + e; float x = src[sidx * 132] * sbeta[sidx]; if (isw) x *= seg[sidx]; v[e] = x; }
;                 v4u pk; pk.x = pk2(v[0], v[1]); pk.y = pk2(v[2], v[3]); pk.z = pk2(v[4], v[5]); pk.w = pk2(v[6], v[7]);
;                 bfr[s2] = __builtin_bit_cast(bf16x8, pk);
;             }
;             f32x4 acc[4];
; #pragma unroll
;             for (int rho = 0; rho < 4; ++rho) { acc[rho] = (f32x4){0.f, 0.f, 0.f, 0.f};
; #pragma unroll
;                 for (int s2 = 0; s2 < 2; ++s2) acc[rho] = __builtin_amdgcn_mfma_f32_16x16x32_bf16(af[rho][s2], bfr[s2], acc[rho], 0, 0, 0); }
;             if (!isw) {
;                 v4u o0, o1;
;                 o0.x = pk2(acc[0].x, acc[0].y); o0.y = pk2(acc[0].z, acc[0].w); o0.z = pk2(acc[1].x, acc[1].y); o0.w = pk2(acc[1].z, acc[1].w);
;                 o1.x = pk2(acc[2].x, acc[2].y); o1.y = pk2(acc[2].z, acc[2].w); o1.z = pk2(acc[3].x, acc[3].y); o1.w = pk2(acc[3].z, acc[3].w);
;                 v4u* d = (v4u*)(UF + (size_t)(2 * (wave & 3) + sig) * 1024 + lane * 16);
;                 st16_wt(d, o0); st16_wt(d + 1, o1);
;             } else {
; #pragma unroll
;                 for (int rho = 0; rho < 4; ++rho)
; #pragma unroll
;                     for (int i = 0; i < 4; ++i) wst[(16 * rho + 4 * g + i) * 136 + jj] = (bf16)f2bf(-acc[rho][i]);
;             }
.LBB0_1327:
	s_movk_i32 s1, 0x7fff
	v_cvt_pk_bf16_f32 v55, v35, v35
	v_cvt_pk_bf16_f32 v35, v37, v37
	v_cvt_pk_bf16_f32 v39, v39, v39
	v_cvt_pk_bf16_f32 v37, v42, v42
	v_cvt_pk_bf16_f32 v41, v41, v41
	v_cvt_pk_bf16_f32 v38, v38, v38
	v_cvt_pk_bf16_f32 v36, v36, v36
	v_cvt_pk_bf16_f32 v34, v34, v34
	v_lshrrev_b32_e32 v34, 16, v34
	v_lshrrev_b32_e32 v42, 16, v36
	v_lshrrev_b32_e32 v36, 16, v38
	v_lshrrev_b32_e32 v38, 16, v41
	s_mov_b32 s10, 0xffff0000
	v_and_or_b32 v37, v37, s10, v38
	v_and_or_b32 v36, v39, s10, v36
	v_and_or_b32 v35, v35, s10, v42
	v_and_or_b32 v34, v55, s10, v34
	v_cvt_pk_bf16_f32 v42, v43, v43
	v_cvt_pk_bf16_f32 v43, v45, v45
	v_cvt_pk_bf16_f32 v39, v47, v47
	v_cvt_pk_bf16_f32 v38, v49, v49
	v_mfma_f32_16x16x32_bf16 v[30:33], v[30:33], v[34:37], 0
	v_cvt_pk_bf16_f32 v48, v48, v48
	v_cvt_pk_bf16_f32 v46, v46, v46
	v_cvt_pk_bf16_f32 v44, v44, v44
	v_cvt_pk_bf16_f32 v40, v40, v40
	v_lshrrev_b32_e32 v45, 16, v40
	v_lshrrev_b32_e32 v44, 16, v44
	v_lshrrev_b32_e32 v40, 16, v46
	v_lshrrev_b32_e32 v41, 16, v48
	v_and_or_b32 v41, v38, s10, v41
	v_and_or_b32 v40, v39, s10, v40
	v_and_or_b32 v39, v43, s10, v44
	v_and_or_b32 v38, v42, s10, v45
	s_and_b64 vcc, exec, s[6:7]
	s_mov_b64 s[6:7], -1
	v_mfma_f32_16x16x32_bf16 v[30:33], v[2:5], v[38:41], v[30:33]
	v_mfma_f32_16x16x32_bf16 v[2:5], v[6:9], v[34:37], 0
	v_mfma_f32_16x16x32_bf16 v[10:13], v[10:13], v[38:41], v[2:5]
	v_mfma_f32_16x16x32_bf16 v[2:5], v[14:17], v[34:37], 0
	v_mfma_f32_16x16x32_bf16 v[6:9], v[18:21], v[38:41], v[2:5]
	v_mfma_f32_16x16x32_bf16 v[2:5], v[22:25], v[34:37], 0
	v_mfma_f32_16x16x32_bf16 v[2:5], v[26:29], v[38:41], v[2:5]
	s_cbranch_vccnz .LBB0_1329
	s_nop 0
	v_xor_b32_e32 v14, 0x80000000, v30
	v_mul_u32_u24_e32 v1, 0x440, v1
	v_cvt_pk_bf16_f32 v14, v14, v14
	v_add3_u32 v1, s54, v1, v95
	ds_write_b16_d16_hi v1, v14 offset:32
	v_xor_b32_e32 v14, 0x80000000, v31
	v_cvt_pk_bf16_f32 v14, v14, v14
	ds_write_b16_d16_hi v1, v14 offset:304
	v_xor_b32_e32 v14, 0x80000000, v32
	v_cvt_pk_bf16_f32 v14, v14, v14
	ds_write_b16_d16_hi v1, v14 offset:576
	v_xor_b32_e32 v14, 0x80000000, v33
	v_cvt_pk_bf16_f32 v14, v14, v14
	ds_write_b16_d16_hi v1, v14 offset:848
	v_xor_b32_e32 v14, 0x80000000, v10
	v_cvt_pk_bf16_f32 v14, v14, v14
	ds_write_b16_d16_hi v1, v14 offset:4384
	v_xor_b32_e32 v14, 0x80000000, v11
	v_cvt_pk_bf16_f32 v14, v14, v14
	ds_write_b16_d16_hi v1, v14 offset:4656
	v_xor_b32_e32 v14, 0x80000000, v12
	v_cvt_pk_bf16_f32 v14, v14, v14
	ds_write_b16_d16_hi v1, v14 offset:4928
	v_xor_b32_e32 v14, 0x80000000, v13
	v_cvt_pk_bf16_f32 v14, v14, v14
	ds_write_b16_d16_hi v1, v14 offset:5200
	v_xor_b32_e32 v14, 0x80000000, v6
	v_cvt_pk_bf16_f32 v14, v14, v14
	ds_write_b16_d16_hi v1, v14 offset:8736
	v_xor_b32_e32 v14, 0x80000000, v7
	v_cvt_pk_bf16_f32 v14, v14, v14
	ds_write_b16_d16_hi v1, v14 offset:9008
	v_xor_b32_e32 v14, 0x80000000, v8
	v_cvt_pk_bf16_f32 v14, v14, v14
	ds_write_b16_d16_hi v1, v14 offset:9280
	v_xor_b32_e32 v14, 0x80000000, v9
	v_cvt_pk_bf16_f32 v14, v14, v14
	ds_write_b16_d16_hi v1, v14 offset:9552
	v_xor_b32_e32 v14, 0x80000000, v2
	v_cvt_pk_bf16_f32 v14, v14, v14
	ds_write_b16_d16_hi v1, v14 offset:13088
	v_xor_b32_e32 v14, 0x80000000, v3
	v_cvt_pk_bf16_f32 v14, v14, v14
	ds_write_b16_d16_hi v1, v14 offset:13360
	v_xor_b32_e32 v14, 0x80000000, v4
	v_cvt_pk_bf16_f32 v14, v14, v14
	ds_write_b16_d16_hi v1, v14 offset:13632
	v_xor_b32_e32 v14, 0x80000000, v5
	v_cvt_pk_bf16_f32 v14, v14, v14
	s_mov_b64 s[6:7], 0
	ds_write_b16_d16_hi v1, v14 offset:13904
